# wt4 + nt on the 61 dwordx4 stores that lacked it (all dwordx4 stores now sc1 nt)
# speedup vs baseline: 1.0071x; 1.0071x over previous
.LBB0_23:
	s_andn2_b64 vcc, exec, s[4:5]
	s_cbranch_vccnz .LBB0_25
	s_ashr_i32 s17, s16, 31
	s_lshl_b64 s[4:5], s[16:17], 22
	s_add_u32 s82, s8, s4
	s_addc_u32 s83, s9, s5
	s_lshl_b64 s[18:19], s[16:17], 21
	v_readlane_b32 s4, v254, 6
	s_add_u32 s5, s4, s18
	v_readlane_b32 s4, v254, 7
	s_addc_u32 s17, s4, s19
	s_mul_i32 s4, s16, 0xffffe200
	s_add_i32 s4, s28, s4
	s_and_b32 s4, s4, 0xfc0
	s_add_i32 s14, s4, 0xfffff600
	s_and_b32 s4, s26, 0x3e0
	s_lshl_b32 s18, s4, 2
	v_or_b32_e32 v2, s14, v26
	s_add_u32 s18, s82, s18
	s_addc_u32 s19, s83, 0
	v_mov_b32_e32 v7, v3
	v_or_b32_e32 v12, 2, v2
	v_mov_b32_e32 v13, v3
	v_or_b32_e32 v14, 4, v2
	v_mov_b32_e32 v15, v3
	v_or_b32_e32 v16, 6, v2
	v_mov_b32_e32 v17, v3
	v_or_b32_e32 v18, 8, v2
	v_mov_b32_e32 v19, v3
	v_or_b32_e32 v20, 10, v2
	v_mov_b32_e32 v21, v3
	v_or_b32_e32 v22, 12, v2
	v_mov_b32_e32 v23, v3
	v_lshl_add_u64 v[8:9], s[18:19], 0, v[6:7]
	v_lshlrev_b64 v[10:11], 12, v[2:3]
	v_lshlrev_b64 v[12:13], 12, v[12:13]
	v_lshlrev_b64 v[14:15], 12, v[14:15]
	v_lshlrev_b64 v[16:17], 12, v[16:17]
	v_lshlrev_b64 v[18:19], 12, v[18:19]
	v_lshlrev_b64 v[20:21], 12, v[20:21]
	v_lshlrev_b64 v[22:23], 12, v[22:23]
	v_or_b32_e32 v24, 14, v2
	v_mov_b32_e32 v25, v3
	v_lshl_add_u64 v[10:11], v[8:9], 0, v[10:11]
	v_lshl_add_u64 v[12:13], v[8:9], 0, v[12:13]
	v_lshl_add_u64 v[14:15], v[8:9], 0, v[14:15]
	v_lshl_add_u64 v[16:17], v[8:9], 0, v[16:17]
	v_lshl_add_u64 v[18:19], v[8:9], 0, v[18:19]
	v_lshl_add_u64 v[20:21], v[8:9], 0, v[20:21]
	v_lshl_add_u64 v[22:23], v[8:9], 0, v[22:23]
	v_lshlrev_b64 v[24:25], 12, v[24:25]
	v_lshl_add_u64 v[24:25], v[8:9], 0, v[24:25]
	global_load_dword v7, v[10:11], off nt
	global_load_dword v77, v[12:13], off nt
	global_load_dword v78, v[14:15], off nt
	global_load_dword v79, v[16:17], off nt
	global_load_dword v80, v[18:19], off nt
	global_load_dword v81, v[20:21], off nt
	global_load_dword v82, v[22:23], off nt
	global_load_dword v83, v[24:25], off nt
	v_or_b32_e32 v10, 16, v2
	v_mov_b32_e32 v11, v3
	v_or_b32_e32 v12, 18, v2
	v_mov_b32_e32 v13, v3
	v_or_b32_e32 v14, 20, v2
	v_mov_b32_e32 v15, v3
	v_or_b32_e32 v16, 22, v2
	v_mov_b32_e32 v17, v3
	v_or_b32_e32 v18, 24, v2
	v_mov_b32_e32 v19, v3
	v_or_b32_e32 v20, 26, v2
	v_mov_b32_e32 v21, v3
	v_or_b32_e32 v22, 28, v2
	v_mov_b32_e32 v23, v3
	v_lshlrev_b64 v[10:11], 12, v[10:11]
	v_lshlrev_b64 v[12:13], 12, v[12:13]
	v_lshlrev_b64 v[14:15], 12, v[14:15]
	v_lshlrev_b64 v[16:17], 12, v[16:17]
	v_lshlrev_b64 v[18:19], 12, v[18:19]
	v_lshlrev_b64 v[20:21], 12, v[20:21]
	v_lshlrev_b64 v[22:23], 12, v[22:23]
	v_or_b32_e32 v24, 30, v2
	v_mov_b32_e32 v25, v3
	v_lshl_add_u64 v[10:11], v[8:9], 0, v[10:11]
	v_lshl_add_u64 v[12:13], v[8:9], 0, v[12:13]
	v_lshl_add_u64 v[14:15], v[8:9], 0, v[14:15]
	v_lshl_add_u64 v[16:17], v[8:9], 0, v[16:17]
	v_lshl_add_u64 v[18:19], v[8:9], 0, v[18:19]
	v_lshl_add_u64 v[20:21], v[8:9], 0, v[20:21]
	v_lshl_add_u64 v[22:23], v[8:9], 0, v[22:23]
	v_lshlrev_b64 v[24:25], 12, v[24:25]
	v_lshl_add_u64 v[24:25], v[8:9], 0, v[24:25]
	global_load_dword v84, v[10:11], off nt
	global_load_dword v85, v[12:13], off nt
	global_load_dword v86, v[14:15], off nt
	global_load_dword v87, v[16:17], off nt
	global_load_dword v88, v[18:19], off nt
	global_load_dword v89, v[20:21], off nt
	global_load_dword v90, v[22:23], off nt
	global_load_dword v91, v[24:25], off nt
	v_or_b32_e32 v10, 32, v2
	v_mov_b32_e32 v11, v3
	v_or_b32_e32 v12, 34, v2
	v_mov_b32_e32 v13, v3
	v_or_b32_e32 v14, 36, v2
	v_mov_b32_e32 v15, v3
	v_or_b32_e32 v16, 38, v2
	v_mov_b32_e32 v17, v3
	v_or_b32_e32 v18, 40, v2
	v_mov_b32_e32 v19, v3
	v_or_b32_e32 v20, 42, v2
	v_mov_b32_e32 v21, v3
	v_or_b32_e32 v22, 44, v2
	v_mov_b32_e32 v23, v3
	v_lshlrev_b64 v[10:11], 12, v[10:11]
	v_lshlrev_b64 v[12:13], 12, v[12:13]
	v_lshlrev_b64 v[14:15], 12, v[14:15]
	v_lshlrev_b64 v[16:17], 12, v[16:17]
	v_lshlrev_b64 v[18:19], 12, v[18:19]
	v_lshlrev_b64 v[20:21], 12, v[20:21]
	v_lshlrev_b64 v[22:23], 12, v[22:23]
	v_or_b32_e32 v24, 46, v2
	v_mov_b32_e32 v25, v3
	v_lshl_add_u64 v[10:11], v[8:9], 0, v[10:11]
	v_lshl_add_u64 v[12:13], v[8:9], 0, v[12:13]
	v_lshl_add_u64 v[14:15], v[8:9], 0, v[14:15]
	v_lshl_add_u64 v[16:17], v[8:9], 0, v[16:17]
	v_lshl_add_u64 v[18:19], v[8:9], 0, v[18:19]
	v_lshl_add_u64 v[20:21], v[8:9], 0, v[20:21]
	v_lshl_add_u64 v[22:23], v[8:9], 0, v[22:23]
	v_lshlrev_b64 v[24:25], 12, v[24:25]
	v_lshl_add_u64 v[24:25], v[8:9], 0, v[24:25]
	global_load_dword v92, v[10:11], off nt
	global_load_dword v93, v[12:13], off nt
	global_load_dword v94, v[14:15], off nt
	global_load_dword v95, v[16:17], off nt
	global_load_dword v96, v[18:19], off nt
	global_load_dword v97, v[20:21], off nt
	global_load_dword v98, v[22:23], off nt
	global_load_dword v99, v[24:25], off nt
	v_or_b32_e32 v10, 48, v2
	v_mov_b32_e32 v11, v3
	v_or_b32_e32 v12, 50, v2
	v_mov_b32_e32 v13, v3
	v_or_b32_e32 v14, 52, v2
	v_mov_b32_e32 v15, v3
	v_or_b32_e32 v16, 54, v2
	v_mov_b32_e32 v17, v3
	v_or_b32_e32 v18, 56, v2
	v_mov_b32_e32 v19, v3
	v_or_b32_e32 v20, 58, v2
	v_mov_b32_e32 v21, v3
	v_or_b32_e32 v22, 60, v2
	v_mov_b32_e32 v23, v3
	v_or_b32_e32 v2, 62, v2
	v_lshlrev_b64 v[10:11], 12, v[10:11]
	v_lshlrev_b64 v[12:13], 12, v[12:13]
	v_lshlrev_b64 v[14:15], 12, v[14:15]
	v_lshlrev_b64 v[16:17], 12, v[16:17]
	v_lshlrev_b64 v[18:19], 12, v[18:19]
	v_lshlrev_b64 v[20:21], 12, v[20:21]
	v_lshlrev_b64 v[22:23], 12, v[22:23]
	v_lshlrev_b64 v[24:25], 12, v[2:3]
	v_lshl_add_u64 v[10:11], v[8:9], 0, v[10:11]
	v_lshl_add_u64 v[12:13], v[8:9], 0, v[12:13]
	v_lshl_add_u64 v[14:15], v[8:9], 0, v[14:15]
	v_lshl_add_u64 v[16:17], v[8:9], 0, v[16:17]
	v_lshl_add_u64 v[18:19], v[8:9], 0, v[18:19]
	v_lshl_add_u64 v[20:21], v[8:9], 0, v[20:21]
	v_lshl_add_u64 v[22:23], v[8:9], 0, v[22:23]
	v_lshl_add_u64 v[8:9], v[8:9], 0, v[24:25]
	global_load_dword v2, v[10:11], off nt
	s_nop 0
	global_load_dword v10, v[12:13], off nt
	global_load_dword v11, v[14:15], off nt
	s_nop 0
	global_load_dword v12, v[16:17], off nt
	global_load_dword v13, v[18:19], off nt
	global_load_dword v14, v[20:21], off nt
	global_load_dword v15, v[22:23], off nt
	s_nop 0
	global_load_dword v8, v[8:9], off nt
	s_waitcnt vmcnt(30)
	ds_write2_b32 v27, v7, v77 offset1:66
	s_waitcnt vmcnt(28)
	ds_write2_b32 v27, v78, v79 offset0:132 offset1:198
	s_waitcnt vmcnt(26)
	ds_write2_b32 v38, v80, v81 offset0:8 offset1:74
	s_waitcnt vmcnt(24)
	ds_write2_b32 v38, v82, v83 offset0:140 offset1:206
	s_waitcnt vmcnt(22)
	ds_write2_b32 v39, v84, v85 offset0:16 offset1:82
	s_waitcnt vmcnt(20)
	ds_write2_b32 v39, v86, v87 offset0:148 offset1:214
	s_waitcnt vmcnt(18)
	ds_write2_b32 v40, v88, v89 offset0:24 offset1:90
	s_waitcnt vmcnt(16)
	ds_write2_b32 v40, v90, v91 offset0:156 offset1:222
	s_waitcnt vmcnt(14)
	ds_write2_b32 v41, v92, v93 offset0:32 offset1:98
	s_waitcnt vmcnt(12)
	ds_write2_b32 v41, v94, v95 offset0:164 offset1:230
	s_waitcnt vmcnt(10)
	ds_write2_b32 v42, v96, v97 offset0:40 offset1:106
	s_waitcnt vmcnt(8)
	ds_write2_b32 v42, v98, v99 offset0:172 offset1:238
	s_waitcnt vmcnt(6)
	ds_write2_b32 v43, v2, v10 offset0:48 offset1:114
	s_waitcnt vmcnt(4)
	ds_write2_b32 v43, v11, v12 offset0:180 offset1:246
	s_waitcnt vmcnt(2)
	ds_write2_b32 v44, v13, v14 offset0:56 offset1:122
	s_waitcnt vmcnt(0)
	ds_write2_b32 v44, v15, v8 offset0:188 offset1:254
	s_waitcnt lgkmcnt(0)
	s_lshl_b64 s[18:19], s[14:15], 1
	ds_read2_b32 v[12:13], v29 offset0:33 offset1:41
	ds_read2_b32 v[14:15], v29 offset1:8
	ds_read2_b32 v[16:17], v29 offset0:66 offset1:74
	ds_read2_b32 v[18:19], v29 offset0:99 offset1:107
	ds_read2_b32 v[20:21], v29 offset0:132 offset1:140
	ds_read2_b32 v[22:23], v29 offset0:165 offset1:173
	ds_read2_b32 v[24:25], v29 offset0:198 offset1:206
	ds_read2_b32 v[78:79], v29 offset0:231 offset1:239
	s_add_u32 s18, s5, s18
	s_addc_u32 s19, s17, s19
	v_lshlrev_b32_e32 v2, 1, v4
	v_lshl_add_u64 v[80:81], s[18:19], 0, v[2:3]
	v_or_b32_e32 v2, s4, v28
	v_lshlrev_b32_e32 v2, 11, v2
	s_waitcnt lgkmcnt(6)
	v_cvt_pk_bf16_f32 v8, v14, v12
	s_waitcnt lgkmcnt(4)
	v_cvt_pk_bf16_f32 v9, v16, v18
	s_waitcnt lgkmcnt(2)
	v_cvt_pk_bf16_f32 v10, v20, v22
	s_waitcnt lgkmcnt(0)
	v_cvt_pk_bf16_f32 v11, v24, v78
	v_lshl_add_u64 v[82:83], v[80:81], 0, v[2:3]
	global_store_dwordx4 v[82:83], v[8:11], off sc1 nt
	v_or_b32_e32 v2, s4, v30
	v_lshlrev_b32_e32 v2, 11, v2
	v_cvt_pk_bf16_f32 v8, v15, v13
	v_cvt_pk_bf16_f32 v9, v17, v19
	v_cvt_pk_bf16_f32 v10, v21, v23
	v_cvt_pk_bf16_f32 v11, v25, v79
	ds_read2_b32 v[14:15], v29 offset0:49 offset1:57
	ds_read2_b32 v[16:17], v29 offset0:16 offset1:24
	ds_read2_b32 v[18:19], v29 offset0:82 offset1:90
	ds_read2_b32 v[20:21], v29 offset0:115 offset1:123
	ds_read2_b32 v[22:23], v29 offset0:148 offset1:156
	ds_read2_b32 v[24:25], v29 offset0:181 offset1:189
	ds_read2_b32 v[78:79], v29 offset0:214 offset1:222
	ds_read2_b32 v[82:83], v29 offset0:247 offset1:255
	v_lshl_add_u64 v[12:13], v[80:81], 0, v[2:3]
	v_or_b32_e32 v2, s4, v31
	v_lshlrev_b32_e32 v2, 11, v2
	global_store_dwordx4 v[12:13], v[8:11], off sc1 nt
	v_lshl_add_u64 v[12:13], v[80:81], 0, v[2:3]
	v_or_b32_e32 v2, s4, v32
	s_waitcnt lgkmcnt(6)
	v_cvt_pk_bf16_f32 v8, v16, v14
	s_waitcnt lgkmcnt(4)
	v_cvt_pk_bf16_f32 v9, v18, v20
	s_waitcnt lgkmcnt(2)
	v_cvt_pk_bf16_f32 v10, v22, v24
	s_waitcnt lgkmcnt(0)
	v_cvt_pk_bf16_f32 v11, v78, v82
	v_lshlrev_b32_e32 v2, 11, v2
	global_store_dwordx4 v[12:13], v[8:11], off sc1 nt
	v_lshl_add_u64 v[12:13], v[80:81], 0, v[2:3]
	s_nop 0
	v_cvt_pk_bf16_f32 v8, v17, v15
	v_cvt_pk_bf16_f32 v9, v19, v21
	v_cvt_pk_bf16_f32 v10, v23, v25
	v_cvt_pk_bf16_f32 v11, v79, v83
	global_store_dwordx4 v[12:13], v[8:11], off sc1 nt
	s_waitcnt lgkmcnt(0)

.LBB0_26:
	s_andn2_b64 vcc, exec, s[4:5]
	s_cbranch_vccnz .LBB0_28
	s_mul_i32 s5, s16, 0xa10000
	s_mul_hi_i32 s4, s16, 0xa10000
	s_add_u32 s18, s6, s5
	s_addc_u32 s19, s7, s4
	s_mul_i32 s5, s16, 0x580000
	s_mul_hi_i32 s4, s16, 0x580000
	s_add_u32 s5, s86, s5
	s_addc_u32 s17, s87, s4
	s_mul_i32 s4, s16, 0xffffe200
	s_add_i32 s4, s28, s4
	s_and_b32 s4, s4, 0xfc0
	s_add_i32 s14, s4, 0xfffffa00
	s_mul_i32 s4, s16, 0xfffe2000
	s_add_i32 s4, s26, s4
	s_and_b32 s82, s4, 0x3e0
	s_lshl_b32 s82, s82, 2
	s_add_u32 s18, s18, s82
	v_or_b32_e32 v2, s14, v26
	s_addc_u32 s19, s19, 0
	v_mov_b32_e32 v7, v3
	v_lshl_add_u64 v[8:9], s[18:19], 0, v[6:7]
	v_mul_i32_i24_e32 v2, 0x2840, v2
	v_lshl_add_u64 v[8:9], v[8:9], 0, v[2:3]
	v_add_co_u32_e32 v10, vcc, s53, v8
	s_lshl_b64 s[18:19], s[14:15], 1
	s_nop 0
	v_addc_co_u32_e32 v11, vcc, 0, v9, vcc
	v_add_co_u32_e32 v12, vcc, s31, v8
	s_add_u32 s18, s5, s18
	s_nop 0
	v_addc_co_u32_e32 v13, vcc, 0, v9, vcc
	v_add_co_u32_e32 v14, vcc, s54, v8
	s_addc_u32 s19, s17, s19
	s_nop 0
	v_addc_co_u32_e32 v15, vcc, 0, v9, vcc
	v_add_co_u32_e32 v16, vcc, s55, v8
	s_and_b32 s5, s24, 0x300
	s_nop 0
	v_addc_co_u32_e32 v17, vcc, 0, v9, vcc
	v_add_co_u32_e32 v18, vcc, s56, v8
	s_and_b32 s14, s22, 0x80
	s_nop 0
	v_addc_co_u32_e32 v19, vcc, 0, v9, vcc
	v_add_co_u32_e32 v20, vcc, s57, v8
	s_and_b32 s4, s4, 0x60
	s_nop 0
	v_addc_co_u32_e32 v21, vcc, 0, v9, vcc
	v_add_co_u32_e32 v22, vcc, s58, v8
	s_or_b32 s5, s5, s14
	s_nop 0
	v_addc_co_u32_e32 v23, vcc, 0, v9, vcc
	v_add_co_u32_e32 v24, vcc, s33, v8
	s_addk_i32 s5, 0x700
	s_nop 0
	v_addc_co_u32_e32 v25, vcc, 0, v9, vcc
	global_load_dword v2, v[10:11], off offset:2112 nt
	global_load_dword v7, v[12:13], off offset:2240 nt
	global_load_dword v77, v[14:15], off offset:2368 nt
	global_load_dword v78, v[16:17], off offset:2496 nt
	global_load_dword v79, v[18:19], off offset:2624 nt
	global_load_dword v80, v[20:21], off offset:2752 nt
	global_load_dword v81, v[22:23], off offset:2880 nt
	global_load_dword v82, v[24:25], off offset:3008 nt
	v_add_co_u32_e32 v10, vcc, s60, v8
	s_nop 1
	v_addc_co_u32_e32 v11, vcc, 0, v9, vcc
	v_add_co_u32_e32 v12, vcc, s61, v8
	s_nop 1
	v_addc_co_u32_e32 v13, vcc, 0, v9, vcc
	v_add_co_u32_e32 v14, vcc, s62, v8
	s_nop 1
	v_addc_co_u32_e32 v15, vcc, 0, v9, vcc
	v_add_co_u32_e32 v16, vcc, s63, v8
	s_nop 1
	v_addc_co_u32_e32 v17, vcc, 0, v9, vcc
	v_add_co_u32_e32 v18, vcc, s64, v8
	s_nop 1
	v_addc_co_u32_e32 v19, vcc, 0, v9, vcc
	v_add_co_u32_e32 v20, vcc, s34, v8
	s_nop 1
	v_addc_co_u32_e32 v21, vcc, 0, v9, vcc
	v_add_co_u32_e32 v22, vcc, s65, v8
	s_nop 1
	v_addc_co_u32_e32 v23, vcc, 0, v9, vcc
	v_add_co_u32_e32 v24, vcc, s66, v8
	s_nop 1
	v_addc_co_u32_e32 v25, vcc, 0, v9, vcc
	global_load_dword v83, v[10:11], off offset:3136 nt
	global_load_dword v84, v[12:13], off offset:3264 nt
	global_load_dword v85, v[14:15], off offset:3392 nt
	global_load_dword v86, v[16:17], off offset:3520 nt
	global_load_dword v87, v[18:19], off offset:3648 nt
	global_load_dword v88, v[20:21], off offset:3776 nt
	global_load_dword v89, v[22:23], off offset:3904 nt
	global_load_dword v90, v[24:25], off offset:4032 nt
	v_add_co_u32_e32 v10, vcc, s67, v8
	s_nop 1
	v_addc_co_u32_e32 v11, vcc, 0, v9, vcc
	v_add_co_u32_e32 v12, vcc, s68, v8
	s_nop 1
	v_addc_co_u32_e32 v13, vcc, 0, v9, vcc
	v_add_co_u32_e32 v14, vcc, s69, v8
	s_nop 1
	v_addc_co_u32_e32 v15, vcc, 0, v9, vcc
	v_add_co_u32_e32 v16, vcc, s70, v8
	s_nop 1
	v_addc_co_u32_e32 v17, vcc, 0, v9, vcc
	v_add_co_u32_e32 v18, vcc, s35, v8
	s_nop 1
	v_addc_co_u32_e32 v19, vcc, 0, v9, vcc
	v_add_co_u32_e32 v20, vcc, s71, v8
	s_nop 1
	v_addc_co_u32_e32 v21, vcc, 0, v9, vcc
	v_add_co_u32_e32 v22, vcc, s72, v8
	s_nop 1
	v_addc_co_u32_e32 v23, vcc, 0, v9, vcc
	v_add_co_u32_e32 v24, vcc, s73, v8
	s_nop 1
	v_addc_co_u32_e32 v25, vcc, 0, v9, vcc
	global_load_dword v91, v[10:11], off offset:64 nt
	global_load_dword v92, v[12:13], off offset:192 nt
	global_load_dword v93, v[14:15], off offset:320 nt
	global_load_dword v94, v[16:17], off offset:448 nt
	global_load_dword v95, v[18:19], off offset:576 nt
	global_load_dword v96, v[20:21], off offset:704 nt
	global_load_dword v97, v[22:23], off offset:832 nt
	s_nop 0
	global_load_dword v24, v[24:25], off offset:960 nt
	v_add_co_u32_e32 v10, vcc, s74, v8
	s_nop 1
	v_addc_co_u32_e32 v11, vcc, 0, v9, vcc
	v_add_co_u32_e32 v12, vcc, s75, v8
	s_nop 1
	v_addc_co_u32_e32 v13, vcc, 0, v9, vcc
	v_add_co_u32_e32 v14, vcc, s38, v8
	s_nop 1
	v_addc_co_u32_e32 v15, vcc, 0, v9, vcc
	v_add_co_u32_e32 v16, vcc, s76, v8
	s_nop 1
	v_addc_co_u32_e32 v17, vcc, 0, v9, vcc
	v_add_co_u32_e32 v18, vcc, s77, v8
	s_nop 1
	v_addc_co_u32_e32 v19, vcc, 0, v9, vcc
	v_add_co_u32_e32 v20, vcc, s78, v8
	s_nop 1
	v_addc_co_u32_e32 v21, vcc, 0, v9, vcc
	v_add_co_u32_e32 v22, vcc, s79, v8
	s_nop 1
	v_addc_co_u32_e32 v23, vcc, 0, v9, vcc
	v_add_co_u32_e32 v8, vcc, s80, v8
	s_nop 1
	v_addc_co_u32_e32 v9, vcc, 0, v9, vcc
	global_load_dword v10, v[10:11], off offset:1088 nt
	s_nop 0
	global_load_dword v11, v[12:13], off offset:1216 nt
	s_nop 0
	global_load_dword v12, v[14:15], off offset:1344 nt
	global_load_dword v13, v[16:17], off offset:1472 nt
	s_nop 0
	global_load_dword v14, v[18:19], off offset:1600 nt
	global_load_dword v15, v[20:21], off offset:1728 nt
	global_load_dword v16, v[22:23], off offset:1856 nt
	s_nop 0
	global_load_dword v8, v[8:9], off offset:1984 nt
	s_waitcnt vmcnt(30)
	ds_write2_b32 v27, v2, v7 offset1:66
	s_waitcnt vmcnt(28)
	ds_write2_b32 v27, v77, v78 offset0:132 offset1:198
	s_waitcnt vmcnt(26)
	ds_write2_b32 v38, v79, v80 offset0:8 offset1:74
	s_waitcnt vmcnt(24)
	ds_write2_b32 v38, v81, v82 offset0:140 offset1:206
	s_waitcnt vmcnt(22)
	ds_write2_b32 v39, v83, v84 offset0:16 offset1:82
	s_waitcnt vmcnt(20)
	ds_write2_b32 v39, v85, v86 offset0:148 offset1:214
	s_waitcnt vmcnt(18)
	ds_write2_b32 v40, v87, v88 offset0:24 offset1:90
	s_waitcnt vmcnt(16)
	ds_write2_b32 v40, v89, v90 offset0:156 offset1:222
	s_waitcnt vmcnt(14)
	ds_write2_b32 v41, v91, v92 offset0:32 offset1:98
	s_waitcnt vmcnt(12)
	ds_write2_b32 v41, v93, v94 offset0:164 offset1:230
	s_waitcnt vmcnt(10)
	ds_write2_b32 v42, v95, v96 offset0:40 offset1:106
	s_waitcnt vmcnt(8)
	ds_write2_b32 v42, v97, v24 offset0:172 offset1:238
	s_waitcnt vmcnt(6)
	ds_write2_b32 v43, v10, v11 offset0:48 offset1:114
	s_waitcnt vmcnt(4)
	ds_write2_b32 v43, v12, v13 offset0:180 offset1:246
	s_waitcnt vmcnt(2)
	ds_write2_b32 v44, v14, v15 offset0:56 offset1:122
	s_waitcnt vmcnt(0)
	ds_write2_b32 v44, v16, v8 offset0:188 offset1:254
	s_waitcnt lgkmcnt(0)
	v_lshlrev_b32_e32 v2, 1, v4
	ds_read2_b32 v[12:13], v29 offset0:33 offset1:41
	ds_read2_b32 v[14:15], v29 offset1:8
	ds_read2_b32 v[16:17], v29 offset0:66 offset1:74
	ds_read2_b32 v[18:19], v29 offset0:99 offset1:107
	ds_read2_b32 v[20:21], v29 offset0:132 offset1:140
	ds_read2_b32 v[22:23], v29 offset0:165 offset1:173
	ds_read2_b32 v[24:25], v29 offset0:198 offset1:206
	ds_read2_b32 v[78:79], v29 offset0:231 offset1:239
	v_lshl_add_u64 v[80:81], s[18:19], 0, v[2:3]
	v_or_b32_e32 v2, s4, v28
	v_or_b32_e32 v2, s5, v2
	v_lshlrev_b32_e32 v2, 11, v2
	v_lshl_add_u64 v[82:83], v[80:81], 0, v[2:3]
	v_or_b32_e32 v2, s4, v30
	s_waitcnt lgkmcnt(6)
	v_cvt_pk_bf16_f32 v8, v14, v12
	s_waitcnt lgkmcnt(4)
	v_cvt_pk_bf16_f32 v9, v16, v18
	s_waitcnt lgkmcnt(2)
	v_cvt_pk_bf16_f32 v10, v20, v22
	s_waitcnt lgkmcnt(0)
	v_cvt_pk_bf16_f32 v11, v24, v78
	v_or_b32_e32 v2, s5, v2
	global_store_dwordx4 v[82:83], v[8:11], off sc1 nt
	v_lshlrev_b32_e32 v2, 11, v2
	s_nop 0
	v_cvt_pk_bf16_f32 v8, v15, v13
	v_cvt_pk_bf16_f32 v9, v17, v19
	v_cvt_pk_bf16_f32 v10, v21, v23
	v_cvt_pk_bf16_f32 v11, v25, v79
	v_lshl_add_u64 v[12:13], v[80:81], 0, v[2:3]
	ds_read2_b32 v[14:15], v29 offset0:49 offset1:57
	ds_read2_b32 v[16:17], v29 offset0:16 offset1:24
	ds_read2_b32 v[18:19], v29 offset0:82 offset1:90
	ds_read2_b32 v[20:21], v29 offset0:115 offset1:123
	ds_read2_b32 v[22:23], v29 offset0:148 offset1:156
	ds_read2_b32 v[24:25], v29 offset0:181 offset1:189
	ds_read2_b32 v[78:79], v29 offset0:214 offset1:222
	ds_read2_b32 v[82:83], v29 offset0:247 offset1:255
	v_or_b32_e32 v2, s4, v31
	v_or_b32_e32 v2, s5, v2
	v_lshlrev_b32_e32 v2, 11, v2
	global_store_dwordx4 v[12:13], v[8:11], off sc1 nt
	v_lshl_add_u64 v[12:13], v[80:81], 0, v[2:3]
	v_or_b32_e32 v2, s4, v32
	v_or_b32_e32 v2, s5, v2
	s_waitcnt lgkmcnt(6)
	v_cvt_pk_bf16_f32 v8, v16, v14
	s_waitcnt lgkmcnt(4)
	v_cvt_pk_bf16_f32 v9, v18, v20
	s_waitcnt lgkmcnt(2)
	v_cvt_pk_bf16_f32 v10, v22, v24
	s_waitcnt lgkmcnt(0)
	v_cvt_pk_bf16_f32 v11, v78, v82
	v_lshlrev_b32_e32 v2, 11, v2
	global_store_dwordx4 v[12:13], v[8:11], off sc1 nt
	v_lshl_add_u64 v[12:13], v[80:81], 0, v[2:3]
	s_nop 0
	v_cvt_pk_bf16_f32 v8, v17, v15
	v_cvt_pk_bf16_f32 v9, v19, v21
	v_cvt_pk_bf16_f32 v10, v23, v25
	v_cvt_pk_bf16_f32 v11, v79, v83
	global_store_dwordx4 v[12:13], v[8:11], off sc1 nt
	s_waitcnt lgkmcnt(0)

.LBB0_29:
	s_andn2_b64 vcc, exec, s[4:5]
	s_cbranch_vccnz .LBB0_8
	s_mul_i32 s5, s16, 0xa10000
	s_mul_hi_i32 s4, s16, 0xa10000
	s_add_u32 s17, s6, s5
	s_addc_u32 s19, s7, s4
	s_mul_i32 s5, s16, 0x580000
	s_mul_hi_i32 s4, s16, 0x580000
	s_add_u32 s18, s86, s5
	s_addc_u32 s14, s87, s4
	s_mul_i32 s4, s81, 0x2aab
	s_lshr_b32 s5, s4, 31
	s_ashr_i32 s4, s4, 19
	s_add_i32 s4, s4, s5
	s_mul_i32 s5, s4, 48
	s_sub_i32 s5, s81, s5
	s_sext_i32_i16 s5, s5
	s_lshl_b32 s16, s4, 6
	s_lshl_b32 s4, s5, 5
	s_ashr_i32 s5, s4, 31
	s_lshl_b64 s[82:83], s[4:5], 2
	v_or_b32_e32 v2, s16, v26
	s_add_u32 s82, s17, s82
	s_addc_u32 s83, s19, s83
	v_mov_b32_e32 v7, v3
	v_mul_i32_i24_e32 v10, 0x2840, v2
	v_mad_i32_i24 v12, v2, s52, v46
	v_mad_i32_i24 v14, v2, s52, v47
	v_mad_i32_i24 v16, v2, s52, v48
	v_mad_i32_i24 v18, v2, s52, v49
	v_mad_i32_i24 v20, v2, s52, v50
	v_mad_i32_i24 v22, v2, s52, v51
	v_mad_i32_i24 v24, v2, s52, v52
	v_mad_i32_i24 v78, v2, s52, v53
	v_mad_i32_i24 v80, v2, s52, v54
	v_mad_i32_i24 v82, v2, s52, v55
	v_mad_i32_i24 v84, v2, s52, v56
	v_mad_i32_i24 v86, v2, s52, v57
	v_mad_i32_i24 v88, v2, s52, v58
	v_mad_i32_i24 v90, v2, s52, v59
	v_mad_i32_i24 v92, v2, s52, v60
	v_mad_i32_i24 v94, v2, s52, v61
	v_mad_i32_i24 v96, v2, s52, v62
	v_mad_i32_i24 v98, v2, s52, v63
	v_mad_i32_i24 v100, v2, s52, v64
	v_mad_i32_i24 v102, v2, s52, v65
	v_mad_i32_i24 v104, v2, s52, v66
	v_mad_i32_i24 v106, v2, s52, v67
	v_mad_i32_i24 v108, v2, s52, v68
	v_mad_i32_i24 v110, v2, s52, v69
	v_mad_i32_i24 v112, v2, s52, v70
	v_mad_i32_i24 v114, v2, s52, v71
	v_mad_i32_i24 v116, v2, s52, v72
	v_mad_i32_i24 v118, v2, s52, v73
	v_mad_i32_i24 v120, v2, s52, v74
	v_mad_i32_i24 v122, v2, s52, v75
	v_mad_i32_i24 v124, v2, s52, v76
	v_lshl_add_u64 v[8:9], s[82:83], 0, v[6:7]
	v_ashrrev_i32_e32 v11, 31, v10
	v_ashrrev_i32_e32 v13, 31, v12
	v_ashrrev_i32_e32 v15, 31, v14
	v_ashrrev_i32_e32 v17, 31, v16
	v_ashrrev_i32_e32 v19, 31, v18
	v_ashrrev_i32_e32 v21, 31, v20
	v_ashrrev_i32_e32 v23, 31, v22
	v_ashrrev_i32_e32 v25, 31, v24
	v_ashrrev_i32_e32 v79, 31, v78
	v_ashrrev_i32_e32 v81, 31, v80
	v_ashrrev_i32_e32 v83, 31, v82
	v_ashrrev_i32_e32 v85, 31, v84
	v_ashrrev_i32_e32 v87, 31, v86
	v_ashrrev_i32_e32 v89, 31, v88
	v_ashrrev_i32_e32 v91, 31, v90
	v_ashrrev_i32_e32 v93, 31, v92
	v_ashrrev_i32_e32 v95, 31, v94
	v_ashrrev_i32_e32 v97, 31, v96
	v_ashrrev_i32_e32 v99, 31, v98
	v_ashrrev_i32_e32 v101, 31, v100
	v_ashrrev_i32_e32 v103, 31, v102
	v_ashrrev_i32_e32 v105, 31, v104
	v_ashrrev_i32_e32 v107, 31, v106
	v_ashrrev_i32_e32 v109, 31, v108
	v_ashrrev_i32_e32 v111, 31, v110
	v_ashrrev_i32_e32 v113, 31, v112
	v_ashrrev_i32_e32 v115, 31, v114
	v_ashrrev_i32_e32 v117, 31, v116
	v_ashrrev_i32_e32 v119, 31, v118
	v_ashrrev_i32_e32 v121, 31, v120
	v_ashrrev_i32_e32 v123, 31, v122
	v_ashrrev_i32_e32 v125, 31, v124
	v_lshl_add_u64 v[10:11], v[8:9], 0, v[10:11]
	v_lshl_add_u64 v[12:13], v[8:9], 0, v[12:13]
	v_lshl_add_u64 v[14:15], v[8:9], 0, v[14:15]
	v_lshl_add_u64 v[16:17], v[8:9], 0, v[16:17]
	v_lshl_add_u64 v[18:19], v[8:9], 0, v[18:19]
	v_lshl_add_u64 v[20:21], v[8:9], 0, v[20:21]
	v_lshl_add_u64 v[22:23], v[8:9], 0, v[22:23]
	v_lshl_add_u64 v[24:25], v[8:9], 0, v[24:25]
	v_lshl_add_u64 v[78:79], v[8:9], 0, v[78:79]
	v_lshl_add_u64 v[80:81], v[8:9], 0, v[80:81]
	v_lshl_add_u64 v[82:83], v[8:9], 0, v[82:83]
	v_lshl_add_u64 v[84:85], v[8:9], 0, v[84:85]
	v_lshl_add_u64 v[86:87], v[8:9], 0, v[86:87]
	v_lshl_add_u64 v[88:89], v[8:9], 0, v[88:89]
	v_lshl_add_u64 v[90:91], v[8:9], 0, v[90:91]
	v_lshl_add_u64 v[92:93], v[8:9], 0, v[92:93]
	v_lshl_add_u64 v[94:95], v[8:9], 0, v[94:95]
	v_lshl_add_u64 v[96:97], v[8:9], 0, v[96:97]
	v_lshl_add_u64 v[98:99], v[8:9], 0, v[98:99]
	v_lshl_add_u64 v[100:101], v[8:9], 0, v[100:101]
	v_lshl_add_u64 v[102:103], v[8:9], 0, v[102:103]
	v_lshl_add_u64 v[104:105], v[8:9], 0, v[104:105]
	v_lshl_add_u64 v[106:107], v[8:9], 0, v[106:107]
	v_lshl_add_u64 v[108:109], v[8:9], 0, v[108:109]
	v_lshl_add_u64 v[110:111], v[8:9], 0, v[110:111]
	v_lshl_add_u64 v[112:113], v[8:9], 0, v[112:113]
	v_lshl_add_u64 v[114:115], v[8:9], 0, v[114:115]
	v_lshl_add_u64 v[116:117], v[8:9], 0, v[116:117]
	v_lshl_add_u64 v[118:119], v[8:9], 0, v[118:119]
	v_lshl_add_u64 v[120:121], v[8:9], 0, v[120:121]
	v_lshl_add_u64 v[122:123], v[8:9], 0, v[122:123]
	v_lshl_add_u64 v[8:9], v[8:9], 0, v[124:125]
	global_load_dword v2, v[10:11], off nt
	global_load_dword v7, v[12:13], off nt
	s_nop 0
	global_load_dword v10, v[14:15], off nt
	global_load_dword v11, v[16:17], off nt
	global_load_dword v12, v[18:19], off nt
	global_load_dword v13, v[20:21], off nt
	s_nop 0
	global_load_dword v14, v[22:23], off nt
	global_load_dword v15, v[24:25], off nt
	global_load_dword v16, v[78:79], off nt
	global_load_dword v17, v[80:81], off nt
	global_load_dword v18, v[82:83], off nt
	global_load_dword v19, v[84:85], off nt
	global_load_dword v20, v[86:87], off nt
	global_load_dword v21, v[88:89], off nt
	global_load_dword v22, v[90:91], off nt
	global_load_dword v23, v[92:93], off nt
	global_load_dword v24, v[94:95], off nt
	global_load_dword v25, v[96:97], off nt
	global_load_dword v77, v[98:99], off nt
	global_load_dword v78, v[100:101], off nt
	global_load_dword v79, v[102:103], off nt
	global_load_dword v80, v[104:105], off nt
	global_load_dword v81, v[106:107], off nt
	global_load_dword v82, v[108:109], off nt
	global_load_dword v83, v[110:111], off nt
	global_load_dword v84, v[112:113], off nt
	global_load_dword v85, v[114:115], off nt
	global_load_dword v86, v[116:117], off nt
	global_load_dword v87, v[118:119], off nt
	global_load_dword v88, v[120:121], off nt
	global_load_dword v89, v[122:123], off nt
	s_nop 0
	global_load_dword v8, v[8:9], off nt
	s_waitcnt vmcnt(30)
	ds_write2_b32 v27, v2, v7 offset1:66
	s_waitcnt vmcnt(28)
	ds_write2_b32 v27, v10, v11 offset0:132 offset1:198
	s_waitcnt vmcnt(26)
	ds_write2_b32 v38, v12, v13 offset0:8 offset1:74
	s_waitcnt vmcnt(24)
	ds_write2_b32 v38, v14, v15 offset0:140 offset1:206
	s_waitcnt vmcnt(22)
	ds_write2_b32 v39, v16, v17 offset0:16 offset1:82
	s_waitcnt vmcnt(20)
	ds_write2_b32 v39, v18, v19 offset0:148 offset1:214
	s_waitcnt vmcnt(18)
	ds_write2_b32 v40, v20, v21 offset0:24 offset1:90
	s_waitcnt vmcnt(16)
	ds_write2_b32 v40, v22, v23 offset0:156 offset1:222
	s_waitcnt vmcnt(14)
	ds_write2_b32 v41, v24, v25 offset0:32 offset1:98
	s_waitcnt vmcnt(12)
	ds_write2_b32 v41, v77, v78 offset0:164 offset1:230
	s_waitcnt vmcnt(10)
	ds_write2_b32 v42, v79, v80 offset0:40 offset1:106
	s_waitcnt vmcnt(8)
	ds_write2_b32 v42, v81, v82 offset0:172 offset1:238
	s_waitcnt vmcnt(6)
	ds_write2_b32 v43, v83, v84 offset0:48 offset1:114
	s_waitcnt vmcnt(4)
	ds_write2_b32 v43, v85, v86 offset0:180 offset1:246
	s_waitcnt vmcnt(2)
	ds_write2_b32 v44, v87, v88 offset0:56 offset1:122
	s_waitcnt vmcnt(0)
	ds_write2_b32 v44, v89, v8 offset0:188 offset1:254
	s_waitcnt lgkmcnt(0)
	s_ashr_i32 s17, s16, 31
	ds_read2_b32 v[12:13], v29 offset0:33 offset1:41
	ds_read2_b32 v[14:15], v29 offset1:8
	ds_read2_b32 v[16:17], v29 offset0:66 offset1:74
	ds_read2_b32 v[18:19], v29 offset0:99 offset1:107
	ds_read2_b32 v[20:21], v29 offset0:132 offset1:140
	ds_read2_b32 v[22:23], v29 offset0:165 offset1:173
	ds_read2_b32 v[24:25], v29 offset0:198 offset1:206
	ds_read2_b32 v[78:79], v29 offset0:231 offset1:239
	s_lshl_b64 s[16:17], s[16:17], 1
	s_add_u32 s16, s18, s16
	v_or_b32_e32 v80, s4, v28
	s_addc_u32 s17, s14, s17
	v_lshlrev_b32_e32 v2, 1, v4
	v_ashrrev_i32_e32 v81, 31, v80
	v_lshlrev_b64 v[80:81], 11, v[80:81]
	v_lshl_add_u64 v[82:83], s[16:17], 0, v[2:3]
	s_waitcnt lgkmcnt(6)
	v_cvt_pk_bf16_f32 v8, v14, v12
	s_waitcnt lgkmcnt(4)
	v_cvt_pk_bf16_f32 v9, v16, v18
	s_waitcnt lgkmcnt(2)
	v_cvt_pk_bf16_f32 v10, v20, v22
	s_waitcnt lgkmcnt(0)
	v_cvt_pk_bf16_f32 v11, v24, v78
	v_lshl_add_u64 v[80:81], v[82:83], 0, v[80:81]
	v_or_b32_e32 v12, s4, v30
	global_store_dwordx4 v[80:81], v[8:11], off sc1 nt
	s_nop 1
	v_cvt_pk_bf16_f32 v8, v15, v13
	v_ashrrev_i32_e32 v13, 31, v12
	v_cvt_pk_bf16_f32 v9, v17, v19
	v_cvt_pk_bf16_f32 v10, v21, v23
	v_cvt_pk_bf16_f32 v11, v25, v79
	ds_read2_b32 v[14:15], v29 offset0:49 offset1:57
	ds_read2_b32 v[16:17], v29 offset0:16 offset1:24
	ds_read2_b32 v[18:19], v29 offset0:82 offset1:90
	ds_read2_b32 v[20:21], v29 offset0:115 offset1:123
	v_lshlrev_b64 v[12:13], 11, v[12:13]
	ds_read2_b32 v[22:23], v29 offset0:148 offset1:156
	ds_read2_b32 v[24:25], v29 offset0:181 offset1:189
	ds_read2_b32 v[78:79], v29 offset0:214 offset1:222
	ds_read2_b32 v[80:81], v29 offset0:247 offset1:255
	v_lshl_add_u64 v[12:13], v[82:83], 0, v[12:13]
	global_store_dwordx4 v[12:13], v[8:11], off sc1 nt
	v_or_b32_e32 v12, s4, v31
	v_ashrrev_i32_e32 v13, 31, v12
	v_lshlrev_b64 v[12:13], 11, v[12:13]
	s_waitcnt lgkmcnt(6)
	v_cvt_pk_bf16_f32 v8, v16, v14
	s_waitcnt lgkmcnt(4)
	v_cvt_pk_bf16_f32 v9, v18, v20
	s_waitcnt lgkmcnt(2)
	v_cvt_pk_bf16_f32 v10, v22, v24
	s_waitcnt lgkmcnt(0)
	v_cvt_pk_bf16_f32 v11, v78, v80
	v_lshl_add_u64 v[12:13], v[82:83], 0, v[12:13]
	global_store_dwordx4 v[12:13], v[8:11], off sc1 nt
	v_or_b32_e32 v12, s4, v32
	v_ashrrev_i32_e32 v13, 31, v12
	v_lshlrev_b64 v[12:13], 11, v[12:13]
	v_cvt_pk_bf16_f32 v8, v17, v15
	v_cvt_pk_bf16_f32 v9, v19, v21
	v_cvt_pk_bf16_f32 v10, v23, v25
	v_cvt_pk_bf16_f32 v11, v79, v81
	v_lshl_add_u64 v[12:13], v[82:83], 0, v[12:13]
	global_store_dwordx4 v[12:13], v[8:11], off sc1 nt
	s_waitcnt lgkmcnt(0)
	s_branch .LBB0_8

.LBB0_33:
	v_ashrrev_i32_e32 v12, 15, v14
	v_bfe_u32 v15, v14, 7, 8
	v_add_u32_e32 v14, s63, v14
	v_mad_i64_i32 v[16:17], s[38:39], v12, s25, v[4:5]
	v_mul_hi_i32_i24_e32 v19, 0x580000, v12
	v_mul_i32_i24_e32 v18, 0x580000, v12
	v_cmp_lt_i32_e32 vcc, s36, v14
	v_lshl_add_u64 v[16:17], v[16:17], 0, v[6:7]
	v_lshl_add_u64 v[144:145], s[86:87], 0, v[18:19]
	s_or_b64 s[8:9], vcc, s[8:9]
	v_add_co_u32_e32 v18, vcc, s26, v16
	v_ashrrev_i32_e32 v13, 31, v12
	s_nop 0
	v_addc_co_u32_e32 v19, vcc, 0, v17, vcc
	v_add_co_u32_e32 v20, vcc, s29, v16
	v_lshl_add_u64 v[40:41], v[16:17], 0, s[6:7]
	s_nop 0
	v_addc_co_u32_e32 v21, vcc, 0, v17, vcc
	v_add_co_u32_e32 v48, vcc, s30, v16
	v_lshl_add_u64 v[44:45], v[16:17], 0, s[10:11]
	s_nop 0
	v_addc_co_u32_e32 v49, vcc, 0, v17, vcc
	v_add_co_u32_e32 v64, vcc, s31, v16
	v_lshl_add_u64 v[60:61], v[16:17], 0, s[12:13]
	s_nop 0
	v_addc_co_u32_e32 v65, vcc, 0, v17, vcc
	v_add_co_u32_e32 v80, vcc, s33, v16
	v_lshl_add_u64 v[76:77], v[16:17], 0, s[14:15]
	s_nop 0
	v_addc_co_u32_e32 v81, vcc, 0, v17, vcc
	v_add_co_u32_e32 v96, vcc, s34, v16
	v_lshl_add_u64 v[92:93], v[16:17], 0, s[16:17]
	s_nop 0
	v_addc_co_u32_e32 v97, vcc, 0, v17, vcc
	v_add_co_u32_e32 v112, vcc, s24, v16
	v_lshl_add_u64 v[108:109], v[16:17], 0, s[18:19]
	s_nop 0
	v_addc_co_u32_e32 v113, vcc, 0, v17, vcc
	v_add_co_u32_e32 v128, vcc, s35, v16
	v_lshl_add_u64 v[124:125], v[16:17], 0, s[20:21]
	v_lshl_add_u64 v[140:141], v[16:17], 0, s[22:23]
	v_addc_co_u32_e32 v129, vcc, 0, v17, vcc
	global_load_dwordx4 v[16:19], v[18:19], off offset:2048
	s_nop 0
	global_load_dwordx4 v[20:23], v[20:21], off offset:64
	s_nop 0
	global_load_dwordx4 v[24:27], v[40:41], off offset:16
	global_load_dwordx4 v[28:31], v[44:45], off offset:16
	global_load_dwordx4 v[32:35], v[40:41], off offset:32
	global_load_dwordx4 v[36:39], v[44:45], off offset:32
	v_lshlrev_b64 v[12:13], 14, v[12:13]
	global_load_dwordx4 v[40:43], v[40:41], off offset:48
	s_nop 0
	global_load_dwordx4 v[44:47], v[44:45], off offset:48
	s_nop 0
	global_load_dwordx4 v[48:51], v[48:49], off offset:2176
	s_nop 0
	global_load_dwordx4 v[52:55], v[60:61], off offset:48
	global_load_dwordx4 v[56:59], v[60:61], off offset:16
	s_nop 0
	global_load_dwordx4 v[60:63], v[60:61], off offset:32
	s_nop 0
	global_load_dwordx4 v[64:67], v[64:65], off offset:192
	s_nop 0
	global_load_dwordx4 v[68:71], v[76:77], off offset:48
	global_load_dwordx4 v[72:75], v[76:77], off offset:16
	s_nop 0
	global_load_dwordx4 v[76:79], v[76:77], off offset:32
	s_nop 0
	global_load_dwordx4 v[80:83], v[80:81], off offset:2304
	s_nop 0
	global_load_dwordx4 v[84:87], v[92:93], off offset:48
	global_load_dwordx4 v[88:91], v[92:93], off offset:16
	s_nop 0
	global_load_dwordx4 v[92:95], v[92:93], off offset:32
	s_nop 0
	global_load_dwordx4 v[96:99], v[96:97], off offset:320
	s_nop 0
	global_load_dwordx4 v[100:103], v[108:109], off offset:48
	global_load_dwordx4 v[104:107], v[108:109], off offset:16
	s_nop 0
	global_load_dwordx4 v[108:111], v[108:109], off offset:32
	s_nop 0
	global_load_dwordx4 v[112:115], v[112:113], off offset:2432
	s_nop 0
	global_load_dwordx4 v[116:119], v[124:125], off offset:48
	global_load_dwordx4 v[120:123], v[124:125], off offset:16
	s_nop 0
	global_load_dwordx4 v[124:127], v[124:125], off offset:32
	s_nop 0
	global_load_dwordx4 v[128:131], v[128:129], off offset:448
	s_nop 0
	global_load_dwordx4 v[132:135], v[140:141], off offset:48
	global_load_dwordx4 v[136:139], v[140:141], off offset:16
	s_nop 0
	global_load_dwordx4 v[140:143], v[140:141], off offset:32
	v_lshlrev_b32_e32 v2, 2, v15
	v_lshl_add_u64 v[12:13], s[0:1], 0, v[12:13]
	v_lshl_add_u64 v[12:13], v[12:13], 0, v[2:3]
	global_load_dword v146, v[12:13], off
	global_load_dword v148, v[12:13], off offset:1024
	global_load_dword v150, v[12:13], off offset:2048
	global_load_dword v152, v[12:13], off offset:3072
	v_add_co_u32_e32 v154, vcc, s26, v12
	v_lshlrev_b32_e32 v2, 11, v15
	s_nop 0
	v_addc_co_u32_e32 v155, vcc, 0, v13, vcc
	v_add_co_u32_e32 v156, vcc, s27, v12
	v_lshl_add_u64 v[144:145], v[144:145], 0, v[2:3]
	s_nop 0
	v_addc_co_u32_e32 v157, vcc, 0, v13, vcc
	global_load_dword v2, v[154:155], off offset:1024
	global_load_dword v158, v[154:155], off offset:2048
	s_nop 0
	global_load_dword v154, v[154:155], off offset:3072
	s_nop 0
	global_load_dword v160, v[156:157], off offset:-4096
	global_load_dword v162, v[156:157], off
	global_load_dword v164, v[156:157], off offset:1024
	global_load_dword v166, v[156:157], off offset:2048
	s_nop 0
	global_load_dword v156, v[156:157], off offset:3072
	v_add_co_u32_e32 v12, vcc, s28, v12
	v_lshl_add_u64 v[144:145], v[144:145], 0, v[10:11]
	s_nop 0
	v_addc_co_u32_e32 v13, vcc, 0, v13, vcc
	global_load_dword v168, v[12:13], off
	global_load_dword v170, v[12:13], off offset:1024
	global_load_dword v172, v[12:13], off offset:2048
	s_nop 0
	global_load_dword v12, v[12:13], off offset:3072
	v_add_co_u32_e32 v144, vcc, 0x300000, v144
	s_waitcnt vmcnt(47)
	v_mov_b32_e32 v174, v16
	s_waitcnt vmcnt(46)
	v_mov_b32_e32 v175, v20
	v_mov_b32_e32 v20, v17
	v_mov_b32_e32 v16, v18
	v_mov_b32_e32 v17, v22
	v_mov_b32_e32 v22, v19
	s_waitcnt vmcnt(45)
	v_mov_b32_e32 v18, v24
	s_waitcnt vmcnt(44)
	v_mov_b32_e32 v19, v28
	v_mov_b32_e32 v28, v25
	v_mov_b32_e32 v24, v26
	v_mov_b32_e32 v25, v30
	v_mov_b32_e32 v30, v27
	s_waitcnt vmcnt(43)
	v_mov_b32_e32 v26, v32
	s_waitcnt vmcnt(42)
	v_mov_b32_e32 v27, v36
	v_mov_b32_e32 v36, v33
	v_mov_b32_e32 v32, v34
	v_mov_b32_e32 v33, v38
	v_mov_b32_e32 v38, v35
	s_waitcnt vmcnt(41)
	v_mov_b32_e32 v34, v40
	s_waitcnt vmcnt(40)
	v_mov_b32_e32 v35, v44
	v_mov_b32_e32 v44, v41
	v_mov_b32_e32 v40, v42
	v_mov_b32_e32 v41, v46
	v_mov_b32_e32 v46, v43
	s_waitcnt vmcnt(39)
	v_mov_b32_e32 v42, v48
	s_waitcnt vmcnt(35)
	v_mov_b32_e32 v43, v64
	v_mov_b32_e32 v64, v49
	v_mov_b32_e32 v48, v50
	v_mov_b32_e32 v49, v66
	v_mov_b32_e32 v66, v51
	v_mov_b32_e32 v50, v56
	s_waitcnt vmcnt(33)
	v_mov_b32_e32 v51, v72
	v_mov_b32_e32 v72, v57
	v_mov_b32_e32 v56, v58
	v_mov_b32_e32 v57, v74
	v_mov_b32_e32 v74, v59
	v_mov_b32_e32 v58, v60
	s_waitcnt vmcnt(32)
	v_mov_b32_e32 v59, v76
	v_mov_b32_e32 v76, v61
	v_mov_b32_e32 v60, v62
	v_mov_b32_e32 v61, v78
	v_mov_b32_e32 v78, v63
	v_mov_b32_e32 v62, v52
	v_mov_b32_e32 v63, v68
	v_mov_b32_e32 v68, v53
	v_mov_b32_e32 v52, v54
	v_mov_b32_e32 v53, v70
	v_mov_b32_e32 v70, v55
	s_waitcnt vmcnt(31)
	v_mov_b32_e32 v54, v80
	s_waitcnt vmcnt(27)
	v_mov_b32_e32 v55, v96
	v_mov_b32_e32 v96, v81
	v_mov_b32_e32 v80, v82
	v_mov_b32_e32 v81, v98
	v_mov_b32_e32 v98, v83
	v_mov_b32_e32 v82, v88
	s_waitcnt vmcnt(25)
	v_mov_b32_e32 v83, v104
	v_mov_b32_e32 v104, v89
	v_mov_b32_e32 v88, v90
	v_mov_b32_e32 v89, v106
	v_mov_b32_e32 v106, v91
	v_mov_b32_e32 v90, v92
	s_waitcnt vmcnt(24)
	v_mov_b32_e32 v91, v108
	v_mov_b32_e32 v108, v93
	v_mov_b32_e32 v92, v94
	v_mov_b32_e32 v93, v110
	v_mov_b32_e32 v110, v95
	v_mov_b32_e32 v94, v84
	v_mov_b32_e32 v95, v100
	v_mov_b32_e32 v100, v85
	v_mov_b32_e32 v84, v86
	v_mov_b32_e32 v85, v102
	v_mov_b32_e32 v102, v87
	s_waitcnt vmcnt(23)
	v_mov_b32_e32 v86, v112
	s_waitcnt vmcnt(19)
	v_mov_b32_e32 v87, v128
	v_mov_b32_e32 v128, v113
	v_mov_b32_e32 v112, v114
	v_mov_b32_e32 v113, v130
	v_mov_b32_e32 v130, v115
	v_mov_b32_e32 v114, v120
	s_waitcnt vmcnt(17)
	v_mov_b32_e32 v115, v136
	v_mov_b32_e32 v136, v121
	v_mov_b32_e32 v120, v122
	v_mov_b32_e32 v121, v138
	v_mov_b32_e32 v138, v123
	v_mov_b32_e32 v122, v124
	s_waitcnt vmcnt(16)
	v_mov_b32_e32 v123, v140
	v_mov_b32_e32 v140, v125
	v_mov_b32_e32 v124, v126
	v_mov_b32_e32 v125, v142
	v_mov_b32_e32 v142, v127
	v_mov_b32_e32 v126, v116
	v_mov_b32_e32 v127, v132
	v_mov_b32_e32 v132, v117
	v_mov_b32_e32 v116, v118
	v_mov_b32_e32 v117, v134
	v_mov_b32_e32 v134, v119
	s_waitcnt vmcnt(15)
	v_pk_fma_f32 v[118:119], v[146:147], v[174:175], 0 op_sel_hi:[0,1,0]
	v_pk_fma_f32 v[42:43], v[146:147], v[42:43], 0 op_sel_hi:[0,1,0]
	v_pk_fma_f32 v[54:55], v[146:147], v[54:55], 0 op_sel_hi:[0,1,0]
	v_pk_fma_f32 v[86:87], v[146:147], v[86:87], 0 op_sel_hi:[0,1,0]
	s_waitcnt vmcnt(14)
	v_pk_fma_f32 v[20:21], v[148:149], v[20:21], v[118:119] op_sel_hi:[0,1,1]
	v_pk_fma_f32 v[42:43], v[148:149], v[64:65], v[42:43] op_sel_hi:[0,1,1]
	v_pk_fma_f32 v[54:55], v[148:149], v[96:97], v[54:55] op_sel_hi:[0,1,1]
	v_pk_fma_f32 v[64:65], v[148:149], v[128:129], v[86:87] op_sel_hi:[0,1,1]
	s_waitcnt vmcnt(13)
	v_pk_fma_f32 v[16:17], v[150:151], v[16:17], v[20:21] op_sel_hi:[0,1,1]
	v_pk_fma_f32 v[20:21], v[150:151], v[48:49], v[42:43] op_sel_hi:[0,1,1]
	v_pk_fma_f32 v[42:43], v[150:151], v[80:81], v[54:55] op_sel_hi:[0,1,1]
	v_pk_fma_f32 v[48:49], v[150:151], v[112:113], v[64:65] op_sel_hi:[0,1,1]
	s_waitcnt vmcnt(12)
	v_pk_fma_f32 v[16:17], v[152:153], v[22:23], v[16:17] op_sel_hi:[0,1,1]
	v_pk_fma_f32 v[20:21], v[152:153], v[66:67], v[20:21] op_sel_hi:[0,1,1]
	v_pk_fma_f32 v[22:23], v[152:153], v[98:99], v[42:43] op_sel_hi:[0,1,1]
	v_pk_fma_f32 v[42:43], v[152:153], v[130:131], v[48:49] op_sel_hi:[0,1,1]
	s_waitcnt vmcnt(8)
	v_pk_fma_f32 v[16:17], v[160:161], v[18:19], v[16:17] op_sel_hi:[0,1,1]
	v_pk_fma_f32 v[18:19], v[160:161], v[50:51], v[20:21] op_sel_hi:[0,1,1]
	v_pk_fma_f32 v[20:21], v[160:161], v[82:83], v[22:23] op_sel_hi:[0,1,1]
	v_pk_fma_f32 v[22:23], v[160:161], v[114:115], v[42:43] op_sel_hi:[0,1,1]
	v_pk_fma_f32 v[16:17], v[2:3], v[28:29], v[16:17] op_sel_hi:[0,1,1]
	v_pk_fma_f32 v[18:19], v[2:3], v[72:73], v[18:19] op_sel_hi:[0,1,1]
	v_pk_fma_f32 v[20:21], v[2:3], v[104:105], v[20:21] op_sel_hi:[0,1,1]
	v_pk_fma_f32 v[22:23], v[2:3], v[136:137], v[22:23] op_sel_hi:[0,1,1]
	v_pk_fma_f32 v[16:17], v[158:159], v[24:25], v[16:17] op_sel_hi:[0,1,1]
	v_pk_fma_f32 v[18:19], v[158:159], v[56:57], v[18:19] op_sel_hi:[0,1,1]
	v_pk_fma_f32 v[20:21], v[158:159], v[88:89], v[20:21] op_sel_hi:[0,1,1]
	v_pk_fma_f32 v[22:23], v[158:159], v[120:121], v[22:23] op_sel_hi:[0,1,1]
	v_pk_fma_f32 v[16:17], v[154:155], v[30:31], v[16:17] op_sel_hi:[0,1,1]
	v_pk_fma_f32 v[18:19], v[154:155], v[74:75], v[18:19] op_sel_hi:[0,1,1]
	v_pk_fma_f32 v[20:21], v[154:155], v[106:107], v[20:21] op_sel_hi:[0,1,1]
	v_pk_fma_f32 v[22:23], v[154:155], v[138:139], v[22:23] op_sel_hi:[0,1,1]
	s_waitcnt vmcnt(7)
	v_pk_fma_f32 v[16:17], v[162:163], v[26:27], v[16:17] op_sel_hi:[0,1,1]
	v_pk_fma_f32 v[18:19], v[162:163], v[58:59], v[18:19] op_sel_hi:[0,1,1]
	v_pk_fma_f32 v[20:21], v[162:163], v[90:91], v[20:21] op_sel_hi:[0,1,1]
	v_pk_fma_f32 v[22:23], v[162:163], v[122:123], v[22:23] op_sel_hi:[0,1,1]
	s_waitcnt vmcnt(6)
	v_pk_fma_f32 v[16:17], v[164:165], v[36:37], v[16:17] op_sel_hi:[0,1,1]
	v_pk_fma_f32 v[18:19], v[164:165], v[76:77], v[18:19] op_sel_hi:[0,1,1]
	v_pk_fma_f32 v[20:21], v[164:165], v[108:109], v[20:21] op_sel_hi:[0,1,1]
	v_pk_fma_f32 v[22:23], v[164:165], v[140:141], v[22:23] op_sel_hi:[0,1,1]
	s_waitcnt vmcnt(5)
	v_pk_fma_f32 v[16:17], v[166:167], v[32:33], v[16:17] op_sel_hi:[0,1,1]
	v_pk_fma_f32 v[18:19], v[166:167], v[60:61], v[18:19] op_sel_hi:[0,1,1]
	v_pk_fma_f32 v[20:21], v[166:167], v[92:93], v[20:21] op_sel_hi:[0,1,1]
	v_pk_fma_f32 v[22:23], v[166:167], v[124:125], v[22:23] op_sel_hi:[0,1,1]
	s_waitcnt vmcnt(4)
	v_pk_fma_f32 v[16:17], v[156:157], v[38:39], v[16:17] op_sel_hi:[0,1,1]
	v_pk_fma_f32 v[18:19], v[156:157], v[78:79], v[18:19] op_sel_hi:[0,1,1]
	v_pk_fma_f32 v[20:21], v[156:157], v[110:111], v[20:21] op_sel_hi:[0,1,1]
	v_pk_fma_f32 v[22:23], v[156:157], v[142:143], v[22:23] op_sel_hi:[0,1,1]
	s_waitcnt vmcnt(3)
	v_pk_fma_f32 v[16:17], v[168:169], v[34:35], v[16:17] op_sel_hi:[0,1,1]
	v_pk_fma_f32 v[18:19], v[168:169], v[62:63], v[18:19] op_sel_hi:[0,1,1]
	v_pk_fma_f32 v[20:21], v[168:169], v[94:95], v[20:21] op_sel_hi:[0,1,1]
	v_pk_fma_f32 v[22:23], v[168:169], v[126:127], v[22:23] op_sel_hi:[0,1,1]
	s_waitcnt vmcnt(2)
	v_pk_fma_f32 v[16:17], v[170:171], v[44:45], v[16:17] op_sel_hi:[0,1,1]
	v_pk_fma_f32 v[18:19], v[170:171], v[68:69], v[18:19] op_sel_hi:[0,1,1]
	v_pk_fma_f32 v[20:21], v[170:171], v[100:101], v[20:21] op_sel_hi:[0,1,1]
	v_pk_fma_f32 v[22:23], v[170:171], v[132:133], v[22:23] op_sel_hi:[0,1,1]
	s_waitcnt vmcnt(1)
	v_pk_fma_f32 v[16:17], v[172:173], v[40:41], v[16:17] op_sel_hi:[0,1,1]
	v_pk_fma_f32 v[18:19], v[172:173], v[52:53], v[18:19] op_sel_hi:[0,1,1]
	v_pk_fma_f32 v[20:21], v[172:173], v[84:85], v[20:21] op_sel_hi:[0,1,1]
	v_pk_fma_f32 v[22:23], v[172:173], v[116:117], v[22:23] op_sel_hi:[0,1,1]
	s_waitcnt vmcnt(0)
	v_pk_fma_f32 v[16:17], v[12:13], v[46:47], v[16:17] op_sel_hi:[0,1,1]
	v_pk_fma_f32 v[18:19], v[12:13], v[70:71], v[18:19] op_sel_hi:[0,1,1]
	v_pk_fma_f32 v[20:21], v[12:13], v[102:103], v[20:21] op_sel_hi:[0,1,1]
	v_pk_fma_f32 v[12:13], v[12:13], v[134:135], v[22:23] op_sel_hi:[0,1,1]
	v_addc_co_u32_e32 v145, vcc, 0, v145, vcc
	v_cvt_pk_bf16_f32 v16, v16, v17
	v_cvt_pk_bf16_f32 v17, v18, v19
	v_cvt_pk_bf16_f32 v18, v20, v21
	v_cvt_pk_bf16_f32 v19, v12, v13
	global_store_dwordx4 v[144:145], v[16:19], off sc1 nt
	s_andn2_b64 exec, exec, s[8:9]
	s_cbranch_execnz .LBB0_33

.LBB0_36:
	s_or_b64 exec, exec, s[4:5]
	s_waitcnt vmcnt(0)
	v_bfe_u32 v10, v19, 16, 1
	v_add3_u32 v10, v19, v10, s18
	v_and_b32_e32 v10, 0xffff0000, v10
	v_sub_f32_e32 v26, v19, v10
	v_bfe_u32 v10, v16, 16, 1
	v_add3_u32 v10, v16, v10, s18
	v_and_b32_e32 v10, 0xffff0000, v10
	v_sub_f32_e32 v27, v16, v10
	v_bfe_u32 v10, v17, 16, 1
	v_add3_u32 v10, v17, v10, s18
	v_and_b32_e32 v10, 0xffff0000, v10
	v_sub_f32_e32 v28, v17, v10
	v_bfe_u32 v10, v15, 16, 1
	v_add3_u32 v10, v15, v10, s18
	v_and_b32_e32 v10, 0xffff0000, v10
	v_sub_f32_e32 v29, v15, v10
	v_bfe_u32 v10, v5, 16, 1
	v_add3_u32 v10, v5, v10, s18
	v_and_b32_e32 v10, 0xffff0000, v10
	v_sub_f32_e32 v30, v5, v10
	v_bfe_u32 v10, v21, 16, 1
	v_add3_u32 v10, v21, v10, s18
	v_bfe_u32 v6, v20, 16, 1
	v_and_b32_e32 v10, 0xffff0000, v10
	v_add3_u32 v6, v20, v6, s18
	v_sub_f32_e32 v31, v21, v10
	v_mad_i32_i24 v10, v4, s19, v2
	v_and_b32_e32 v6, 0xffff0000, v6
	v_ashrrev_i32_e32 v11, 31, v10
	v_sub_f32_e32 v7, v20, v6
	v_bfe_u32 v6, v18, 16, 1
	v_cvt_pk_bf16_f32 v22, v15, v5
	v_lshlrev_b64 v[4:5], 11, v[10:11]
	v_readlane_b32 s4, v255, 26
	v_add_u32_e32 v10, 48, v10
	v_add3_u32 v6, v18, v6, s18
	v_readlane_b32 s5, v255, 27
	v_ashrrev_i32_e32 v11, 31, v10
	v_and_b32_e32 v6, 0xffff0000, v6
	v_lshl_add_u64 v[4:5], s[4:5], 0, v[4:5]
	v_lshlrev_b32_e32 v2, 1, v14
	v_lshlrev_b64 v[10:11], 11, v[10:11]
	v_add_u32_e32 v13, s63, v13
	v_sub_f32_e32 v6, v18, v6
	v_cvt_pk_bf16_f32 v23, v16, v17
	v_cvt_pk_bf16_f32 v24, v18, v19
	v_cvt_pk_bf16_f32 v25, v20, v21
	v_lshl_add_u64 v[4:5], v[4:5], 0, v[2:3]
	v_lshl_add_u64 v[10:11], s[4:5], 0, v[10:11]
	v_cmp_lt_i32_e32 vcc, s20, v13
	global_store_dwordx4 v[4:5], v[22:25], off sc1 nt
	v_cvt_pk_bf16_f32 v4, v29, v30
	v_cvt_pk_bf16_f32 v5, v27, v28
	v_cvt_pk_bf16_f32 v6, v6, v26
	v_cvt_pk_bf16_f32 v7, v7, v31
	v_lshl_add_u64 v[10:11], v[10:11], 0, v[2:3]
	s_or_b64 s[10:11], vcc, s[10:11]
	v_add_u32_e32 v12, s16, v12
	global_store_dwordx4 v[10:11], v[4:7], off sc1 nt
	s_andn2_b64 exec, exec, s[10:11]
	s_cbranch_execz .LBB0_85

.LBB0_110:
	s_add_i32 s30, s29, s3
	s_lshl_b64 s[20:21], s[8:9], 2
	s_add_u32 s18, s18, s20
	s_addc_u32 s19, s19, s21
	v_lshl_add_u64 v[22:23], s[18:19], 0, v[2:3]
	s_ashr_i32 s18, s30, 31
	s_mul_i32 s31, s16, s18
	s_mul_hi_u32 s18, s16, s30
	s_add_i32 s18, s18, s31
	s_mul_i32 s19, s17, s30
	s_add_i32 s19, s18, s19
	s_mul_i32 s18, s16, s30
	v_lshl_add_u64 v[24:25], s[18:19], 2, v[22:23]
	s_lshl_b64 s[18:19], s[16:17], 2
	v_lshl_add_u64 v[26:27], v[24:25], 0, s[18:19]
	global_load_dword v30, v[26:27], off nt
	s_or_b32 s20, s30, 2
	s_mul_hi_u32 s21, s16, s20
	s_add_i32 s21, s21, s31
	s_mul_i32 s33, s17, s20
	s_add_i32 s21, s21, s33
	s_mul_i32 s20, s16, s20
	v_lshl_add_u64 v[28:29], s[20:21], 2, v[22:23]
	global_load_dword v31, v[28:29], off nt
	global_load_dword v32, v[24:25], off nt
	global_load_dword v33, v[24:25], off offset:256 nt
	global_load_dword v34, v[24:25], off offset:512 nt
	global_load_dword v35, v[24:25], off offset:768 nt
	global_load_dword v36, v[24:25], off offset:1024 nt
	global_load_dword v37, v[24:25], off offset:1280 nt
	global_load_dword v38, v[24:25], off offset:1536 nt
	global_load_dword v39, v[24:25], off offset:1792 nt
	v_lshl_add_u64 v[24:25], v[28:29], 0, s[18:19]
	global_load_dword v40, v[24:25], off nt
	global_load_dword v41, v[28:29], off offset:256 nt
	global_load_dword v42, v[26:27], off offset:256 nt
	global_load_dword v43, v[26:27], off offset:512 nt
	global_load_dword v44, v[26:27], off offset:768 nt
	global_load_dword v45, v[26:27], off offset:1024 nt
	global_load_dword v46, v[26:27], off offset:1280 nt
	global_load_dword v47, v[26:27], off offset:1536 nt
	global_load_dword v48, v[26:27], off offset:1792 nt
	global_load_dword v49, v[24:25], off offset:256 nt
	global_load_dword v50, v[28:29], off offset:512 nt
	global_load_dword v51, v[28:29], off offset:768 nt
	global_load_dword v52, v[28:29], off offset:1024 nt
	global_load_dword v53, v[28:29], off offset:1280 nt
	global_load_dword v54, v[28:29], off offset:1536 nt
	s_nop 0
	global_load_dword v29, v[28:29], off offset:1792 nt
	s_nop 0
	global_load_dword v28, v[24:25], off offset:512 nt
	global_load_dword v55, v[24:25], off offset:768 nt
	global_load_dword v56, v[24:25], off offset:1024 nt
	global_load_dword v57, v[24:25], off offset:1280 nt
	global_load_dword v58, v[24:25], off offset:1536 nt
	global_load_dword v59, v[24:25], off offset:1792 nt
	s_or_b32 s20, s30, 4
	s_mul_hi_u32 s21, s16, s20
	s_add_i32 s21, s21, s31
	s_mul_i32 s33, s17, s20
	s_add_i32 s21, s21, s33
	s_mul_i32 s20, s16, s20
	v_lshl_add_u64 v[24:25], s[20:21], 2, v[22:23]
	s_or_b32 s20, s30, 6
	v_lshl_add_u64 v[26:27], v[24:25], 0, s[18:19]
	global_load_dword v60, v[24:25], off nt
	global_load_dword v61, v[24:25], off offset:256 nt
	global_load_dword v62, v[24:25], off offset:512 nt
	global_load_dword v63, v[24:25], off offset:768 nt
	global_load_dword v64, v[24:25], off offset:1024 nt
	global_load_dword v65, v[24:25], off offset:1280 nt
	global_load_dword v66, v[24:25], off offset:1536 nt
	global_load_dword v67, v[24:25], off offset:1792 nt
	global_load_dword v68, v[26:27], off nt
	global_load_dword v69, v[26:27], off offset:256 nt
	global_load_dword v70, v[26:27], off offset:512 nt
	global_load_dword v71, v[26:27], off offset:768 nt
	global_load_dword v72, v[26:27], off offset:1024 nt
	global_load_dword v73, v[26:27], off offset:1280 nt
	global_load_dword v74, v[26:27], off offset:1536 nt
	global_load_dword v75, v[26:27], off offset:1792 nt
	s_mul_hi_u32 s21, s16, s20
	s_add_i32 s21, s21, s31
	s_mul_i32 s17, s17, s20
	s_add_i32 s17, s21, s17
	s_mul_i32 s16, s16, s20
	v_lshl_add_u64 v[22:23], s[16:17], 2, v[22:23]
	v_lshl_add_u64 v[24:25], v[22:23], 0, s[18:19]
	global_load_dword v27, v[22:23], off nt
	global_load_dword v76, v[22:23], off offset:256 nt
	global_load_dword v77, v[22:23], off offset:512 nt
	global_load_dword v78, v[22:23], off offset:768 nt
	global_load_dword v79, v[22:23], off offset:1024 nt
	global_load_dword v80, v[22:23], off offset:1280 nt
	global_load_dword v81, v[22:23], off offset:1536 nt
	global_load_dword v82, v[22:23], off offset:1792 nt
	global_load_dword v83, v[24:25], off nt
	global_load_dword v84, v[24:25], off offset:256 nt
	global_load_dword v85, v[24:25], off offset:512 nt
	global_load_dword v86, v[24:25], off offset:768 nt
	global_load_dword v87, v[24:25], off offset:1024 nt
	global_load_dword v88, v[24:25], off offset:1280 nt
	global_load_dword v89, v[24:25], off offset:1536 nt
	global_load_dword v90, v[24:25], off offset:1792 nt
	s_lshl_b64 s[12:13], s[12:13], 20
	v_readlane_b32 s16, v255, 30
	s_add_u32 s16, s16, s12
	v_readlane_b32 s12, v255, 31
	s_addc_u32 s17, s12, s13
	v_readlane_b32 s12, v255, 32
	s_add_u32 s14, s12, s14
	v_readlane_b32 s12, v255, 33
	s_addc_u32 s15, s12, s15
	s_and_b64 s[12:13], s[10:11], exec
	s_cselect_b32 s12, s14, s16
	s_waitcnt vmcnt(63) expcnt(7) lgkmcnt(15)
	s_barrier
	s_cselect_b32 s13, s15, s17
	s_add_u32 s12, s12, s29
	s_addc_u32 s13, s13, 0
	s_waitcnt vmcnt(62)
	v_mul_f32_e32 v24, 0x42000000, v31
	s_waitcnt vmcnt(61)
	v_mul_f32_e32 v22, 0x42000000, v32
	v_mul_f32_e32 v23, 0x42000000, v30
	v_med3_f32 v25, v22, s25, v16
	v_med3_f32 v23, v23, s25, v16
	v_mov_b32_e32 v22, 0
	v_cvt_pk_fp8_f32 v22, v25, v23
	s_waitcnt vmcnt(53)
	v_mul_f32_e32 v23, 0x42000000, v40
	v_med3_f32 v24, v24, s25, v16
	v_med3_f32 v23, v23, s25, v16
	v_cvt_pk_fp8_f32 v22, v24, v23 op_sel:[0,0,1]
	v_mul_f32_e32 v23, 0x42000000, v33
	s_waitcnt vmcnt(51)
	v_mul_f32_e32 v24, 0x42000000, v42
	v_med3_f32 v23, v23, s25, v16
	v_med3_f32 v26, v24, s25, v16
	v_mov_b32_e32 v24, 0
	v_cvt_pk_fp8_f32 v24, v23, v26
	v_mul_f32_e32 v25, 0x42000000, v41
	s_waitcnt vmcnt(44)
	v_mul_f32_e32 v23, 0x42000000, v49
	v_med3_f32 v25, v25, s25, v16
	v_med3_f32 v23, v23, s25, v16
	v_cvt_pk_fp8_f32 v24, v25, v23 op_sel:[0,0,1]
	v_mul_f32_e32 v23, 0x42000000, v34
	v_mul_f32_e32 v25, 0x42000000, v43
	v_med3_f32 v23, v23, s25, v16
	v_med3_f32 v25, v25, s25, v16
	v_mov_b32_e32 v26, 0
	v_cvt_pk_fp8_f32 v26, v23, v25
	s_waitcnt vmcnt(43)
	v_mul_f32_e32 v30, 0x42000000, v50
	s_waitcnt vmcnt(37)
	v_mul_f32_e32 v23, 0x42000000, v28
	v_med3_f32 v25, v30, s25, v16
	v_med3_f32 v23, v23, s25, v16
	v_cvt_pk_fp8_f32 v26, v25, v23 op_sel:[0,0,1]
	v_mul_f32_e32 v23, 0x42000000, v35
	v_mul_f32_e32 v25, 0x42000000, v44
	v_med3_f32 v23, v23, s25, v16
	v_med3_f32 v25, v25, s25, v16
	v_mov_b32_e32 v28, 0
	v_cvt_pk_fp8_f32 v28, v23, v25
	v_mul_f32_e32 v30, 0x42000000, v51
	s_waitcnt vmcnt(36)
	v_mul_f32_e32 v23, 0x42000000, v55
	v_med3_f32 v25, v30, s25, v16
	v_med3_f32 v23, v23, s25, v16
	v_cvt_pk_fp8_f32 v28, v25, v23 op_sel:[0,0,1]
	v_mul_f32_e32 v23, 0x42000000, v36
	v_mul_f32_e32 v25, 0x42000000, v45
	v_med3_f32 v23, v23, s25, v16
	v_med3_f32 v25, v25, s25, v16
	v_mov_b32_e32 v30, 0
	v_cvt_pk_fp8_f32 v30, v23, v25
	v_mul_f32_e32 v31, 0x42000000, v52
	s_waitcnt vmcnt(35)
	v_mul_f32_e32 v23, 0x42000000, v56
	v_med3_f32 v25, v31, s25, v16
	v_med3_f32 v23, v23, s25, v16
	v_cvt_pk_fp8_f32 v30, v25, v23 op_sel:[0,0,1]
	v_mul_f32_e32 v23, 0x42000000, v37
	v_mul_f32_e32 v25, 0x42000000, v46
	v_med3_f32 v23, v23, s25, v16
	v_med3_f32 v25, v25, s25, v16
	v_mov_b32_e32 v32, 0
	v_cvt_pk_fp8_f32 v32, v23, v25
	v_mul_f32_e32 v31, 0x42000000, v53
	s_waitcnt vmcnt(34)
	v_mul_f32_e32 v23, 0x42000000, v57
	v_med3_f32 v25, v31, s25, v16
	v_med3_f32 v23, v23, s25, v16
	v_cvt_pk_fp8_f32 v32, v25, v23 op_sel:[0,0,1]
	v_mul_f32_e32 v23, 0x42000000, v38
	v_mul_f32_e32 v25, 0x42000000, v47
	v_med3_f32 v23, v23, s25, v16
	v_med3_f32 v25, v25, s25, v16
	v_mov_b32_e32 v34, 0
	v_cvt_pk_fp8_f32 v34, v23, v25
	v_mul_f32_e32 v31, 0x42000000, v54
	s_waitcnt vmcnt(33)
	v_mul_f32_e32 v23, 0x42000000, v58
	v_med3_f32 v25, v31, s25, v16
	v_med3_f32 v23, v23, s25, v16
	v_cvt_pk_fp8_f32 v34, v25, v23 op_sel:[0,0,1]
	v_mul_f32_e32 v23, 0x42000000, v39
	v_mul_f32_e32 v25, 0x42000000, v48
	v_med3_f32 v23, v23, s25, v16
	v_med3_f32 v25, v25, s25, v16
	v_mov_b32_e32 v36, 0
	v_cvt_pk_fp8_f32 v36, v23, v25
	v_mul_f32_e32 v29, 0x42000000, v29
	s_waitcnt vmcnt(32)
	v_mul_f32_e32 v23, 0x42000000, v59
	v_med3_f32 v25, v29, s25, v16
	v_med3_f32 v23, v23, s25, v16
	v_cvt_pk_fp8_f32 v36, v25, v23 op_sel:[0,0,1]
	s_waitcnt vmcnt(31)
	v_mul_f32_e32 v23, 0x42000000, v60
	s_waitcnt vmcnt(23)
	v_mul_f32_e32 v25, 0x42000000, v68
	v_med3_f32 v29, v23, s25, v16
	v_med3_f32 v25, v25, s25, v16
	v_mov_b32_e32 v23, 0
	v_cvt_pk_fp8_f32 v23, v29, v25
	s_waitcnt vmcnt(15)
	v_mul_f32_e32 v27, 0x42000000, v27
	s_waitcnt vmcnt(7)
	v_mul_f32_e32 v25, 0x42000000, v83
	v_med3_f32 v27, v27, s25, v16
	v_med3_f32 v25, v25, s25, v16
	v_cvt_pk_fp8_f32 v23, v27, v25 op_sel:[0,0,1]
	v_mul_f32_e32 v25, 0x42000000, v61
	v_mul_f32_e32 v27, 0x42000000, v69
	v_med3_f32 v31, v25, s25, v16
	v_med3_f32 v27, v27, s25, v16
	v_mov_b32_e32 v25, 0
	v_cvt_pk_fp8_f32 v25, v31, v27
	v_mul_f32_e32 v29, 0x42000000, v76
	s_waitcnt vmcnt(6)
	v_mul_f32_e32 v27, 0x42000000, v84
	v_med3_f32 v29, v29, s25, v16
	v_med3_f32 v27, v27, s25, v16
	v_cvt_pk_fp8_f32 v25, v29, v27 op_sel:[0,0,1]
	v_mul_f32_e32 v27, 0x42000000, v62
	v_mul_f32_e32 v29, 0x42000000, v70
	v_med3_f32 v33, v27, s25, v16
	v_med3_f32 v29, v29, s25, v16
	v_mov_b32_e32 v27, 0
	v_cvt_pk_fp8_f32 v27, v33, v29
	v_mul_f32_e32 v31, 0x42000000, v77
	s_waitcnt vmcnt(5)
	v_mul_f32_e32 v29, 0x42000000, v85
	v_med3_f32 v31, v31, s25, v16
	v_med3_f32 v29, v29, s25, v16
	v_cvt_pk_fp8_f32 v27, v31, v29 op_sel:[0,0,1]
	v_mul_f32_e32 v29, 0x42000000, v63
	v_mul_f32_e32 v31, 0x42000000, v71
	v_med3_f32 v35, v29, s25, v16
	v_med3_f32 v31, v31, s25, v16
	v_mov_b32_e32 v29, 0
	v_cvt_pk_fp8_f32 v29, v35, v31
	v_mul_f32_e32 v33, 0x42000000, v78
	s_waitcnt vmcnt(4)
	v_mul_f32_e32 v31, 0x42000000, v86
	v_med3_f32 v33, v33, s25, v16
	v_med3_f32 v31, v31, s25, v16
	v_cvt_pk_fp8_f32 v29, v33, v31 op_sel:[0,0,1]
	v_mul_f32_e32 v31, 0x42000000, v64
	v_mul_f32_e32 v33, 0x42000000, v72
	v_med3_f32 v37, v31, s25, v16
	v_med3_f32 v33, v33, s25, v16
	v_mov_b32_e32 v31, 0
	v_cvt_pk_fp8_f32 v31, v37, v33
	v_mul_f32_e32 v35, 0x42000000, v79
	s_waitcnt vmcnt(3)
	v_mul_f32_e32 v33, 0x42000000, v87
	v_med3_f32 v35, v35, s25, v16
	v_med3_f32 v33, v33, s25, v16
	v_cvt_pk_fp8_f32 v31, v35, v33 op_sel:[0,0,1]
	v_mul_f32_e32 v33, 0x42000000, v65
	v_mul_f32_e32 v35, 0x42000000, v73
	v_med3_f32 v38, v33, s25, v16
	v_med3_f32 v35, v35, s25, v16
	v_mov_b32_e32 v33, 0
	v_cvt_pk_fp8_f32 v33, v38, v35
	v_mul_f32_e32 v37, 0x42000000, v80
	s_waitcnt vmcnt(2)
	v_mul_f32_e32 v35, 0x42000000, v88
	v_med3_f32 v37, v37, s25, v16
	v_med3_f32 v35, v35, s25, v16
	v_cvt_pk_fp8_f32 v33, v37, v35 op_sel:[0,0,1]
	v_mul_f32_e32 v35, 0x42000000, v66
	v_mul_f32_e32 v37, 0x42000000, v74
	v_med3_f32 v39, v35, s25, v16
	v_med3_f32 v37, v37, s25, v16
	v_mov_b32_e32 v35, 0
	v_cvt_pk_fp8_f32 v35, v39, v37
	v_mul_f32_e32 v38, 0x42000000, v81
	s_waitcnt vmcnt(1)
	v_mul_f32_e32 v37, 0x42000000, v89
	v_med3_f32 v38, v38, s25, v16
	v_med3_f32 v37, v37, s25, v16
	v_cvt_pk_fp8_f32 v35, v38, v37 op_sel:[0,0,1]
	v_mul_f32_e32 v37, 0x42000000, v67
	v_mul_f32_e32 v38, 0x42000000, v75
	v_med3_f32 v40, v37, s25, v16
	v_med3_f32 v38, v38, s25, v16
	v_mov_b32_e32 v37, 0
	v_cvt_pk_fp8_f32 v37, v40, v38
	v_mul_f32_e32 v39, 0x42000000, v82
	s_waitcnt vmcnt(0)
	v_mul_f32_e32 v38, 0x42000000, v90
	v_med3_f32 v39, v39, s25, v16
	v_med3_f32 v38, v38, s25, v16
	v_cvt_pk_fp8_f32 v37, v39, v38 op_sel:[0,0,1]
	ds_write2st64_b64 v17, v[22:23], v[24:25] offset1:9
	ds_write2st64_b64 v17, v[26:27], v[28:29] offset0:18 offset1:27
	ds_write2st64_b64 v17, v[30:31], v[32:33] offset0:36 offset1:45
	ds_write2st64_b64 v17, v[34:35], v[36:37] offset0:54 offset1:63
	v_add_u32_e32 v27, s8, v4
	s_waitcnt lgkmcnt(0)
	s_barrier
	ds_read2_b64 v[22:25], v18 offset1:1
	v_or_b32_e32 v26, s28, v5
	v_and_or_b32 v27, v27, s22, v6
	v_cndmask_b32_e64 v26, v26, v27, s[10:11]
	v_lshl_add_u64 v[30:31], s[12:13], 0, v[0:1]
	s_and_b64 s[12:13], s[10:11], exec
	v_ashrrev_i32_e32 v27, 31, v26
	s_cselect_b32 s12, 9, 10
	v_lshlrev_b64 v[26:27], s12, v[26:27]
	v_lshl_add_u64 v[32:33], v[30:31], 0, v[26:27]
	ds_read2_b64 v[26:29], v19 offset1:1
	s_waitcnt lgkmcnt(1)
	global_store_dwordx4 v[32:33], v[22:25], off sc1 nt
	s_add_i32 s27, s27, s44
	s_add_i32 s23, s23, s24
	v_add_u32_e32 v22, s8, v7
	v_and_or_b32 v22, v22, s22, v9
	v_or_b32_e32 v23, s28, v8
	v_cndmask_b32_e64 v22, v23, v22, s[10:11]
	v_ashrrev_i32_e32 v23, 31, v22
	v_lshlrev_b64 v[22:23], s12, v[22:23]
	v_lshl_add_u64 v[22:23], v[30:31], 0, v[22:23]
	s_waitcnt lgkmcnt(0)
	global_store_dwordx4 v[22:23], v[26:29], off sc1 nt
	ds_read2_b64 v[22:25], v20 offset1:1
	s_add_i32 s26, s26, s63
	v_add_u32_e32 v26, s8, v10
	v_and_or_b32 v26, v26, s22, v12
	v_or_b32_e32 v27, s28, v11
	v_cndmask_b32_e64 v26, v27, v26, s[10:11]
	v_ashrrev_i32_e32 v27, 31, v26
	v_lshlrev_b64 v[26:27], s12, v[26:27]
	v_lshl_add_u64 v[32:33], v[30:31], 0, v[26:27]
	ds_read2_b64 v[26:29], v21 offset1:1
	s_waitcnt lgkmcnt(1)
	global_store_dwordx4 v[32:33], v[22:25], off sc1 nt
	s_cmpk_lt_i32 s27, 0x600
	s_nop 0
	v_add_u32_e32 v22, s8, v13
	v_and_or_b32 v22, v22, s22, v15
	v_or_b32_e32 v23, s28, v14
	v_cndmask_b32_e64 v22, v23, v22, s[10:11]
	v_ashrrev_i32_e32 v23, 31, v22
	v_lshlrev_b64 v[22:23], s12, v[22:23]
	v_lshl_add_u64 v[22:23], v[30:31], 0, v[22:23]
	s_waitcnt lgkmcnt(0)
	global_store_dwordx4 v[22:23], v[26:29], off sc1 nt
	s_cbranch_scc0 .LBB0_119

.LBB0_172:
	s_add_i32 s15, s29, s7
	s_lshl_b64 s[20:21], s[66:67], 2
	s_add_u32 s18, s18, s20
	s_addc_u32 s19, s19, s21
	v_lshl_add_u64 v[20:21], s[18:19], 0, v[0:1]
	s_ashr_i32 s18, s15, 31
	s_mul_i32 s22, s16, s18
	s_mul_hi_u32 s18, s16, s15
	s_add_i32 s18, s18, s22
	s_mul_i32 s19, s17, s15
	s_add_i32 s19, s18, s19
	s_mul_i32 s18, s16, s15
	v_lshl_add_u64 v[22:23], s[18:19], 2, v[20:21]
	s_lshl_b64 s[18:19], s[16:17], 2
	v_lshl_add_u64 v[24:25], v[22:23], 0, s[18:19]
	global_load_dword v19, v[24:25], off nt
	s_or_b32 s20, s15, 2
	s_mul_hi_u32 s21, s16, s20
	s_add_i32 s21, s21, s22
	s_mul_i32 s23, s17, s20
	s_add_i32 s21, s21, s23
	s_mul_i32 s20, s16, s20
	v_lshl_add_u64 v[26:27], s[20:21], 2, v[20:21]
	global_load_dword v28, v[26:27], off nt
	global_load_dword v29, v[22:23], off nt
	global_load_dword v30, v[22:23], off offset:256 nt
	global_load_dword v31, v[22:23], off offset:512 nt
	global_load_dword v32, v[22:23], off offset:768 nt
	global_load_dword v33, v[22:23], off offset:1024 nt
	global_load_dword v34, v[22:23], off offset:1280 nt
	global_load_dword v35, v[22:23], off offset:1536 nt
	global_load_dword v36, v[22:23], off offset:1792 nt
	v_lshl_add_u64 v[22:23], v[26:27], 0, s[18:19]
	global_load_dword v37, v[22:23], off nt
	global_load_dword v38, v[26:27], off offset:256 nt
	global_load_dword v39, v[24:25], off offset:256 nt
	global_load_dword v40, v[24:25], off offset:512 nt
	global_load_dword v41, v[24:25], off offset:768 nt
	global_load_dword v42, v[24:25], off offset:1024 nt
	global_load_dword v43, v[24:25], off offset:1280 nt
	global_load_dword v44, v[24:25], off offset:1536 nt
	global_load_dword v45, v[24:25], off offset:1792 nt
	global_load_dword v46, v[22:23], off offset:256 nt
	global_load_dword v47, v[26:27], off offset:512 nt
	global_load_dword v48, v[26:27], off offset:768 nt
	global_load_dword v49, v[26:27], off offset:1024 nt
	global_load_dword v50, v[26:27], off offset:1280 nt
	global_load_dword v51, v[26:27], off offset:1536 nt
	s_nop 0
	global_load_dword v27, v[26:27], off offset:1792 nt
	s_nop 0
	global_load_dword v26, v[22:23], off offset:512 nt
	global_load_dword v52, v[22:23], off offset:768 nt
	global_load_dword v53, v[22:23], off offset:1024 nt
	global_load_dword v54, v[22:23], off offset:1280 nt
	global_load_dword v55, v[22:23], off offset:1536 nt
	global_load_dword v56, v[22:23], off offset:1792 nt
	s_or_b32 s20, s15, 4
	s_mul_hi_u32 s21, s16, s20
	s_add_i32 s21, s21, s22
	s_mul_i32 s23, s17, s20
	s_add_i32 s21, s21, s23
	s_mul_i32 s20, s16, s20
	v_lshl_add_u64 v[22:23], s[20:21], 2, v[20:21]
	s_or_b32 s15, s15, 6
	v_lshl_add_u64 v[24:25], v[22:23], 0, s[18:19]
	global_load_dword v57, v[22:23], off nt
	global_load_dword v58, v[22:23], off offset:256 nt
	global_load_dword v59, v[22:23], off offset:512 nt
	global_load_dword v60, v[22:23], off offset:768 nt
	global_load_dword v61, v[22:23], off offset:1024 nt
	global_load_dword v62, v[22:23], off offset:1280 nt
	global_load_dword v63, v[22:23], off offset:1536 nt
	global_load_dword v66, v[22:23], off offset:1792 nt
	global_load_dword v67, v[24:25], off nt
	global_load_dword v68, v[24:25], off offset:256 nt
	global_load_dword v69, v[24:25], off offset:512 nt
	global_load_dword v70, v[24:25], off offset:768 nt
	global_load_dword v71, v[24:25], off offset:1024 nt
	global_load_dword v72, v[24:25], off offset:1280 nt
	global_load_dword v73, v[24:25], off offset:1536 nt
	global_load_dword v74, v[24:25], off offset:1792 nt
	s_mul_hi_u32 s20, s16, s15
	s_add_i32 s20, s20, s22
	s_mul_i32 s17, s17, s15
	s_add_i32 s17, s20, s17
	s_mul_i32 s16, s16, s15
	v_lshl_add_u64 v[20:21], s[16:17], 2, v[20:21]
	v_lshl_add_u64 v[22:23], v[20:21], 0, s[18:19]
	global_load_dword v25, v[20:21], off nt
	global_load_dword v75, v[20:21], off offset:256 nt
	global_load_dword v76, v[20:21], off offset:512 nt
	global_load_dword v77, v[20:21], off offset:768 nt
	global_load_dword v78, v[20:21], off offset:1024 nt
	global_load_dword v79, v[20:21], off offset:1280 nt
	global_load_dword v80, v[20:21], off offset:1536 nt
	global_load_dword v81, v[20:21], off offset:1792 nt
	global_load_dword v82, v[22:23], off nt
	global_load_dword v83, v[22:23], off offset:256 nt
	global_load_dword v84, v[22:23], off offset:512 nt
	global_load_dword v85, v[22:23], off offset:768 nt
	global_load_dword v86, v[22:23], off offset:1024 nt
	global_load_dword v87, v[22:23], off offset:1280 nt
	global_load_dword v88, v[22:23], off offset:1536 nt
	global_load_dword v89, v[22:23], off offset:1792 nt
	v_mov_b32_e32 v24, v65
	s_ashr_i32 s15, s14, 31
	s_lshl_b64 s[16:17], s[14:15], 20
	v_readlane_b32 s18, v255, 30
	s_add_u32 s16, s18, s16
	v_readlane_b32 s18, v255, 31
	s_addc_u32 s17, s18, s17
	s_lshl_b64 s[14:15], s[14:15], 19
	v_readlane_b32 s18, v255, 32
	s_add_u32 s18, s18, s14
	v_readlane_b32 s14, v255, 33
	s_addc_u32 s19, s14, s15
	s_and_b64 s[14:15], s[12:13], exec
	s_cselect_b32 s14, s18, s16
	s_waitcnt vmcnt(63) expcnt(7) lgkmcnt(15)
	s_barrier
	s_movk_i32 s20, 0xff00
	s_cselect_b32 s15, s19, s17
	s_add_u32 s14, s14, s29
	s_addc_u32 s15, s15, 0
	s_waitcnt vmcnt(52)
	v_mul_f32_e32 v23, 0x42000000, v38
	v_mul_f32_e32 v21, 0x42000000, v28
	v_mul_f32_e32 v20, 0x42000000, v29
	v_mul_f32_e32 v19, 0x42000000, v19
	v_med3_f32 v22, v20, s55, v228
	v_med3_f32 v19, v19, s55, v228
	v_mov_b32_e32 v20, v65
	v_cvt_pk_fp8_f32 v20, v22, v19
	v_mul_f32_e32 v19, 0x42000000, v37
	v_med3_f32 v21, v21, s55, v228
	v_med3_f32 v19, v19, s55, v228
	v_cvt_pk_fp8_f32 v20, v21, v19 op_sel:[0,0,1]
	v_mul_f32_e32 v19, 0x42000000, v30
	s_waitcnt vmcnt(51)
	v_mul_f32_e32 v21, 0x42000000, v39
	v_med3_f32 v19, v19, s55, v228
	v_med3_f32 v21, v21, s55, v228
	v_mov_b32_e32 v22, v65
	v_cvt_pk_fp8_f32 v22, v19, v21
	s_waitcnt vmcnt(44)
	v_mul_f32_e32 v19, 0x42000000, v46
	v_med3_f32 v21, v23, s55, v228
	v_med3_f32 v19, v19, s55, v228
	v_cvt_pk_fp8_f32 v22, v21, v19 op_sel:[0,0,1]
	v_mul_f32_e32 v19, 0x42000000, v31
	v_mul_f32_e32 v21, 0x42000000, v40
	v_med3_f32 v19, v19, s55, v228
	v_med3_f32 v21, v21, s55, v228
	v_cvt_pk_fp8_f32 v24, v19, v21
	s_waitcnt vmcnt(43)
	v_mul_f32_e32 v23, 0x42000000, v47
	s_waitcnt vmcnt(37)
	v_mul_f32_e32 v19, 0x42000000, v26
	v_med3_f32 v21, v23, s55, v228
	v_med3_f32 v19, v19, s55, v228
	v_cvt_pk_fp8_f32 v24, v21, v19 op_sel:[0,0,1]
	v_mul_f32_e32 v19, 0x42000000, v32
	v_mul_f32_e32 v21, 0x42000000, v41
	v_med3_f32 v19, v19, s55, v228
	v_med3_f32 v21, v21, s55, v228
	v_mov_b32_e32 v26, v65
	v_cvt_pk_fp8_f32 v26, v19, v21
	v_mul_f32_e32 v23, 0x42000000, v48
	s_waitcnt vmcnt(36)
	v_mul_f32_e32 v19, 0x42000000, v52
	v_med3_f32 v21, v23, s55, v228
	v_med3_f32 v19, v19, s55, v228
	v_cvt_pk_fp8_f32 v26, v21, v19 op_sel:[0,0,1]
	v_mul_f32_e32 v19, 0x42000000, v33
	v_mul_f32_e32 v21, 0x42000000, v42
	v_med3_f32 v19, v19, s55, v228
	v_med3_f32 v21, v21, s55, v228
	v_mov_b32_e32 v28, v65
	v_cvt_pk_fp8_f32 v28, v19, v21
	v_mul_f32_e32 v23, 0x42000000, v49
	s_waitcnt vmcnt(35)
	v_mul_f32_e32 v19, 0x42000000, v53
	v_med3_f32 v21, v23, s55, v228
	v_med3_f32 v19, v19, s55, v228
	v_cvt_pk_fp8_f32 v28, v21, v19 op_sel:[0,0,1]
	v_mul_f32_e32 v19, 0x42000000, v34
	v_mul_f32_e32 v21, 0x42000000, v43
	v_med3_f32 v19, v19, s55, v228
	v_med3_f32 v21, v21, s55, v228
	v_mov_b32_e32 v30, v65
	v_cvt_pk_fp8_f32 v30, v19, v21
	v_mul_f32_e32 v23, 0x42000000, v50
	s_waitcnt vmcnt(34)
	v_mul_f32_e32 v19, 0x42000000, v54
	v_med3_f32 v21, v23, s55, v228
	v_med3_f32 v19, v19, s55, v228
	v_cvt_pk_fp8_f32 v30, v21, v19 op_sel:[0,0,1]
	v_mul_f32_e32 v19, 0x42000000, v35
	v_mul_f32_e32 v21, 0x42000000, v44
	v_med3_f32 v19, v19, s55, v228
	v_med3_f32 v21, v21, s55, v228
	v_mov_b32_e32 v32, v65
	v_cvt_pk_fp8_f32 v32, v19, v21
	v_mul_f32_e32 v23, 0x42000000, v51
	s_waitcnt vmcnt(33)
	v_mul_f32_e32 v19, 0x42000000, v55
	v_med3_f32 v21, v23, s55, v228
	v_med3_f32 v19, v19, s55, v228
	v_cvt_pk_fp8_f32 v32, v21, v19 op_sel:[0,0,1]
	v_mul_f32_e32 v19, 0x42000000, v36
	v_mul_f32_e32 v21, 0x42000000, v45
	v_med3_f32 v19, v19, s55, v228
	v_med3_f32 v21, v21, s55, v228
	v_mov_b32_e32 v34, v65
	v_cvt_pk_fp8_f32 v34, v19, v21
	v_mul_f32_e32 v23, 0x42000000, v27
	s_waitcnt vmcnt(32)
	v_mul_f32_e32 v19, 0x42000000, v56
	v_med3_f32 v21, v23, s55, v228
	v_med3_f32 v19, v19, s55, v228
	v_cvt_pk_fp8_f32 v34, v21, v19 op_sel:[0,0,1]
	s_waitcnt vmcnt(31)
	v_mul_f32_e32 v19, 0x42000000, v57
	s_waitcnt vmcnt(23)
	v_mul_f32_e32 v21, 0x42000000, v67
	s_waitcnt vmcnt(15)
	v_mul_f32_e32 v23, 0x42000000, v25
	v_med3_f32 v19, v19, s55, v228
	v_med3_f32 v25, v21, s55, v228
	v_mov_b32_e32 v21, v65
	v_cvt_pk_fp8_f32 v21, v19, v25
	s_waitcnt vmcnt(7)
	v_mul_f32_e32 v19, 0x42000000, v82
	v_med3_f32 v23, v23, s55, v228
	v_med3_f32 v19, v19, s55, v228
	v_cvt_pk_fp8_f32 v21, v23, v19 op_sel:[0,0,1]
	v_mul_f32_e32 v19, 0x42000000, v58
	v_mul_f32_e32 v23, 0x42000000, v68
	v_med3_f32 v19, v19, s55, v228
	v_med3_f32 v27, v23, s55, v228
	v_mov_b32_e32 v23, v65
	v_cvt_pk_fp8_f32 v23, v19, v27
	v_mul_f32_e32 v25, 0x42000000, v75
	s_waitcnt vmcnt(6)
	v_mul_f32_e32 v19, 0x42000000, v83
	v_med3_f32 v25, v25, s55, v228
	v_med3_f32 v19, v19, s55, v228
	v_cvt_pk_fp8_f32 v23, v25, v19 op_sel:[0,0,1]
	v_mul_f32_e32 v19, 0x42000000, v59
	v_mul_f32_e32 v25, 0x42000000, v69
	v_med3_f32 v19, v19, s55, v228
	v_med3_f32 v29, v25, s55, v228
	v_mov_b32_e32 v25, v65
	v_cvt_pk_fp8_f32 v25, v19, v29
	v_mul_f32_e32 v27, 0x42000000, v76
	s_waitcnt vmcnt(5)
	v_mul_f32_e32 v19, 0x42000000, v84
	v_med3_f32 v27, v27, s55, v228
	v_med3_f32 v19, v19, s55, v228
	v_cvt_pk_fp8_f32 v25, v27, v19 op_sel:[0,0,1]
	v_mul_f32_e32 v19, 0x42000000, v60
	v_mul_f32_e32 v27, 0x42000000, v70
	v_med3_f32 v19, v19, s55, v228
	v_med3_f32 v31, v27, s55, v228
	v_mov_b32_e32 v27, v65
	v_cvt_pk_fp8_f32 v27, v19, v31
	v_mul_f32_e32 v29, 0x42000000, v77
	s_waitcnt vmcnt(4)
	v_mul_f32_e32 v19, 0x42000000, v85
	v_med3_f32 v29, v29, s55, v228
	v_med3_f32 v19, v19, s55, v228
	v_cvt_pk_fp8_f32 v27, v29, v19 op_sel:[0,0,1]
	v_mul_f32_e32 v19, 0x42000000, v61
	v_mul_f32_e32 v29, 0x42000000, v71
	v_med3_f32 v19, v19, s55, v228
	v_med3_f32 v33, v29, s55, v228
	v_mov_b32_e32 v29, v65
	v_cvt_pk_fp8_f32 v29, v19, v33
	v_mul_f32_e32 v31, 0x42000000, v78
	s_waitcnt vmcnt(3)
	v_mul_f32_e32 v19, 0x42000000, v86
	v_med3_f32 v31, v31, s55, v228
	v_med3_f32 v19, v19, s55, v228
	v_cvt_pk_fp8_f32 v29, v31, v19 op_sel:[0,0,1]
	v_mul_f32_e32 v19, 0x42000000, v62
	v_mul_f32_e32 v31, 0x42000000, v72
	v_med3_f32 v19, v19, s55, v228
	v_med3_f32 v35, v31, s55, v228
	v_mov_b32_e32 v31, v65
	v_cvt_pk_fp8_f32 v31, v19, v35
	v_mul_f32_e32 v33, 0x42000000, v79
	s_waitcnt vmcnt(2)
	v_mul_f32_e32 v19, 0x42000000, v87
	v_med3_f32 v33, v33, s55, v228
	v_med3_f32 v19, v19, s55, v228
	v_cvt_pk_fp8_f32 v31, v33, v19 op_sel:[0,0,1]
	v_mul_f32_e32 v19, 0x42000000, v63
	v_mul_f32_e32 v33, 0x42000000, v73
	v_med3_f32 v19, v19, s55, v228
	v_med3_f32 v36, v33, s55, v228
	v_mov_b32_e32 v33, v65
	v_cvt_pk_fp8_f32 v33, v19, v36
	v_mul_f32_e32 v35, 0x42000000, v80
	s_waitcnt vmcnt(1)
	v_mul_f32_e32 v19, 0x42000000, v88
	v_med3_f32 v35, v35, s55, v228
	v_med3_f32 v19, v19, s55, v228
	v_cvt_pk_fp8_f32 v33, v35, v19 op_sel:[0,0,1]
	v_mul_f32_e32 v19, 0x42000000, v66
	v_mul_f32_e32 v35, 0x42000000, v74
	v_med3_f32 v19, v19, s55, v228
	v_med3_f32 v37, v35, s55, v228
	v_mov_b32_e32 v35, v65
	v_cvt_pk_fp8_f32 v35, v19, v37
	v_mul_f32_e32 v36, 0x42000000, v81
	s_waitcnt vmcnt(0)
	v_mul_f32_e32 v19, 0x42000000, v89
	v_med3_f32 v36, v36, s55, v228
	v_med3_f32 v19, v19, s55, v228
	v_cvt_pk_fp8_f32 v35, v36, v19 op_sel:[0,0,1]
	ds_write2st64_b64 v14, v[20:21], v[22:23] offset1:9
	ds_write2st64_b64 v14, v[24:25], v[26:27] offset0:18 offset1:27
	ds_write2st64_b64 v14, v[28:29], v[30:31] offset0:36 offset1:45
	ds_write2st64_b64 v14, v[32:33], v[34:35] offset0:54 offset1:63
	v_add_u32_e32 v24, s66, v2
	s_waitcnt lgkmcnt(0)
	s_barrier
	ds_read2_b64 v[20:23], v15 offset1:1
	v_or_b32_e32 v19, s28, v3
	v_and_or_b32 v24, v24, s20, v4
	v_cndmask_b32_e64 v24, v19, v24, s[12:13]
	v_lshl_add_u64 v[28:29], s[14:15], 0, v[64:65]
	s_and_b64 s[14:15], s[12:13], exec
	v_ashrrev_i32_e32 v25, 31, v24
	s_cselect_b32 s14, 9, 10
	v_lshlrev_b64 v[24:25], s14, v[24:25]
	v_lshl_add_u64 v[30:31], v[28:29], 0, v[24:25]
	v_add_u32_e32 v19, s66, v5
	ds_read2_b64 v[24:27], v16 offset1:1
	s_waitcnt lgkmcnt(1)
	global_store_dwordx4 v[30:31], v[20:23], off sc1 nt
	v_and_or_b32 v19, v19, s20, v7
	s_add_i32 s27, s27, s44
	v_or_b32_e32 v20, s28, v6
	v_cndmask_b32_e64 v20, v20, v19, s[12:13]
	v_ashrrev_i32_e32 v21, 31, v20
	v_lshlrev_b64 v[20:21], s14, v[20:21]
	v_lshl_add_u64 v[20:21], v[28:29], 0, v[20:21]
	v_add_u32_e32 v19, s66, v8
	s_waitcnt lgkmcnt(0)
	global_store_dwordx4 v[20:21], v[24:27], off sc1 nt
	ds_read2_b64 v[20:23], v17 offset1:1
	v_and_or_b32 v19, v19, s20, v10
	v_or_b32_e32 v24, s28, v9
	v_cndmask_b32_e64 v24, v24, v19, s[12:13]
	v_ashrrev_i32_e32 v25, 31, v24
	v_lshlrev_b64 v[24:25], s14, v[24:25]
	v_lshl_add_u64 v[30:31], v[28:29], 0, v[24:25]
	v_add_u32_e32 v19, s66, v11
	ds_read2_b64 v[24:27], v18 offset1:1
	s_waitcnt lgkmcnt(1)
	global_store_dwordx4 v[30:31], v[20:23], off sc1 nt
	v_and_or_b32 v19, v19, s20, v13
	s_add_i32 s26, s26, s24
	v_or_b32_e32 v20, s28, v12
	v_cndmask_b32_e64 v20, v20, v19, s[12:13]
	v_ashrrev_i32_e32 v21, 31, v20
	v_lshlrev_b64 v[20:21], s14, v[20:21]
	s_add_i32 s25, s25, s63
	v_lshl_add_u64 v[20:21], v[28:29], 0, v[20:21]
	s_cmpk_lt_i32 s27, 0x600
	s_waitcnt lgkmcnt(0)
	global_store_dwordx4 v[20:21], v[24:27], off sc1 nt
	s_cbranch_scc0 .LBB0_181

.LBB0_414:
	v_add3_u32 v64, s23, v173, v171
	ds_read_b64_tr_b16 v[90:91], v64 offset:36864
	s_nop 1
	ds_read_b64_tr_b16 v[86:87], v64 offset:36896
	ds_read_b64_tr_b16 v[100:101], v64 offset:36928
	ds_read_b64_tr_b16 v[108:109], v64 offset:36960
	ds_read_b64_tr_b16 v[92:93], v64 offset:39168
	ds_read_b64_tr_b16 v[88:89], v64 offset:39200
	ds_read_b64_tr_b16 v[102:103], v64 offset:39232
	ds_read_b64_tr_b16 v[110:111], v64 offset:39264
	ds_read_b64_tr_b16 v[104:105], v64 offset:41472
	ds_read_b64_tr_b16 v[112:113], v64 offset:41504
	ds_read_b64_tr_b16 v[118:119], v64 offset:41536
	ds_read_b64_tr_b16 v[126:127], v64 offset:41568
	ds_read_b64_tr_b16 v[106:107], v64 offset:43776
	ds_read_b64_tr_b16 v[114:115], v64 offset:43808
	ds_read_b64_tr_b16 v[120:121], v64 offset:43840
	ds_read_b64_tr_b16 v[128:129], v64 offset:43872
	ds_read_b64_tr_b16 v[122:123], v64 offset:46080
	ds_read_b64_tr_b16 v[130:131], v64 offset:46112
	ds_read_b64_tr_b16 v[138:139], v64 offset:46144
	ds_read_b64_tr_b16 v[146:147], v64 offset:46176
	ds_read_b64_tr_b16 v[124:125], v64 offset:48384
	ds_read_b64_tr_b16 v[132:133], v64 offset:48416
	ds_read_b64_tr_b16 v[140:141], v64 offset:48448
	ds_read_b64_tr_b16 v[148:149], v64 offset:48480
	ds_read_b64_tr_b16 v[142:143], v64 offset:50688
	ds_read_b64_tr_b16 v[152:153], v64 offset:50720
	ds_read_b64_tr_b16 v[156:157], v64 offset:50752
	ds_read_b64_tr_b16 v[134:135], v64 offset:50784
	ds_read_b64_tr_b16 v[144:145], v64 offset:52992
	ds_read_b64_tr_b16 v[154:155], v64 offset:53024
	ds_read_b64_tr_b16 v[158:159], v64 offset:53056
	ds_read_b64_tr_b16 v[136:137], v64 offset:53088
	ds_read_b64_tr_b16 v[150:151], v64 offset:55296
	ds_read_b64_tr_b16 v[116:117], v64 offset:55328
	ds_read_b64_tr_b16 v[98:99], v64 offset:55360
	ds_read_b64_tr_b16 v[94:95], v64 offset:55392
	v_max3_f32 v64, v82, s84, v83
	v_max3_f32 v64, v64, v84, v85
	v_max3_f32 v64, v64, v78, v79
	v_max3_f32 v64, v64, v80, v81
	v_max3_f32 v64, v64, v74, v75
	v_max3_f32 v64, v64, v76, v77
	v_max3_f32 v64, v64, v70, v71
	v_max3_f32 v64, v64, v72, v73
	v_max3_f32 v64, v64, v66, v67
	v_max3_f32 v64, v64, v68, v69
	v_max3_f32 v64, v64, v60, v61
	v_max3_f32 v64, v64, v62, v63
	v_max3_f32 v64, v64, v56, v57
	v_max3_f32 v64, v64, v58, v59
	v_max3_f32 v64, v64, v52, v53
	v_max3_f32 v64, v64, v54, v55
	v_max3_f32 v64, v64, v48, v49
	v_max3_f32 v64, v64, v50, v51
	v_mov_b32_e32 v96, v64
	s_nop 1
	v_permlane16_swap_b32_e32 v64, v96
	v_max_f32_e32 v96, v96, v96
	v_max_f32_e32 v64, v64, v64
	v_max_f32_e32 v64, v64, v96
	v_mov_b32_e32 v96, v64
	s_nop 1
	v_permlane32_swap_b32_e32 v64, v96
	v_max_f32_e32 v96, v96, v96
	v_max_f32_e32 v64, v64, v64
	v_max_f32_e32 v170, v64, v96
	v_pk_add_f32 v[82:83], v[82:83], v[170:171] op_sel_hi:[1,0] neg_lo:[0,1] neg_hi:[0,1]
	v_pk_add_f32 v[84:85], v[84:85], v[170:171] op_sel_hi:[1,0] neg_lo:[0,1] neg_hi:[0,1]
	v_exp_f32_e32 v82, v82
	v_exp_f32_e32 v83, v83
	v_exp_f32_e32 v84, v84
	v_exp_f32_e32 v85, v85
	v_pk_add_f32 v[78:79], v[78:79], v[170:171] op_sel_hi:[1,0] neg_lo:[0,1] neg_hi:[0,1]
	v_pk_add_f32 v[80:81], v[80:81], v[170:171] op_sel_hi:[1,0] neg_lo:[0,1] neg_hi:[0,1]
	v_exp_f32_e32 v78, v78
	v_exp_f32_e32 v79, v79
	v_exp_f32_e32 v80, v80
	v_exp_f32_e32 v81, v81
	v_pk_add_f32 v[74:75], v[74:75], v[170:171] op_sel_hi:[1,0] neg_lo:[0,1] neg_hi:[0,1]
	v_pk_add_f32 v[96:97], v[82:83], 0 op_sel_hi:[1,0]
	v_pk_add_f32 v[76:77], v[76:77], v[170:171] op_sel_hi:[1,0] neg_lo:[0,1] neg_hi:[0,1]
	v_exp_f32_e32 v192, v74
	v_exp_f32_e32 v193, v75
	v_pk_add_f32 v[96:97], v[84:85], v[96:97]
	v_exp_f32_e32 v194, v76
	v_exp_f32_e32 v195, v77
	v_pk_add_f32 v[70:71], v[70:71], v[170:171] op_sel_hi:[1,0] neg_lo:[0,1] neg_hi:[0,1]
	v_pk_add_f32 v[74:75], v[78:79], v[96:97]
	v_pk_add_f32 v[72:73], v[72:73], v[170:171] op_sel_hi:[1,0] neg_lo:[0,1] neg_hi:[0,1]
	v_exp_f32_e32 v96, v70
	v_exp_f32_e32 v97, v71
	v_pk_add_f32 v[74:75], v[80:81], v[74:75]
	v_exp_f32_e32 v196, v72
	v_exp_f32_e32 v197, v73
	v_pk_add_f32 v[66:67], v[66:67], v[170:171] op_sel_hi:[1,0] neg_lo:[0,1] neg_hi:[0,1]
	v_pk_add_f32 v[74:75], v[192:193], v[74:75]
	v_pk_add_f32 v[68:69], v[68:69], v[170:171] op_sel_hi:[1,0] neg_lo:[0,1] neg_hi:[0,1]
	v_exp_f32_e32 v198, v66
	v_exp_f32_e32 v199, v67
	v_pk_add_f32 v[74:75], v[194:195], v[74:75]
	v_exp_f32_e32 v200, v68
	v_exp_f32_e32 v201, v69
	v_pk_add_f32 v[66:67], v[96:97], v[74:75]
	v_cvt_pk_bf16_f32 v68, v78, v79
	v_pk_add_f32 v[66:67], v[196:197], v[66:67]
	v_cvt_pk_bf16_f32 v69, v80, v81
	v_pk_add_f32 v[66:67], v[198:199], v[66:67]
	v_pk_add_f32 v[74:75], v[60:61], v[170:171] op_sel_hi:[1,0] neg_lo:[0,1] neg_hi:[0,1]
	v_pk_add_f32 v[202:203], v[200:201], v[66:67]
	v_cvt_pk_bf16_f32 v66, v82, v83
	v_cvt_pk_bf16_f32 v67, v84, v85
	v_pk_add_f32 v[76:77], v[62:63], v[170:171] op_sel_hi:[1,0] neg_lo:[0,1] neg_hi:[0,1]
	v_exp_f32_e32 v78, v74
	s_waitcnt lgkmcnt(14)
	v_mfma_f32_16x16x32_bf16 v[70:73], v[90:93], v[66:69], 0
	v_exp_f32_e32 v79, v75
	v_exp_f32_e32 v80, v76
	v_exp_f32_e32 v81, v77
	v_mfma_f32_16x16x32_bf16 v[60:63], v[86:89], v[66:69], 0
	v_add_f32_e64 v84, v56, -v170
	v_add_f32_e64 v85, v57, -v170
	v_pk_add_f32 v[86:87], v[58:59], v[170:171] op_sel_hi:[1,0] neg_lo:[0,1] neg_hi:[0,1]
	v_exp_f32_e32 v84, v84
	v_mfma_f32_16x16x32_bf16 v[74:77], v[100:103], v[66:69], 0
	v_exp_f32_e32 v85, v85
	v_exp_f32_e32 v86, v86
	v_exp_f32_e32 v87, v87
	v_mfma_f32_16x16x32_bf16 v[56:59], v[108:111], v[66:69], 0
	v_cvt_pk_bf16_f32 v66, v192, v193
	v_cvt_pk_bf16_f32 v67, v194, v195
	v_cvt_pk_bf16_f32 v68, v96, v97
	v_cvt_pk_bf16_f32 v69, v196, v197
	v_pk_add_f32 v[88:89], v[52:53], v[170:171] op_sel_hi:[1,0] neg_lo:[0,1] neg_hi:[0,1]
	v_pk_add_f32 v[82:83], v[78:79], v[202:203]
	v_mfma_f32_16x16x32_bf16 v[70:73], v[104:107], v[66:69], v[70:73]
	v_add_f32_e64 v90, v54, -v170
	v_add_f32_e64 v91, v55, -v170
	v_pk_add_f32 v[82:83], v[80:81], v[82:83]
	v_pk_add_f32 v[48:49], v[48:49], v[170:171] op_sel_hi:[1,0] neg_lo:[0,1] neg_hi:[0,1]
	v_mfma_f32_16x16x32_bf16 v[60:63], v[112:115], v[66:69], v[60:63]
	v_add_f32_e64 v82, v84, v82
	v_add_f32_e64 v83, v85, v83
	s_waitcnt lgkmcnt(1)
	v_mov_b32_e32 v100, v98
	v_pk_add_f32 v[82:83], v[86:87], v[82:83]
	v_mfma_f32_16x16x32_bf16 v[74:77], v[118:121], v[66:69], v[74:77]
	v_mov_b32_e32 v118, v116
	v_mov_b32_e32 v119, v117
	v_mov_b32_e32 v101, v99
	v_mfma_f32_16x16x32_bf16 v[52:55], v[126:129], v[66:69], v[56:59]
	s_waitcnt lgkmcnt(0)
	v_mov_b32_e32 v96, v94
	v_mov_b32_e32 v97, v95
	v_mov_b32_e32 v64, v65
	v_cvt_pk_bf16_f32 v58, v78, v79
	v_exp_f32_e32 v78, v88
	v_exp_f32_e32 v79, v89
	v_cvt_pk_bf16_f32 v56, v198, v199
	v_cvt_pk_bf16_f32 v57, v200, v201
	v_cvt_pk_bf16_f32 v59, v80, v81
	v_exp_f32_e32 v80, v90
	v_exp_f32_e32 v81, v91
	v_mfma_f32_16x16x32_bf16 v[66:69], v[122:125], v[56:59], v[70:73]
	v_add_f32_e64 v82, v78, v82
	v_add_f32_e64 v83, v79, v83
	s_cmp_eq_u32 s30, 1
	s_mov_b32 s23, 0xe800000
	v_mfma_f32_16x16x32_bf16 v[60:63], v[130:133], v[56:59], v[60:63]
	s_cselect_b32 s23, s23, 0x2e800000
	s_cmp_lg_u32 s30, 0
	s_cselect_b32 s23, s23, 0x12800000
	v_mfma_f32_16x16x32_bf16 v[70:73], v[138:141], v[56:59], v[74:77]
	s_add_u32 s36, s42, s23
	s_addc_u32 s37, s43, 0
	s_lshl_b32 s66, s22, 6
	v_pk_add_f32 v[74:75], v[50:51], v[170:171] op_sel_hi:[1,0] neg_lo:[0,1] neg_hi:[0,1]
	v_exp_f32_e32 v76, v48
	v_exp_f32_e32 v77, v49
	v_exp_f32_e32 v74, v74
	v_exp_f32_e32 v75, v75
	v_mfma_f32_16x16x32_bf16 v[48:51], v[146:149], v[56:59], v[52:55]
	s_nop 2
	v_cvt_pk_bf16_f32 v52, v84, v85
	v_cvt_pk_bf16_f32 v53, v86, v87
	v_cvt_pk_bf16_f32 v54, v78, v79
	v_cvt_pk_bf16_f32 v55, v80, v81
	v_pk_add_f32 v[78:79], v[80:81], v[82:83]
	s_nop 0
	v_mfma_f32_16x16x32_bf16 v[56:59], v[142:145], v[52:55], v[66:69]
	v_mfma_f32_16x16x32_bf16 v[66:69], v[152:155], v[52:55], v[60:63]
	v_mov_b32_e32 v152, v150
	v_mov_b32_e32 v153, v151
	s_nop 0
	v_pk_add_f32 v[60:61], v[76:77], v[78:79]
	v_mfma_f32_16x16x32_bf16 v[70:73], v[156:159], v[52:55], v[70:73]
	v_add_f32_e64 v60, v74, v60
	v_add_f32_e64 v61, v75, v61
	v_cvt_pk_bf16_f32 v62, v76, v77
	v_pk_add_f32 v[60:61], v[60:61], v[60:61] op_sel:[0,1] op_sel_hi:[1,0]
	v_mfma_f32_16x16x32_bf16 v[48:51], v[134:137], v[52:55], v[48:51]
	v_mov_b32_e32 v61, v60
	s_nop 1
	v_permlane16_swap_b32_e32 v60, v61
	v_cvt_pk_bf16_f32 v63, v74, v75
	v_add_f32_e32 v74, v60, v61
	s_nop 0
	v_mfma_f32_16x16x32_bf16 v[52:55], v[150:153], v[62:65], v[56:59]
	v_mfma_f32_16x16x32_bf16 v[56:59], v[116:119], v[62:65], v[66:69]
	v_mfma_f32_16x16x32_bf16 v[66:69], v[98:101], v[62:65], v[70:73]
	s_nop 2
	v_mov_b32_e32 v70, v74
	s_nop 1
	v_permlane32_swap_b32_e32 v74, v70
	v_mfma_f32_16x16x32_bf16 v[60:63], v[94:97], v[62:65], v[48:51]
	s_nop 2
	v_add_f32_e32 v48, v74, v70
	v_rcp_f32_e32 v49, v48
	s_nop 0
	v_mul_f32_e32 v49, 0x42800000, v49
	v_mul_f32_e32 v50, v49, v52
	v_mul_f32_e32 v51, v49, v53
	v_med3_f32 v53, v50, s55, v228
	v_med3_f32 v51, v51, s55, v228
	v_mov_b32_e32 v50, v65
	v_cvt_pk_fp8_f32 v50, v53, v51
	v_mul_f32_e32 v52, v49, v54
	v_mul_f32_e32 v51, v49, v55
	v_med3_f32 v52, v52, s55, v228
	v_med3_f32 v51, v51, s55, v228
	v_cvt_pk_fp8_f32 v50, v52, v51 op_sel:[0,0,1]
	v_mul_f32_e32 v51, v49, v56
	v_mul_f32_e32 v52, v49, v57
	v_med3_f32 v54, v51, s55, v228
	v_med3_f32 v52, v52, s55, v228
	v_mov_b32_e32 v51, v65
	v_cvt_pk_fp8_f32 v51, v54, v52
	v_mul_f32_e32 v53, v49, v58
	v_mul_f32_e32 v52, v49, v59
	v_med3_f32 v53, v53, s55, v228
	v_med3_f32 v52, v52, s55, v228
	v_cvt_pk_fp8_f32 v51, v53, v52 op_sel:[0,0,1]
	v_mul_f32_e32 v52, v49, v66
	v_mul_f32_e32 v53, v49, v67
	v_med3_f32 v55, v52, s55, v228
	v_med3_f32 v53, v53, s55, v228
	v_mov_b32_e32 v52, v65
	v_cvt_pk_fp8_f32 v52, v55, v53
	v_mul_f32_e32 v54, v49, v68
	v_mul_f32_e32 v53, v49, v69
	v_med3_f32 v54, v54, s55, v228
	v_med3_f32 v53, v53, s55, v228
	v_cvt_pk_fp8_f32 v52, v54, v53 op_sel:[0,0,1]
	v_mul_f32_e32 v53, v49, v60
	v_mul_f32_e32 v54, v49, v61
	v_med3_f32 v56, v53, s55, v228
	v_med3_f32 v54, v54, s55, v228
	v_mov_b32_e32 v53, v65
	v_cvt_pk_fp8_f32 v53, v56, v54
	v_mul_f32_e32 v55, v49, v62
	v_mul_f32_e32 v49, v49, v63
	v_med3_f32 v54, v55, s55, v228
	v_med3_f32 v49, v49, s55, v228
	v_cvt_pk_fp8_f32 v53, v54, v49 op_sel:[0,0,1]
	v_lshlrev_b64 v[54:55], 10, v[166:167]
	v_lshl_add_u64 v[54:55], s[36:37], 0, v[54:55]
	v_lshl_add_u64 v[54:55], v[54:55], 0, s[66:67]
	v_lshl_add_u64 v[54:55], v[54:55], 0, v[160:161]
	global_store_dwordx4 v[54:55], v[50:53], off sc1 nt
	s_and_saveexec_b64 s[36:37], vcc
	s_cbranch_execz .LBB0_416
	v_log_f32_e32 v48, v48
	s_ashr_i32 s31, s30, 31
	s_lshl_b64 s[30:31], s[30:31], 22
	v_readlane_b32 s23, v254, 30
	s_add_u32 s30, s23, s30
	v_readlane_b32 s23, v254, 31
	v_add_f32_e32 v48, v170, v48
	s_addc_u32 s31, s23, s31
	v_mul_f32_e32 v50, 0x3f317218, v48
	v_lshlrev_b64 v[48:49], 6, v[166:167]
	v_lshl_add_u64 v[48:49], s[30:31], 0, v[48:49]
	s_mov_b32 s23, s67
	v_lshl_add_u64 v[48:49], s[22:23], 2, v[48:49]
	global_store_dword v[48:49], v50, off

.LBB0_420:
	v_readlane_b32 s6, v255, 3
	s_mov_b32 s63, s71
	s_nop 0
	v_add3_u32 v10, s6, v173, v171
	v_add3_u32 v12, s6, v171, v173
	ds_read_b64_tr_b16 v[44:45], v10
	ds_read_b64_tr_b16 v[8:9], v10 offset:32
	ds_read_b64_tr_b16 v[50:51], v10 offset:64
	ds_read_b64_tr_b16 v[58:59], v10 offset:96
	ds_read_b64_tr_b16 v[46:47], v12 offset:2304
	ds_read_b64_tr_b16 v[10:11], v12 offset:2336
	ds_read_b64_tr_b16 v[52:53], v12 offset:2368
	ds_read_b64_tr_b16 v[60:61], v12 offset:2400
	ds_read_b64_tr_b16 v[54:55], v12 offset:4608
	ds_read_b64_tr_b16 v[66:67], v12 offset:4640
	ds_read_b64_tr_b16 v[70:71], v12 offset:4672
	ds_read_b64_tr_b16 v[78:79], v12 offset:4704
	ds_read_b64_tr_b16 v[56:57], v12 offset:6912
	ds_read_b64_tr_b16 v[68:69], v12 offset:6944
	ds_read_b64_tr_b16 v[72:73], v12 offset:6976
	ds_read_b64_tr_b16 v[80:81], v12 offset:7008
	ds_read_b64_tr_b16 v[74:75], v12 offset:9216
	ds_read_b64_tr_b16 v[82:83], v12 offset:9248
	ds_read_b64_tr_b16 v[90:91], v12 offset:9280
	ds_read_b64_tr_b16 v[98:99], v12 offset:9312
	ds_read_b64_tr_b16 v[76:77], v12 offset:11520
	ds_read_b64_tr_b16 v[84:85], v12 offset:11552
	ds_read_b64_tr_b16 v[92:93], v12 offset:11584
	ds_read_b64_tr_b16 v[100:101], v12 offset:11616
	ds_read_b64_tr_b16 v[94:95], v12 offset:13824
	ds_read_b64_tr_b16 v[104:105], v12 offset:13856
	ds_read_b64_tr_b16 v[108:109], v12 offset:13888
	ds_read_b64_tr_b16 v[86:87], v12 offset:13920
	ds_read_b64_tr_b16 v[96:97], v12 offset:16128
	ds_read_b64_tr_b16 v[106:107], v12 offset:16160
	ds_read_b64_tr_b16 v[110:111], v12 offset:16192
	ds_read_b64_tr_b16 v[88:89], v12 offset:16224
	ds_read_b64_tr_b16 v[102:103], v12 offset:18432
	ds_read_b64_tr_b16 v[14:15], v12 offset:18464
	ds_read_b64_tr_b16 v[48:49], v12 offset:18496
	ds_read_b64_tr_b16 v[12:13], v12 offset:18528
	v_max3_f32 v62, v40, s84, v41
	v_max3_f32 v62, v62, v42, v43
	v_max3_f32 v62, v62, v36, v37
	v_max3_f32 v62, v62, v38, v39
	v_max3_f32 v62, v62, v32, v33
	v_max3_f32 v62, v62, v34, v35
	v_max3_f32 v62, v62, v28, v29
	v_max3_f32 v62, v62, v30, v31
	v_max3_f32 v62, v62, v24, v25
	v_max3_f32 v62, v62, v26, v27
	v_max3_f32 v62, v62, v20, v21
	v_max3_f32 v62, v62, v22, v23
	v_max3_f32 v62, v62, v16, v17
	v_max3_f32 v62, v62, v18, v19
	v_max3_f32 v62, v62, v4, v5
	v_max3_f32 v62, v62, v6, v7
	v_max3_f32 v62, v62, v0, v1
	v_max3_f32 v62, v62, v2, v3
	v_mov_b32_e32 v63, v62
	s_nop 1
	v_permlane16_swap_b32_e32 v62, v63
	v_max_f32_e32 v63, v63, v63
	v_max_f32_e32 v62, v62, v62
	v_max_f32_e32 v62, v62, v63
	v_mov_b32_e32 v63, v62
	s_nop 1
	v_permlane32_swap_b32_e32 v62, v63
	v_max_f32_e32 v63, v63, v63
	v_max_f32_e32 v62, v62, v62
	v_max_f32_e32 v112, v62, v63
	v_pk_add_f32 v[40:41], v[40:41], v[112:113] op_sel_hi:[1,0] neg_lo:[0,1] neg_hi:[0,1]
	v_pk_add_f32 v[42:43], v[42:43], v[112:113] op_sel_hi:[1,0] neg_lo:[0,1] neg_hi:[0,1]
	v_exp_f32_e32 v40, v40
	v_exp_f32_e32 v41, v41
	v_exp_f32_e32 v42, v42
	v_exp_f32_e32 v43, v43
	v_pk_add_f32 v[36:37], v[36:37], v[112:113] op_sel_hi:[1,0] neg_lo:[0,1] neg_hi:[0,1]
	v_pk_add_f32 v[38:39], v[38:39], v[112:113] op_sel_hi:[1,0] neg_lo:[0,1] neg_hi:[0,1]
	v_exp_f32_e32 v36, v36
	v_exp_f32_e32 v37, v37
	v_exp_f32_e32 v38, v38
	v_exp_f32_e32 v39, v39
	v_pk_add_f32 v[32:33], v[32:33], v[112:113] op_sel_hi:[1,0] neg_lo:[0,1] neg_hi:[0,1]
	v_pk_add_f32 v[62:63], v[40:41], 0 op_sel_hi:[1,0]
	v_pk_add_f32 v[34:35], v[34:35], v[112:113] op_sel_hi:[1,0] neg_lo:[0,1] neg_hi:[0,1]
	v_exp_f32_e32 v32, v32
	v_exp_f32_e32 v33, v33
	v_pk_add_f32 v[62:63], v[42:43], v[62:63]
	v_exp_f32_e32 v34, v34
	v_exp_f32_e32 v35, v35
	v_pk_add_f32 v[28:29], v[28:29], v[112:113] op_sel_hi:[1,0] neg_lo:[0,1] neg_hi:[0,1]
	v_pk_add_f32 v[62:63], v[36:37], v[62:63]
	v_pk_add_f32 v[30:31], v[30:31], v[112:113] op_sel_hi:[1,0] neg_lo:[0,1] neg_hi:[0,1]
	v_exp_f32_e32 v114, v28
	v_exp_f32_e32 v115, v29
	v_pk_add_f32 v[62:63], v[38:39], v[62:63]
	v_exp_f32_e32 v116, v30
	v_exp_f32_e32 v117, v31
	v_pk_add_f32 v[24:25], v[24:25], v[112:113] op_sel_hi:[1,0] neg_lo:[0,1] neg_hi:[0,1]
	v_pk_add_f32 v[62:63], v[32:33], v[62:63]
	v_pk_add_f32 v[26:27], v[26:27], v[112:113] op_sel_hi:[1,0] neg_lo:[0,1] neg_hi:[0,1]
	v_exp_f32_e32 v118, v24
	v_exp_f32_e32 v119, v25
	v_pk_add_f32 v[62:63], v[34:35], v[62:63]
	v_exp_f32_e32 v120, v26
	v_exp_f32_e32 v121, v27
	v_pk_add_f32 v[24:25], v[114:115], v[62:63]
	v_cvt_pk_bf16_f32 v26, v36, v37
	v_pk_add_f32 v[24:25], v[116:117], v[24:25]
	v_cvt_pk_bf16_f32 v27, v38, v39
	v_pk_add_f32 v[24:25], v[118:119], v[24:25]
	v_pk_add_f32 v[20:21], v[20:21], v[112:113] op_sel_hi:[1,0] neg_lo:[0,1] neg_hi:[0,1]
	v_pk_add_f32 v[62:63], v[120:121], v[24:25]
	v_cvt_pk_bf16_f32 v24, v40, v41
	v_cvt_pk_bf16_f32 v25, v42, v43
	v_pk_add_f32 v[22:23], v[22:23], v[112:113] op_sel_hi:[1,0] neg_lo:[0,1] neg_hi:[0,1]
	v_exp_f32_e32 v36, v20
	s_waitcnt lgkmcnt(14)
	v_mfma_f32_16x16x32_bf16 v[28:31], v[44:47], v[24:27], 0
	v_exp_f32_e32 v37, v21
	v_exp_f32_e32 v38, v22
	v_exp_f32_e32 v39, v23
	v_mfma_f32_16x16x32_bf16 v[8:11], v[8:11], v[24:27], 0
	v_add_f32_e64 v42, v16, -v112
	v_add_f32_e64 v43, v17, -v112
	v_pk_add_f32 v[44:45], v[18:19], v[112:113] op_sel_hi:[1,0] neg_lo:[0,1] neg_hi:[0,1]
	v_pk_add_f32 v[40:41], v[36:37], v[62:63]
	v_mfma_f32_16x16x32_bf16 v[20:23], v[50:53], v[24:27], 0
	v_add_f32_e64 v40, v38, v40
	v_add_f32_e64 v41, v39, v41
	v_pk_add_f32 v[0:1], v[0:1], v[112:113] op_sel_hi:[1,0] neg_lo:[0,1] neg_hi:[0,1]
	v_mov_b32_e32 v64, v65
	v_mfma_f32_16x16x32_bf16 v[16:19], v[58:61], v[24:27], 0
	v_cvt_pk_bf16_f32 v24, v32, v33
	v_cvt_pk_bf16_f32 v25, v34, v35
	v_cvt_pk_bf16_f32 v26, v114, v115
	v_cvt_pk_bf16_f32 v27, v116, v117
	v_exp_f32_e32 v32, v42
	v_exp_f32_e32 v33, v43
	v_mfma_f32_16x16x32_bf16 v[28:31], v[54:57], v[24:27], v[28:31]
	v_exp_f32_e32 v34, v44
	v_exp_f32_e32 v35, v45
	v_pk_add_f32 v[42:43], v[4:5], v[112:113] op_sel_hi:[1,0] neg_lo:[0,1] neg_hi:[0,1]
	v_mfma_f32_16x16x32_bf16 v[8:11], v[66:69], v[24:27], v[8:11]
	v_add_f32_e64 v44, v6, -v112
	v_add_f32_e64 v45, v7, -v112
	v_pk_add_f32 v[40:41], v[32:33], v[40:41]
	s_waitcnt lgkmcnt(1)
	v_mov_b32_e32 v50, v48
	v_mfma_f32_16x16x32_bf16 v[4:7], v[78:81], v[24:27], v[16:19]
	v_add_f32_e64 v40, v34, v40
	v_add_f32_e64 v41, v35, v41
	v_mov_b32_e32 v51, v49
	s_and_b64 s[6:7], s[26:27], exec
	v_cvt_pk_bf16_f32 v16, v118, v119
	v_cvt_pk_bf16_f32 v17, v120, v121
	v_cvt_pk_bf16_f32 v18, v36, v37
	v_cvt_pk_bf16_f32 v19, v38, v39
	v_mfma_f32_16x16x32_bf16 v[20:23], v[70:73], v[24:27], v[20:23]
	v_add_f32_e64 v38, v2, -v112
	v_add_f32_e64 v39, v3, -v112
	s_mov_b32 s6, 0xe800000
	s_cselect_b32 s8, s6, 0x2e800000
	v_mfma_f32_16x16x32_bf16 v[24:27], v[74:77], v[16:19], v[28:31]
	s_and_b64 s[6:7], s[28:29], exec
	s_cselect_b32 s6, 0x12800000, s8
	s_add_u32 s6, s42, s6
	v_exp_f32_e32 v28, v42
	v_exp_f32_e32 v29, v43
	v_exp_f32_e32 v30, v44
	v_exp_f32_e32 v31, v45
	v_mfma_f32_16x16x32_bf16 v[8:11], v[82:85], v[16:19], v[8:11]
	v_add_f32_e64 v36, v28, v40
	v_add_f32_e64 v37, v29, v41
	v_exp_f32_e32 v40, v0
	v_exp_f32_e32 v41, v1
	v_mfma_f32_16x16x32_bf16 v[0:3], v[98:101], v[16:19], v[4:7]
	s_addc_u32 s7, s43, 0
	s_lshl_b32 s66, s22, 6
	v_cvt_pk_bf16_f32 v62, v40, v41
	v_cvt_pk_bf16_f32 v4, v32, v33
	v_cvt_pk_bf16_f32 v5, v34, v35
	v_cvt_pk_bf16_f32 v6, v28, v29
	v_cvt_pk_bf16_f32 v7, v30, v31
	v_mfma_f32_16x16x32_bf16 v[20:23], v[90:93], v[16:19], v[20:23]
	s_nop 0
	v_mfma_f32_16x16x32_bf16 v[16:19], v[94:97], v[4:7], v[24:27]
	s_nop 2
	v_exp_f32_e32 v24, v38
	v_exp_f32_e32 v25, v39
	v_mfma_f32_16x16x32_bf16 v[8:11], v[104:107], v[4:7], v[8:11]
	v_mov_b32_e32 v104, v102
	v_mov_b32_e32 v105, v103
	v_cvt_pk_bf16_f32 v63, v24, v25
	v_mfma_f32_16x16x32_bf16 v[20:23], v[108:111], v[4:7], v[20:23]
	v_add_f32_e64 v26, v30, v36
	v_add_f32_e64 v27, v31, v37
	v_pk_add_f32 v[26:27], v[40:41], v[26:27]
	v_mfma_f32_16x16x32_bf16 v[0:3], v[86:89], v[4:7], v[0:3]
	v_add_f32_e64 v26, v24, v26
	v_add_f32_e64 v27, v25, v27
	v_pk_add_f32 v[26:27], v[26:27], v[26:27] op_sel:[0,1] op_sel_hi:[1,0]
	v_mfma_f32_16x16x32_bf16 v[4:7], v[102:105], v[62:65], v[16:19]
	v_mov_b32_e32 v27, v26
	s_nop 1
	v_permlane16_swap_b32_e32 v26, v27
	v_mov_b32_e32 v16, v14
	v_mov_b32_e32 v17, v15
	v_add_f32_e32 v24, v26, v27
	s_nop 0
	v_mfma_f32_16x16x32_bf16 v[8:11], v[14:17], v[62:65], v[8:11]
	s_waitcnt lgkmcnt(0)
	v_mov_b32_e32 v14, v12
	v_mov_b32_e32 v15, v13
	v_mfma_f32_16x16x32_bf16 v[16:19], v[48:51], v[62:65], v[20:23]
	s_nop 2
	v_mov_b32_e32 v20, v24
	s_nop 1
	v_permlane32_swap_b32_e32 v24, v20
	v_mfma_f32_16x16x32_bf16 v[12:15], v[12:15], v[62:65], v[0:3]
	s_nop 2
	v_add_f32_e32 v0, v24, v20
	v_rcp_f32_e32 v1, v0
	s_nop 0
	v_mul_f32_e32 v1, 0x42800000, v1
	v_mul_f32_e32 v2, v1, v4
	v_mul_f32_e32 v3, v1, v5
	v_med3_f32 v5, v2, s55, v228
	v_med3_f32 v3, v3, s55, v228
	v_mov_b32_e32 v2, v65
	v_cvt_pk_fp8_f32 v2, v5, v3
	v_mul_f32_e32 v4, v1, v6
	v_mul_f32_e32 v3, v1, v7
	v_med3_f32 v4, v4, s55, v228
	v_med3_f32 v3, v3, s55, v228
	v_cvt_pk_fp8_f32 v2, v4, v3 op_sel:[0,0,1]
	v_mul_f32_e32 v3, v1, v8
	v_mul_f32_e32 v4, v1, v9
	v_med3_f32 v6, v3, s55, v228
	v_med3_f32 v4, v4, s55, v228
	v_mov_b32_e32 v3, v65
	v_cvt_pk_fp8_f32 v3, v6, v4
	v_mul_f32_e32 v5, v1, v10
	v_mul_f32_e32 v4, v1, v11
	v_med3_f32 v5, v5, s55, v228
	v_med3_f32 v4, v4, s55, v228
	v_cvt_pk_fp8_f32 v3, v5, v4 op_sel:[0,0,1]
	v_mul_f32_e32 v4, v1, v16
	v_mul_f32_e32 v5, v1, v17
	v_med3_f32 v7, v4, s55, v228
	v_med3_f32 v5, v5, s55, v228
	v_mov_b32_e32 v4, v65
	v_cvt_pk_fp8_f32 v4, v7, v5
	v_mul_f32_e32 v6, v1, v18
	v_mul_f32_e32 v5, v1, v19
	v_med3_f32 v6, v6, s55, v228
	v_med3_f32 v5, v5, s55, v228
	v_cvt_pk_fp8_f32 v4, v6, v5 op_sel:[0,0,1]
	v_mul_f32_e32 v5, v1, v12
	v_mul_f32_e32 v6, v1, v13
	v_med3_f32 v8, v5, s55, v228
	v_med3_f32 v6, v6, s55, v228
	v_mov_b32_e32 v5, v65
	v_cvt_pk_fp8_f32 v5, v8, v6
	v_mul_f32_e32 v7, v1, v14
	v_mul_f32_e32 v1, v1, v15
	v_med3_f32 v6, v7, s55, v228
	v_med3_f32 v1, v1, s55, v228
	v_cvt_pk_fp8_f32 v5, v6, v1 op_sel:[0,0,1]
	v_lshlrev_b64 v[6:7], 10, v[164:165]
	v_lshl_add_u64 v[6:7], s[6:7], 0, v[6:7]
	v_lshl_add_u64 v[6:7], v[6:7], 0, s[66:67]
	v_lshl_add_u64 v[6:7], v[6:7], 0, v[160:161]
	global_store_dwordx4 v[6:7], v[2:5], off sc1 nt
	s_and_saveexec_b64 s[6:7], vcc
	s_cbranch_execz .LBB0_422
	v_log_f32_e32 v0, v0
	s_ashr_i32 s25, s24, 31
	s_lshl_b64 s[8:9], s[24:25], 22
	v_readlane_b32 s10, v254, 30
	s_add_u32 s8, s10, s8
	v_readlane_b32 s10, v254, 31
	s_addc_u32 s9, s10, s9
	v_add_f32_e32 v0, v112, v0
	v_mul_f32_e32 v2, 0x3f317218, v0
	v_lshl_add_u64 v[0:1], s[8:9], 0, v[162:163]
	s_lshl_b32 s66, s22, 2
	v_lshl_add_u64 v[0:1], v[0:1], 0, s[66:67]
	global_store_dword v[0:1], v2, off

.LBB0_472:
	s_and_b32 s24, s30, 3
	s_lshl_b32 s25, s24, 8
	v_mov_b32_e32 v16, s25
	s_barrier
	global_load_dwordx4 v[20:23], v16, s[22:23]
	s_nop 0
	global_load_dwordx4 v[16:19], v16, s[22:23] offset:16
	s_waitcnt vmcnt(4)
	v_lshlrev_b32_e32 v50, 16, v4
	v_and_b32_e32 v51, 0xffff0000, v4
	v_lshlrev_b32_e32 v52, 16, v5
	v_readlane_b32 s26, v254, 34
	s_or_b32 s24, s24, s26
	v_and_b32_e32 v53, 0xffff0000, v5
	v_lshlrev_b32_e32 v34, 16, v0
	v_and_b32_e32 v35, 0xffff0000, v0
	v_lshlrev_b32_e32 v49, 16, v6
	v_and_b32_e32 v48, 0xffff0000, v6
	v_lshlrev_b32_e32 v47, 16, v7
	v_and_b32_e32 v46, 0xffff0000, v7
	s_lshr_b32 s25, s30, 2
	s_add_i32 s25, s25, s3
	s_lshl_b32 s24, s24, 7
	s_add_i32 s24, s25, s24
	s_ashr_i32 s25, s24, 31
	s_lshl_b64 s[24:25], s[24:25], 6
	s_waitcnt vmcnt(3)
	ds_write_b128 v42, v[8:11] offset:39168
	s_waitcnt vmcnt(2)
	ds_write_b128 v43, v[12:15] offset:39168
	s_waitcnt vmcnt(1)
	v_add_f32_e32 v20, v20, v50
	v_add_f32_e32 v21, v21, v51
	v_min_f32_e32 v50, 0, v20
	v_mul_f32_e64 v20, |v20|, s0
	v_min_f32_e32 v51, 0, v21
	v_mul_f32_e64 v21, |v21|, s0
	v_exp_f32_e32 v20, v20
	v_exp_f32_e32 v21, v21
	v_add_f32_e32 v22, v22, v52
	v_min_f32_e32 v52, 0, v22
	v_add_f32_e32 v20, 1.0, v20
	v_add_f32_e32 v21, 1.0, v21
	v_log_f32_e32 v20, v20
	v_log_f32_e32 v21, v21
	v_mul_f32_e64 v22, |v22|, s0
	v_exp_f32_e32 v22, v22
	v_fmac_f32_e32 v50, 0xbf317218, v20
	v_fmac_f32_e32 v51, 0xbf317218, v21
	v_mul_f32_e32 v20, 0x3d800000, v50
	v_mul_f32_e32 v21, 0x3d800000, v51
	v_add_f32_e32 v22, 1.0, v22
	v_mov_b32_dpp v20, v20 row_shr:1 row_mask:0xf bank_mask:0xf bound_ctrl:1
	v_mov_b32_dpp v21, v21 row_shr:1 row_mask:0xf bank_mask:0xf bound_ctrl:1
	v_log_f32_e32 v22, v22
	v_fmac_f32_e32 v20, 0x3d800000, v50
	v_fmac_f32_e32 v21, 0x3d800000, v51
	v_add_f32_e32 v23, v23, v53
	v_add_f32_dpp v20, v20, v20 row_shr:2 row_mask:0xf bank_mask:0xf bound_ctrl:1
	v_add_f32_dpp v21, v21, v21 row_shr:2 row_mask:0xf bank_mask:0xf bound_ctrl:1
	v_fmac_f32_e32 v52, 0xbf317218, v22
	v_add_f32_dpp v20, v20, v20 row_shr:4 row_mask:0xf bank_mask:0xf bound_ctrl:1
	v_add_f32_dpp v21, v21, v21 row_shr:4 row_mask:0xf bank_mask:0xf bound_ctrl:1
	v_mul_f32_e32 v22, 0x3d800000, v52
	v_add_f32_dpp v20, v20, v20 row_shr:8 row_mask:0xf bank_mask:0xf bound_ctrl:1
	v_add_f32_dpp v21, v21, v21 row_shr:8 row_mask:0xf bank_mask:0xf bound_ctrl:1
	v_readlane_b32 s26, v20, 15
	v_readlane_b32 s34, v21, 15
	v_readlane_b32 s27, v20, 31
	v_readlane_b32 s35, v21, 31
	v_mov_b32_e32 v50, s26
	v_mov_b32_e32 v54, s34
	v_mov_b32_dpp v22, v22 row_shr:1 row_mask:0xf bank_mask:0xf bound_ctrl:1
	v_readlane_b32 s31, v20, 47
	v_readlane_b32 s36, v21, 47
	v_mov_b32_e32 v51, s27
	v_mov_b32_e32 v55, s35
	v_cndmask_b32_e64 v50, v50, 0, vcc
	v_cndmask_b32_e64 v54, v54, 0, vcc
	v_fmac_f32_e32 v22, 0x3d800000, v52
	v_mov_b32_e32 v52, s31
	v_mov_b32_e32 v56, s36
	v_cndmask_b32_e64 v51, 0, v51, s[6:7]
	v_cndmask_b32_e64 v55, 0, v55, s[6:7]
	v_add_f32_e32 v20, v50, v20
	v_add_f32_e32 v21, v21, v54
	v_cndmask_b32_e64 v52, 0, v52, s[8:9]
	v_cndmask_b32_e64 v56, 0, v56, s[8:9]
	v_add_f32_e32 v20, v51, v20
	v_add_f32_e32 v21, v21, v55
	v_add_f32_e32 v20, v52, v20
	v_add_f32_e32 v21, v21, v56
	v_readlane_b32 s34, v20, 63
	v_readlane_b32 s31, v21, 63
	v_mul_f32_e64 v53, |v23|, s0
	v_sub_f32_e32 v20, s34, v20
	v_sub_f32_e32 v21, s31, v21
	v_mul_f32_e32 v20, 0x3fb8aa3b, v20
	v_mul_f32_e32 v21, 0x3fb8aa3b, v21
	v_exp_f32_e32 v53, v53
	v_exp_f32_e32 v20, v20
	v_exp_f32_e32 v21, v21
	v_min_f32_e32 v23, 0, v23
	v_add_f32_dpp v22, v22, v22 row_shr:2 row_mask:0xf bank_mask:0xf bound_ctrl:1
	s_waitcnt vmcnt(0)
	v_add_f32_e32 v16, v16, v49
	v_pk_mul_f32 v[20:21], v[20:21], v[34:35]
	v_add_f32_e32 v34, 1.0, v53
	v_log_f32_e32 v34, v34
	v_add_f32_dpp v22, v22, v22 row_shr:4 row_mask:0xf bank_mask:0xf bound_ctrl:1
	v_add_f32_e32 v17, v17, v48
	v_add_f32_e32 v18, v18, v47
	v_fmac_f32_e32 v23, 0xbf317218, v34
	v_mul_f32_e32 v34, 0x3d800000, v23
	v_add_f32_dpp v22, v22, v22 row_shr:8 row_mask:0xf bank_mask:0xf bound_ctrl:1
	v_add_f32_e32 v19, v19, v46
	v_mov_b32_dpp v34, v34 row_shr:1 row_mask:0xf bank_mask:0xf bound_ctrl:1
	v_fmac_f32_e32 v34, 0x3d800000, v23
	v_readlane_b32 s37, v22, 15
	v_readlane_b32 s38, v22, 31
	v_add_f32_dpp v23, v34, v34 row_shr:2 row_mask:0xf bank_mask:0xf bound_ctrl:1
	v_mov_b32_e32 v57, s37
	v_readlane_b32 s39, v22, 47
	v_add_f32_dpp v23, v23, v23 row_shr:4 row_mask:0xf bank_mask:0xf bound_ctrl:1
	v_mov_b32_e32 v58, s38
	v_cndmask_b32_e64 v57, v57, 0, vcc
	v_add_f32_dpp v23, v23, v23 row_shr:8 row_mask:0xf bank_mask:0xf bound_ctrl:1
	v_mov_b32_e32 v59, s39
	v_readlane_b32 s26, v23, 15
	v_readlane_b32 s27, v23, 31
	v_readlane_b32 s36, v23, 47
	v_mov_b32_e32 v34, s26
	v_cndmask_b32_e64 v34, v34, 0, vcc
	v_add_f32_e32 v23, v23, v34
	v_mov_b32_e32 v34, s27
	v_cndmask_b32_e64 v34, 0, v34, s[6:7]
	v_add_f32_e32 v23, v23, v34
	v_mov_b32_e32 v34, s36
	v_cndmask_b32_e64 v34, 0, v34, s[8:9]
	v_add_f32_e32 v23, v23, v34
	v_mul_f32_e64 v34, |v16|, s0
	v_cndmask_b32_e64 v58, 0, v58, s[6:7]
	v_add_f32_e32 v22, v22, v57
	v_exp_f32_e32 v35, v34
	v_cndmask_b32_e64 v59, 0, v59, s[8:9]
	v_add_f32_e32 v22, v22, v58
	v_add_f32_e32 v22, v22, v59
	v_readlane_b32 s36, v23, 63
	v_readlane_b32 s35, v22, 63
	v_add_f32_e32 v35, 1.0, v35
	v_sub_f32_e32 v23, s36, v23
	v_sub_f32_e32 v22, s35, v22
	v_mul_f32_e32 v22, 0x3fb8aa3b, v22
	v_mul_f32_e32 v23, 0x3fb8aa3b, v23
	v_log_f32_e32 v49, v35
	v_exp_f32_e32 v22, v22
	v_exp_f32_e32 v23, v23
	v_min_f32_e32 v16, 0, v16
	v_lshlrev_b32_e32 v34, 16, v1
	v_and_b32_e32 v35, 0xffff0000, v1
	v_fmac_f32_e32 v16, 0xbf317218, v49
	v_pk_mul_f32 v[22:23], v[22:23], v[34:35]
	v_mul_f32_e32 v34, 0x3d800000, v16
	v_mul_f32_e64 v35, |v17|, s0
	v_exp_f32_e32 v35, v35
	v_mov_b32_dpp v34, v34 row_shr:1 row_mask:0xf bank_mask:0xf bound_ctrl:1
	v_fmac_f32_e32 v34, 0x3d800000, v16
	v_min_f32_e32 v17, 0, v17
	v_mul_f32_e64 v46, |v19|, s0
	v_add_f32_dpp v16, v34, v34 row_shr:2 row_mask:0xf bank_mask:0xf bound_ctrl:1
	v_exp_f32_e32 v46, v46
	v_min_f32_e32 v19, 0, v19
	v_add_f32_dpp v16, v16, v16 row_shr:4 row_mask:0xf bank_mask:0xf bound_ctrl:1
	v_add_f32_e32 v46, 1.0, v46
	s_nop 0
	v_add_f32_dpp v16, v16, v16 row_shr:8 row_mask:0xf bank_mask:0xf bound_ctrl:1
	v_log_f32_e32 v46, v46
	v_readlane_b32 s26, v16, 15
	v_readlane_b32 s27, v16, 31
	v_readlane_b32 s37, v16, 47
	v_mov_b32_e32 v34, s26
	v_cndmask_b32_e64 v34, v34, 0, vcc
	v_add_f32_e32 v16, v16, v34
	v_mov_b32_e32 v34, s27
	v_cndmask_b32_e64 v34, 0, v34, s[6:7]
	v_add_f32_e32 v16, v16, v34
	v_mov_b32_e32 v34, s37
	v_cndmask_b32_e64 v34, 0, v34, s[8:9]
	v_add_f32_e32 v16, v16, v34
	v_add_f32_e32 v34, 1.0, v35
	v_log_f32_e32 v34, v34
	v_fmac_f32_e32 v19, 0xbf317218, v46
	v_mul_f32_e32 v46, 0x3d800000, v19
	v_readlane_b32 s37, v16, 63
	v_fmac_f32_e32 v17, 0xbf317218, v34
	v_mul_f32_e32 v34, 0x3d800000, v17
	v_mov_b32_dpp v46, v46 row_shr:1 row_mask:0xf bank_mask:0xf bound_ctrl:1
	v_fmac_f32_e32 v46, 0x3d800000, v19
	v_mov_b32_dpp v34, v34 row_shr:1 row_mask:0xf bank_mask:0xf bound_ctrl:1
	v_fmac_f32_e32 v34, 0x3d800000, v17
	v_add_f32_dpp v19, v46, v46 row_shr:2 row_mask:0xf bank_mask:0xf bound_ctrl:1
	v_sub_f32_e32 v16, s37, v16
	v_add_f32_dpp v17, v34, v34 row_shr:2 row_mask:0xf bank_mask:0xf bound_ctrl:1
	v_add_f32_dpp v19, v19, v19 row_shr:4 row_mask:0xf bank_mask:0xf bound_ctrl:1
	v_mul_f32_e32 v16, 0x3fb8aa3b, v16
	v_add_f32_dpp v17, v17, v17 row_shr:4 row_mask:0xf bank_mask:0xf bound_ctrl:1
	v_add_f32_dpp v19, v19, v19 row_shr:8 row_mask:0xf bank_mask:0xf bound_ctrl:1
	v_exp_f32_e32 v16, v16
	v_add_f32_dpp v17, v17, v17 row_shr:8 row_mask:0xf bank_mask:0xf bound_ctrl:1
	v_readlane_b32 s49, v19, 47
	v_readlane_b32 s26, v17, 15
	v_readlane_b32 s27, v17, 31
	v_readlane_b32 s38, v17, 47
	v_mov_b32_e32 v34, s26
	v_cndmask_b32_e64 v34, v34, 0, vcc
	v_add_f32_e32 v17, v17, v34
	v_mov_b32_e32 v34, s27
	v_cndmask_b32_e64 v34, 0, v34, s[6:7]
	v_add_f32_e32 v17, v17, v34
	v_mov_b32_e32 v34, s38
	v_cndmask_b32_e64 v34, 0, v34, s[8:9]
	v_add_f32_e32 v17, v17, v34
	v_mul_f32_e64 v34, |v18|, s0
	v_exp_f32_e32 v34, v34
	v_min_f32_e32 v18, 0, v18
	v_readlane_b32 s38, v17, 63
	v_and_b32_e32 v35, 0xffff0000, v2
	v_add_f32_e32 v34, 1.0, v34
	v_log_f32_e32 v47, v34
	v_sub_f32_e32 v17, s38, v17
	v_mul_f32_e32 v17, 0x3fb8aa3b, v17
	v_exp_f32_e32 v17, v17
	v_fmac_f32_e32 v18, 0xbf317218, v47
	v_mul_f32_e32 v47, 0x3d800000, v18
	v_lshlrev_b32_e32 v34, 16, v2
	v_pk_mul_f32 v[34:35], v[16:17], v[34:35]
	v_mov_b32_dpp v47, v47 row_shr:1 row_mask:0xf bank_mask:0xf bound_ctrl:1
	v_fmac_f32_e32 v47, 0x3d800000, v18
	v_lshlrev_b32_e32 v16, 16, v3
	v_and_b32_e32 v17, 0xffff0000, v3
	v_add_f32_dpp v18, v47, v47 row_shr:2 row_mask:0xf bank_mask:0xf bound_ctrl:1
	s_nop 1
	v_add_f32_dpp v18, v18, v18 row_shr:4 row_mask:0xf bank_mask:0xf bound_ctrl:1
	s_nop 1
	v_add_f32_dpp v18, v18, v18 row_shr:8 row_mask:0xf bank_mask:0xf bound_ctrl:1
	s_nop 0
	v_readlane_b32 s26, v18, 15
	v_readlane_b32 s27, v18, 31
	v_readlane_b32 s39, v18, 47
	v_mov_b32_e32 v47, s26
	v_readlane_b32 s26, v19, 15
	v_cndmask_b32_e64 v47, v47, 0, vcc
	v_add_f32_e32 v18, v18, v47
	v_mov_b32_e32 v46, s26
	v_mov_b32_e32 v47, s27
	v_readlane_b32 s27, v19, 31
	v_cndmask_b32_e64 v46, v46, 0, vcc
	v_add_f32_e32 v19, v19, v46
	v_mov_b32_e32 v46, s27
	v_cndmask_b32_e64 v47, 0, v47, s[6:7]
	v_cndmask_b32_e64 v46, 0, v46, s[6:7]
	v_add_f32_e32 v18, v18, v47
	v_mov_b32_e32 v47, s39
	v_add_f32_e32 v19, v19, v46
	v_mov_b32_e32 v46, s49
	v_cndmask_b32_e64 v47, 0, v47, s[8:9]
	v_cndmask_b32_e64 v46, 0, v46, s[8:9]
	v_add_f32_e32 v18, v18, v47
	v_add_f32_e32 v19, v19, v46
	v_readlane_b32 s39, v18, 63
	v_readlane_b32 s49, v19, 63
	s_nop 0
	v_sub_f32_e32 v18, s39, v18
	v_sub_f32_e32 v19, s49, v19
	v_mul_f32_e32 v18, 0x3fb8aa3b, v18
	v_mul_f32_e32 v19, 0x3fb8aa3b, v19
	v_exp_f32_e32 v18, v18
	v_exp_f32_e32 v19, v19
	s_nop 0
	v_pk_mul_f32 v[46:47], v[18:19], v[16:17]
	v_cvt_pk_bf16_f32 v16, v20, v21
	v_cvt_pk_bf16_f32 v17, v22, v23
	v_cvt_pk_bf16_f32 v18, v34, v35
	v_cvt_pk_bf16_f32 v19, v46, v47
	ds_write_b128 v44, v[16:19] offset:28928
	s_and_saveexec_b64 s[26:27], s[10:11]
	s_cbranch_execz .LBB0_474
	v_mov_b32_e32 v23, 0x3fb8aa3b
	v_mul_f32_e32 v16, s34, v23
	v_mul_f32_e32 v17, s31, v23
	v_mul_f32_e32 v18, s35, v23
	v_mul_f32_e32 v19, s36, v23
	v_exp_f32_e32 v16, v16
	v_exp_f32_e32 v17, v17
	v_exp_f32_e32 v18, v18
	v_exp_f32_e32 v19, v19
	v_mul_f32_e32 v20, s37, v23
	v_mul_f32_e32 v21, s38, v23
	v_mul_f32_e32 v22, s39, v23
	v_mul_f32_e32 v23, s49, v23
	v_exp_f32_e32 v20, v20
	v_exp_f32_e32 v21, v21
	v_exp_f32_e32 v22, v22
	v_exp_f32_e32 v23, v23
	s_lshl_b64 s[34:35], s[24:25], 2
	s_add_u32 s34, s28, s34
	s_addc_u32 s35, s29, s35
	global_store_dwordx4 v65, v[16:19], s[34:35] sc1 nt
	global_store_dwordx4 v65, v[20:23], s[34:35] offset:16 sc1 nt

.LBB0_571:
	s_or_b64 exec, exec, s[28:29]
	s_waitcnt lgkmcnt(0)
	s_barrier
	ds_read_b128 v[52:55], v100
	ds_read_b128 v[56:59], v100 offset:256
	s_lshl_b32 s28, s49, 7
	s_lshl_b32 s66, s28, 1
	s_add_i32 s59, s59, 1
	s_cmp_lg_u32 s59, 16
	s_waitcnt lgkmcnt(0)
	v_add_f32_e32 v52, v52, v56
	v_fmamk_f32 v52, v52, 0x3c000000, v229
	v_rsq_f32_e32 v52, v52
	s_nop 0
	v_mul_f32_e32 v56, v36, v52
	global_load_dword v36, v[84:85], off
	s_waitcnt vmcnt(0)
	v_mul_f32_e32 v56, v36, v56
	v_bfe_u32 v60, v56, 16, 1
	v_add3_u32 v56, v56, v60, s60
	v_add_u32_e32 v60, v108, v101
	ds_write_b16_d16_hi v60, v56 offset:57600
	v_mul_f32_e32 v56, v40, v52
	global_load_dword v40, v[86:87], off
	s_waitcnt vmcnt(0)
	v_mul_f32_e32 v56, v40, v56
	v_bfe_u32 v60, v56, 16, 1
	v_add3_u32 v56, v56, v60, s60
	v_add_u32_e32 v60, v108, v102
	ds_write_b16_d16_hi v60, v56 offset:57600
	v_mul_f32_e32 v56, v44, v52
	global_load_dword v44, v[88:89], off
	v_mul_f32_e32 v52, v48, v52
	global_load_dword v48, v[90:91], off
	s_waitcnt vmcnt(1)
	v_mul_f32_e32 v56, v44, v56
	v_bfe_u32 v60, v56, 16, 1
	v_add3_u32 v56, v56, v60, s60
	v_add_u32_e32 v60, v108, v103
	s_waitcnt vmcnt(0)
	v_mul_f32_e32 v52, v52, v48
	ds_write_b16_d16_hi v60, v56 offset:57600
	v_bfe_u32 v56, v52, 16, 1
	v_add3_u32 v52, v52, v56, s60
	v_add_u32_e32 v56, v108, v104
	ds_write_b16_d16_hi v56, v52 offset:57600
	v_add_f32_e32 v52, v53, v57
	v_fmamk_f32 v52, v52, 0x3c000000, v229
	v_rsq_f32_e32 v52, v52
	s_nop 0
	v_mul_f32_e32 v37, v37, v52
	v_mul_f32_e32 v37, v36, v37
	v_bfe_u32 v53, v37, 16, 1
	v_add3_u32 v37, v37, v53, s60
	v_add_u32_e32 v53, v109, v101
	ds_write_b16_d16_hi v53, v37 offset:57600
	v_mul_f32_e32 v37, v41, v52
	v_mul_f32_e32 v37, v40, v37
	v_bfe_u32 v41, v37, 16, 1
	v_add3_u32 v37, v37, v41, s60
	v_add_u32_e32 v41, v109, v102
	ds_write_b16_d16_hi v41, v37 offset:57600
	v_mul_f32_e32 v37, v45, v52
	v_mul_f32_e32 v37, v44, v37
	v_bfe_u32 v41, v37, 16, 1
	v_add3_u32 v37, v37, v41, s60
	v_add_u32_e32 v41, v109, v103
	ds_write_b16_d16_hi v41, v37 offset:57600
	v_mul_f32_e32 v37, v49, v52
	v_mul_f32_e32 v37, v48, v37
	v_bfe_u32 v41, v37, 16, 1
	v_add3_u32 v37, v37, v41, s60
	v_add_u32_e32 v41, v109, v104
	ds_write_b16_d16_hi v41, v37 offset:57600
	v_add_f32_e32 v37, v54, v58
	v_fmamk_f32 v37, v37, 0x3c000000, v229
	v_rsq_f32_e32 v37, v37
	v_and_b32_e32 v45, 0xffff0000, v32
	v_mul_f32_e32 v38, v38, v37
	v_mul_f32_e32 v38, v36, v38
	v_bfe_u32 v41, v38, 16, 1
	v_add3_u32 v38, v38, v41, s60
	v_add_u32_e32 v41, v110, v101
	ds_write_b16_d16_hi v41, v38 offset:57600
	v_mul_f32_e32 v38, v42, v37
	v_mul_f32_e32 v38, v40, v38
	v_bfe_u32 v41, v38, 16, 1
	v_add3_u32 v38, v38, v41, s60
	v_add_u32_e32 v41, v110, v102
	ds_write_b16_d16_hi v41, v38 offset:57600
	v_mul_f32_e32 v38, v46, v37
	v_mul_f32_e32 v38, v44, v38
	v_bfe_u32 v41, v38, 16, 1
	v_mul_f32_e32 v37, v50, v37
	v_add3_u32 v38, v38, v41, s60
	v_add_u32_e32 v41, v110, v103
	v_mul_f32_e32 v37, v48, v37
	ds_write_b16_d16_hi v41, v38 offset:57600
	v_bfe_u32 v38, v37, 16, 1
	v_add3_u32 v37, v37, v38, s60
	v_add_u32_e32 v38, v110, v104
	ds_write_b16_d16_hi v38, v37 offset:57600
	v_add_f32_e32 v37, v55, v59
	v_fmamk_f32 v37, v37, 0x3c000000, v229
	v_rsq_f32_e32 v37, v37
	s_nop 0
	v_mul_f32_e32 v38, v39, v37
	v_mul_f32_e32 v36, v36, v38
	v_bfe_u32 v38, v36, 16, 1
	v_add3_u32 v36, v36, v38, s60
	v_add_u32_e32 v38, v111, v101
	ds_write_b16_d16_hi v38, v36 offset:57600
	v_mul_f32_e32 v36, v43, v37
	v_mul_f32_e32 v36, v40, v36
	v_bfe_u32 v38, v36, 16, 1
	v_add3_u32 v36, v36, v38, s60
	v_add_u32_e32 v38, v111, v102
	ds_write_b16_d16_hi v38, v36 offset:57600
	v_mul_f32_e32 v36, v47, v37
	v_mul_f32_e32 v36, v44, v36
	v_lshlrev_b32_e32 v44, 16, v32
	v_mul_f32_e32 v32, 0xbfb8aa3b, v44
	v_exp_f32_e32 v32, v32
	v_bfe_u32 v38, v36, 16, 1
	v_add3_u32 v36, v36, v38, s60
	v_add_u32_e32 v38, v111, v103
	v_add_f32_e32 v32, 1.0, v32
	v_rcp_f32_e32 v46, v32
	v_mul_f32_e32 v32, 0xbfb8aa3b, v45
	ds_write_b16_d16_hi v38, v36 offset:57600
	v_mul_f32_e32 v36, v51, v37
	v_exp_f32_e32 v32, v32
	v_mul_f32_e32 v36, v48, v36
	v_bfe_u32 v37, v36, 16, 1
	v_add3_u32 v36, v36, v37, s60
	v_add_u32_e32 v37, v111, v104
	ds_write_b16_d16_hi v37, v36 offset:57600
	s_waitcnt lgkmcnt(0)
	s_barrier
	ds_read_b128 v[38:41], v116 offset:57600
	v_add_f32_e32 v32, 1.0, v32
	v_rcp_f32_e32 v47, v32
	v_lshlrev_b32_e32 v32, 16, v33
	v_and_b32_e32 v33, 0xffff0000, v33
	s_waitcnt lgkmcnt(0)
	v_lshlrev_b32_e32 v42, 16, v38
	v_and_b32_e32 v43, 0xffff0000, v38
	v_pk_mul_f32 v[44:45], v[46:47], v[44:45]
	v_lshlrev_b32_e32 v38, 16, v39
	v_pk_mul_f32 v[42:43], v[44:45], v[42:43]
	v_mul_f32_e32 v44, 0xbfb8aa3b, v32
	v_mul_f32_e32 v45, 0xbfb8aa3b, v33
	v_exp_f32_e32 v44, v44
	v_exp_f32_e32 v45, v45
	v_and_b32_e32 v39, 0xffff0000, v39
	v_lshl_add_u64 v[36:37], v[80:81], 0, s[66:67]
	v_add_f32_e32 v44, 1.0, v44
	v_add_f32_e32 v45, 1.0, v45
	v_rcp_f32_e32 v44, v44
	v_rcp_f32_e32 v45, v45
	s_nop 0
	v_pk_mul_f32 v[32:33], v[44:45], v[32:33]
	v_lshlrev_b32_e32 v44, 16, v34
	v_and_b32_e32 v45, 0xffff0000, v34
	v_mul_f32_e32 v34, 0xbfb8aa3b, v44
	v_exp_f32_e32 v34, v34
	v_pk_mul_f32 v[38:39], v[32:33], v[38:39]
	v_lshlrev_b32_e32 v32, 16, v40
	v_and_b32_e32 v33, 0xffff0000, v40
	v_add_f32_e32 v34, 1.0, v34
	v_rcp_f32_e32 v46, v34
	v_mul_f32_e32 v34, 0xbfb8aa3b, v45
	v_exp_f32_e32 v34, v34
	s_nop 0
	v_add_f32_e32 v34, 1.0, v34
	v_rcp_f32_e32 v47, v34
	v_lshlrev_b32_e32 v34, 16, v35
	v_and_b32_e32 v35, 0xffff0000, v35
	v_mul_f32_e32 v40, 0xbfb8aa3b, v34
	v_pk_mul_f32 v[44:45], v[46:47], v[44:45]
	v_exp_f32_e32 v40, v40
	v_pk_mul_f32 v[44:45], v[44:45], v[32:33]
	v_lshlrev_b32_e32 v32, 16, v41
	v_and_b32_e32 v33, 0xffff0000, v41
	v_mul_f32_e32 v41, 0xbfb8aa3b, v35
	v_exp_f32_e32 v41, v41
	v_add_f32_e32 v40, 1.0, v40
	v_rcp_f32_e32 v40, v40
	v_add_f32_e32 v41, 1.0, v41
	v_rcp_f32_e32 v41, v41
	s_nop 0
	v_pk_mul_f32 v[34:35], v[40:41], v[34:35]
	s_nop 0
	v_pk_mul_f32 v[40:41], v[34:35], v[32:33]
	v_cvt_pk_bf16_f32 v32, v42, v43
	v_cvt_pk_bf16_f32 v35, v40, v41
	v_lshlrev_b32_e32 v40, 16, v28
	v_and_b32_e32 v41, 0xffff0000, v28
	v_mul_f32_e32 v28, 0xbfb8aa3b, v40
	v_exp_f32_e32 v28, v28
	v_cvt_pk_bf16_f32 v33, v38, v39
	v_lshlrev_b64 v[38:39], 11, v[94:95]
	v_cvt_pk_bf16_f32 v34, v44, v45
	v_add_f32_e32 v28, 1.0, v28
	v_rcp_f32_e32 v42, v28
	v_mul_f32_e32 v28, 0xbfb8aa3b, v41
	v_exp_f32_e32 v28, v28
	v_lshl_add_u64 v[38:39], v[36:37], 0, v[38:39]
	global_store_dwordx4 v[38:39], v[32:35], off sc1 nt
	ds_read_b128 v[32:35], v117 offset:57600
	v_add_f32_e32 v28, 1.0, v28
	v_rcp_f32_e32 v43, v28
	v_lshlrev_b32_e32 v28, 16, v29
	v_and_b32_e32 v29, 0xffff0000, v29
	s_waitcnt lgkmcnt(0)
	v_lshlrev_b32_e32 v38, 16, v32
	v_and_b32_e32 v39, 0xffff0000, v32
	v_pk_mul_f32 v[40:41], v[42:43], v[40:41]
	v_lshlrev_b32_e32 v32, 16, v33
	v_pk_mul_f32 v[38:39], v[40:41], v[38:39]
	v_mul_f32_e32 v40, 0xbfb8aa3b, v28
	v_mul_f32_e32 v41, 0xbfb8aa3b, v29
	v_exp_f32_e32 v40, v40
	v_exp_f32_e32 v41, v41
	v_and_b32_e32 v33, 0xffff0000, v33
	v_add_f32_e32 v40, 1.0, v40
	v_add_f32_e32 v41, 1.0, v41
	v_rcp_f32_e32 v40, v40
	v_rcp_f32_e32 v41, v41
	s_nop 0
	v_pk_mul_f32 v[28:29], v[40:41], v[28:29]
	v_lshlrev_b32_e32 v40, 16, v30
	v_and_b32_e32 v41, 0xffff0000, v30
	v_mul_f32_e32 v30, 0xbfb8aa3b, v40
	v_exp_f32_e32 v30, v30
	v_pk_mul_f32 v[32:33], v[28:29], v[32:33]
	v_lshlrev_b32_e32 v28, 16, v34
	v_and_b32_e32 v29, 0xffff0000, v34
	v_add_f32_e32 v30, 1.0, v30
	v_rcp_f32_e32 v42, v30
	v_mul_f32_e32 v30, 0xbfb8aa3b, v41
	v_exp_f32_e32 v30, v30
	s_nop 0
	v_add_f32_e32 v30, 1.0, v30
	v_rcp_f32_e32 v43, v30
	v_lshlrev_b32_e32 v30, 16, v31
	v_and_b32_e32 v31, 0xffff0000, v31
	v_mul_f32_e32 v34, 0xbfb8aa3b, v30
	v_pk_mul_f32 v[40:41], v[42:43], v[40:41]
	v_exp_f32_e32 v34, v34
	v_pk_mul_f32 v[40:41], v[40:41], v[28:29]
	v_lshlrev_b32_e32 v28, 16, v35
	v_and_b32_e32 v29, 0xffff0000, v35
	v_mul_f32_e32 v35, 0xbfb8aa3b, v31
	v_exp_f32_e32 v35, v35
	v_add_f32_e32 v34, 1.0, v34
	v_rcp_f32_e32 v34, v34
	v_add_f32_e32 v35, 1.0, v35
	v_rcp_f32_e32 v35, v35
	s_nop 0
	v_pk_mul_f32 v[30:31], v[34:35], v[30:31]
	s_nop 0
	v_pk_mul_f32 v[34:35], v[30:31], v[28:29]
	v_cvt_pk_bf16_f32 v29, v32, v33
	v_lshlrev_b64 v[32:33], 11, v[92:93]
	v_cvt_pk_bf16_f32 v28, v38, v39
	v_cvt_pk_bf16_f32 v30, v40, v41
	v_cvt_pk_bf16_f32 v31, v34, v35
	v_lshl_add_u64 v[32:33], v[36:37], 0, v[32:33]
	global_store_dwordx4 v[32:33], v[28:31], off sc1 nt
	s_cbranch_scc0 .LBB0_596

.LBB0_675:
	v_mov_b32_e32 v64, v136
	v_mov_b32_e32 v130, v137
	s_mov_b32 s14, s2
	s_lshl_b32 s14, s14, 8
	s_lshl_b32 s15, s34, 8
	s_add_i32 s14, s14, s27
	s_or_b32 s15, s15, s28
	v_add_u32_e32 v140, s14, v64
	v_lshl_add_u32 v130, v130, 3, s15
	v_ashrrev_i32_e32 v141, 31, v140
	v_readlane_b32 s14, v254, 24
	v_lshlrev_b64 v[140:141], 11, v[140:141]
	v_readlane_b32 s15, v254, 25
	v_ashrrev_i32_e32 v131, 31, v130
	v_pk_mul_f32 v[128:129], v[128:129], s[58:59] op_sel_hi:[1,0]
	v_lshl_add_u64 v[140:141], s[14:15], 0, v[140:141]
	v_lshl_add_u64 v[130:131], v[130:131], 1, v[140:141]
	v_pk_mul_f32 v[126:127], v[126:127], s[58:59] op_sel_hi:[1,0]
	v_pk_mul_f32 v[140:141], v[124:125], s[58:59] op_sel_hi:[1,0]
	v_pk_mul_f32 v[124:125], v[122:123], s[58:59] op_sel_hi:[1,0]
	v_cvt_pk_bf16_f32 v122, v126, v127
	v_cvt_pk_bf16_f32 v123, v128, v129
	v_pk_mul_f32 v[120:121], v[120:121], s[58:59] op_sel_hi:[1,0]
	v_cvt_pk_bf16_f32 v124, v124, v125
	v_cvt_pk_bf16_f32 v125, v140, v141
	global_store_dwordx4 v[130:131], v[122:125], off sc1 nt
	v_pk_mul_f32 v[118:119], v[118:119], s[58:59] op_sel_hi:[1,0]
	s_mov_b64 s[14:15], 0x8000
	v_pk_mul_f32 v[122:123], v[112:113], s[58:59] op_sel_hi:[1,0]
	v_pk_mul_f32 v[112:113], v[110:111], s[58:59] op_sel_hi:[1,0]
	v_cvt_pk_bf16_f32 v110, v118, v119
	v_cvt_pk_bf16_f32 v111, v120, v121
	v_pk_mul_f32 v[114:115], v[114:115], s[58:59] op_sel_hi:[1,0]
	v_cvt_pk_bf16_f32 v112, v112, v113
	v_cvt_pk_bf16_f32 v113, v122, v123
	global_store_dwordx4 v[130:131], v[110:113], off offset:256 sc1 nt
	v_pk_mul_f32 v[104:105], v[104:105], s[58:59] op_sel_hi:[1,0]
	v_pk_mul_f32 v[102:103], v[102:103], s[58:59] op_sel_hi:[1,0]
	v_lshl_add_u64 v[110:111], v[130:131], 0, s[14:15]
	v_pk_mul_f32 v[112:113], v[116:117], s[58:59] op_sel_hi:[1,0]
	s_mov_b32 s14, 0x8000
	v_pk_mul_f32 v[116:117], v[108:109], s[58:59] op_sel_hi:[1,0]
	v_pk_mul_f32 v[108:109], v[106:107], s[58:59] op_sel_hi:[1,0]
	v_cvt_pk_bf16_f32 v106, v114, v115
	v_cvt_pk_bf16_f32 v107, v112, v113
	v_add_co_u32_e32 v112, vcc, s14, v130
	v_cvt_pk_bf16_f32 v108, v108, v109
	v_cvt_pk_bf16_f32 v109, v116, v117
	s_mov_b64 s[14:15], 0x10000
	s_nop 0
	v_addc_co_u32_e32 v113, vcc, 0, v131, vcc
	global_store_dwordx4 v[112:113], v[106:109], off sc1 nt
	v_pk_mul_f32 v[98:99], v[98:99], s[58:59] op_sel_hi:[1,0]
	v_pk_mul_f32 v[88:89], v[88:89], s[58:59] op_sel_hi:[1,0]
	v_pk_mul_f32 v[106:107], v[96:97], s[58:59] op_sel_hi:[1,0]
	v_pk_mul_f32 v[96:97], v[94:95], s[58:59] op_sel_hi:[1,0]
	v_cvt_pk_bf16_f32 v94, v102, v103
	v_cvt_pk_bf16_f32 v95, v104, v105
	v_pk_mul_f32 v[86:87], v[86:87], s[58:59] op_sel_hi:[1,0]
	v_cvt_pk_bf16_f32 v96, v96, v97
	v_cvt_pk_bf16_f32 v97, v106, v107
	global_store_dwordx4 v[110:111], v[94:97], off offset:256 sc1 nt
	v_pk_mul_f32 v[82:83], v[82:83], s[58:59] op_sel_hi:[1,0]
	v_pk_mul_f32 v[72:73], v[72:73], s[58:59] op_sel_hi:[1,0]
	v_lshl_add_u64 v[94:95], v[130:131], 0, s[14:15]
	v_pk_mul_f32 v[96:97], v[100:101], s[58:59] op_sel_hi:[1,0]
	s_mov_b32 s14, 0x10000
	v_pk_mul_f32 v[100:101], v[92:93], s[58:59] op_sel_hi:[1,0]
	v_pk_mul_f32 v[92:93], v[90:91], s[58:59] op_sel_hi:[1,0]
	v_cvt_pk_bf16_f32 v90, v98, v99
	v_cvt_pk_bf16_f32 v91, v96, v97
	v_add_co_u32_e32 v96, vcc, s14, v130
	v_cvt_pk_bf16_f32 v92, v92, v93
	v_cvt_pk_bf16_f32 v93, v100, v101
	s_mov_b64 s[14:15], 0x18000
	s_nop 0
	v_addc_co_u32_e32 v97, vcc, 0, v131, vcc
	global_store_dwordx4 v[96:97], v[90:93], off sc1 nt
	v_pk_mul_f32 v[70:71], v[70:71], s[58:59] op_sel_hi:[1,0]
	v_pk_mul_f32 v[60:61], v[60:61], s[58:59] op_sel_hi:[1,0]
	v_pk_mul_f32 v[90:91], v[80:81], s[58:59] op_sel_hi:[1,0]
	v_pk_mul_f32 v[80:81], v[78:79], s[58:59] op_sel_hi:[1,0]
	v_cvt_pk_bf16_f32 v78, v86, v87
	v_cvt_pk_bf16_f32 v79, v88, v89
	v_pk_mul_f32 v[62:63], v[62:63], s[58:59] op_sel_hi:[1,0]
	v_cvt_pk_bf16_f32 v80, v80, v81
	v_cvt_pk_bf16_f32 v81, v90, v91
	global_store_dwordx4 v[94:95], v[78:81], off offset:256 sc1 nt
	v_pk_mul_f32 v[54:55], v[54:55], s[58:59] op_sel_hi:[1,0]
	v_pk_mul_f32 v[52:53], v[52:53], s[58:59] op_sel_hi:[1,0]
	v_lshl_add_u64 v[78:79], v[130:131], 0, s[14:15]
	v_pk_mul_f32 v[80:81], v[84:85], s[58:59] op_sel_hi:[1,0]
	s_mov_b32 s14, 0x18000
	v_pk_mul_f32 v[84:85], v[76:77], s[58:59] op_sel_hi:[1,0]
	v_pk_mul_f32 v[76:77], v[74:75], s[58:59] op_sel_hi:[1,0]
	v_cvt_pk_bf16_f32 v74, v82, v83
	v_cvt_pk_bf16_f32 v75, v80, v81
	v_add_co_u32_e32 v80, vcc, s14, v130
	v_cvt_pk_bf16_f32 v76, v76, v77
	v_cvt_pk_bf16_f32 v77, v84, v85
	s_mov_b32 s14, 0x40000
	s_nop 0
	v_addc_co_u32_e32 v81, vcc, 0, v131, vcc
	global_store_dwordx4 v[80:81], v[74:77], off sc1 nt
	v_pk_mul_f32 v[48:49], v[48:49], s[58:59] op_sel_hi:[1,0]
	v_pk_mul_f32 v[38:39], v[38:39], s[58:59] op_sel_hi:[1,0]
	v_pk_mul_f32 v[74:75], v[68:69], s[58:59] op_sel_hi:[1,0]
	v_pk_mul_f32 v[68:69], v[66:67], s[58:59] op_sel_hi:[1,0]
	v_cvt_pk_bf16_f32 v66, v70, v71
	v_cvt_pk_bf16_f32 v67, v72, v73
	v_pk_mul_f32 v[36:37], v[36:37], s[58:59] op_sel_hi:[1,0]
	v_cvt_pk_bf16_f32 v68, v68, v69
	v_cvt_pk_bf16_f32 v69, v74, v75
	global_store_dwordx4 v[78:79], v[66:69], off offset:256 sc1 nt
	v_pk_mul_f32 v[32:33], v[32:33], s[58:59] op_sel_hi:[1,0]
	v_pk_mul_f32 v[22:23], v[22:23], s[58:59] op_sel_hi:[1,0]
	v_pk_mul_f32 v[68:69], v[58:59], s[58:59] op_sel_hi:[1,0]
	v_pk_mul_f32 v[58:59], v[56:57], s[58:59] op_sel_hi:[1,0]
	v_cvt_pk_bf16_f32 v56, v60, v61
	v_add_co_u32_e32 v60, vcc, s14, v130
	v_cvt_pk_bf16_f32 v57, v62, v63
	v_cvt_pk_bf16_f32 v58, v58, v59
	v_cvt_pk_bf16_f32 v59, v68, v69
	v_lshl_add_u64 v[66:67], v[130:131], 0, s[90:91]
	s_nop 0
	v_addc_co_u32_e32 v61, vcc, 0, v131, vcc
	global_store_dwordx4 v[60:61], v[56:59], off sc1 nt
	s_mov_b64 s[14:15], 0x48000
	v_pk_mul_f32 v[20:21], v[20:21], s[58:59] op_sel_hi:[1,0]
	v_pk_mul_f32 v[56:57], v[46:47], s[58:59] op_sel_hi:[1,0]
	v_pk_mul_f32 v[46:47], v[44:45], s[58:59] op_sel_hi:[1,0]
	v_cvt_pk_bf16_f32 v44, v52, v53
	v_cvt_pk_bf16_f32 v45, v54, v55
	v_pk_mul_f32 v[16:17], v[16:17], s[58:59] op_sel_hi:[1,0]
	v_cvt_pk_bf16_f32 v46, v46, v47
	v_cvt_pk_bf16_f32 v47, v56, v57
	global_store_dwordx4 v[66:67], v[44:47], off offset:256 sc1 nt
	s_cmp_eq_u32 s34, 3
	v_pk_mul_f32 v[6:7], v[6:7], s[58:59] op_sel_hi:[1,0]
	v_lshl_add_u64 v[44:45], v[130:131], 0, s[14:15]
	v_pk_mul_f32 v[46:47], v[50:51], s[58:59] op_sel_hi:[1,0]
	s_mov_b32 s14, 0x48000
	v_pk_mul_f32 v[50:51], v[42:43], s[58:59] op_sel_hi:[1,0]
	v_pk_mul_f32 v[42:43], v[40:41], s[58:59] op_sel_hi:[1,0]
	v_cvt_pk_bf16_f32 v40, v48, v49
	v_cvt_pk_bf16_f32 v41, v46, v47
	v_add_co_u32_e32 v46, vcc, s14, v130
	v_cvt_pk_bf16_f32 v42, v42, v43
	v_cvt_pk_bf16_f32 v43, v50, v51
	s_mov_b64 s[14:15], 0x50000
	s_nop 0
	v_addc_co_u32_e32 v47, vcc, 0, v131, vcc
	global_store_dwordx4 v[46:47], v[40:43], off sc1 nt
	v_pk_mul_f32 v[4:5], v[4:5], s[58:59] op_sel_hi:[1,0]
	s_nop 0
	v_pk_mul_f32 v[40:41], v[30:31], s[58:59] op_sel_hi:[1,0]
	v_pk_mul_f32 v[30:31], v[28:29], s[58:59] op_sel_hi:[1,0]
	v_cvt_pk_bf16_f32 v28, v36, v37
	v_cvt_pk_bf16_f32 v29, v38, v39
	s_nop 0
	v_cvt_pk_bf16_f32 v30, v30, v31
	v_cvt_pk_bf16_f32 v31, v40, v41
	global_store_dwordx4 v[44:45], v[28:31], off offset:256 sc1 nt
	s_nop 1
	v_lshl_add_u64 v[28:29], v[130:131], 0, s[14:15]
	v_pk_mul_f32 v[30:31], v[34:35], s[58:59] op_sel_hi:[1,0]
	s_mov_b32 s14, 0x50000
	v_pk_mul_f32 v[34:35], v[26:27], s[58:59] op_sel_hi:[1,0]
	v_pk_mul_f32 v[26:27], v[24:25], s[58:59] op_sel_hi:[1,0]
	v_cvt_pk_bf16_f32 v24, v32, v33
	v_cvt_pk_bf16_f32 v25, v30, v31
	v_add_co_u32_e32 v30, vcc, s14, v130
	v_cvt_pk_bf16_f32 v26, v26, v27
	v_cvt_pk_bf16_f32 v27, v34, v35
	s_mov_b64 s[14:15], 0x58000
	s_nop 0
	v_addc_co_u32_e32 v31, vcc, 0, v131, vcc
	global_store_dwordx4 v[30:31], v[24:27], off sc1 nt
	s_nop 1
	v_pk_mul_f32 v[24:25], v[14:15], s[58:59] op_sel_hi:[1,0]
	v_pk_mul_f32 v[14:15], v[12:13], s[58:59] op_sel_hi:[1,0]
	v_cvt_pk_bf16_f32 v12, v20, v21
	v_cvt_pk_bf16_f32 v13, v22, v23
	s_nop 0
	v_cvt_pk_bf16_f32 v14, v14, v15
	v_cvt_pk_bf16_f32 v15, v24, v25
	global_store_dwordx4 v[28:29], v[12:15], off offset:256 sc1 nt
	s_nop 1
	v_lshl_add_u64 v[12:13], v[130:131], 0, s[14:15]
	v_pk_mul_f32 v[14:15], v[18:19], s[58:59] op_sel_hi:[1,0]
	s_mov_b32 s14, 0x58000
	v_pk_mul_f32 v[18:19], v[10:11], s[58:59] op_sel_hi:[1,0]
	v_pk_mul_f32 v[10:11], v[8:9], s[58:59] op_sel_hi:[1,0]
	v_cvt_pk_bf16_f32 v8, v16, v17
	v_cvt_pk_bf16_f32 v9, v14, v15
	v_add_co_u32_e32 v14, vcc, s14, v130
	v_cvt_pk_bf16_f32 v10, v10, v11
	v_cvt_pk_bf16_f32 v11, v18, v19
	s_mov_b64 s[14:15], -1
	s_nop 0
	v_addc_co_u32_e32 v15, vcc, 0, v131, vcc
	global_store_dwordx4 v[14:15], v[8:11], off sc1 nt
	s_nop 1
	v_pk_mul_f32 v[8:9], v[2:3], s[58:59] op_sel_hi:[1,0]
	v_pk_mul_f32 v[2:3], v[0:1], s[58:59] op_sel_hi:[1,0]
	v_cvt_pk_bf16_f32 v0, v4, v5
	v_cvt_pk_bf16_f32 v1, v6, v7
	s_nop 0
	v_cvt_pk_bf16_f32 v2, v2, v3
	v_cvt_pk_bf16_f32 v3, v8, v9
	global_store_dwordx4 v[12:13], v[0:3], off offset:256 sc1 nt
	s_cbranch_scc1 .LBB0_670
	s_andn2_b64 vcc, exec, s[8:9]
	s_cbranch_vccnz .LBB0_669
	s_barrier
	s_branch .LBB0_669

.LBB0_689:
	v_mov_b32_e32 v64, v136
	v_mov_b32_e32 v130, v137
	s_mov_b32 s14, s2
	s_lshl_b32 s14, s14, 8
	s_lshl_b32 s15, s30, 8
	s_add_i32 s14, s14, s25
	s_or_b32 s15, s15, s26
	v_add_u32_e32 v140, s14, v64
	v_lshl_add_u32 v130, v130, 3, s15
	v_ashrrev_i32_e32 v141, 31, v140
	v_readlane_b32 s14, v254, 24
	v_lshlrev_b64 v[140:141], 11, v[140:141]
	v_readlane_b32 s15, v254, 25
	v_ashrrev_i32_e32 v131, 31, v130
	v_cvt_pk_bf16_f32 v126, v126, v127
	v_cvt_pk_bf16_f32 v127, v128, v129
	v_cvt_pk_bf16_f32 v128, v122, v123
	v_cvt_pk_bf16_f32 v129, v124, v125
	s_nop 0
	v_lshl_add_u64 v[140:141], s[14:15], 0, v[140:141]
	v_lshl_add_u64 v[130:131], v[130:131], 1, v[140:141]
	global_store_dwordx4 v[130:131], v[126:129], off sc1 nt
	v_cvt_pk_bf16_f32 v114, v114, v115
	v_cvt_pk_bf16_f32 v115, v116, v117
	s_mov_b64 s[14:15], 0x8000
	v_cvt_pk_bf16_f32 v116, v106, v107
	v_cvt_pk_bf16_f32 v117, v108, v109
	global_store_dwordx4 v[130:131], v[114:117], off offset:256 sc1 nt
	v_cvt_pk_bf16_f32 v106, v118, v119
	v_cvt_pk_bf16_f32 v107, v120, v121
	v_cvt_pk_bf16_f32 v108, v110, v111
	v_cvt_pk_bf16_f32 v109, v112, v113
	s_cmp_eq_u32 s30, 3
	s_nop 0
	v_lshl_add_u64 v[114:115], v[130:131], 0, s[14:15]
	s_mov_b32 s14, 0x8000
	v_add_co_u32_e32 v110, vcc, s14, v130
	s_mov_b64 s[14:15], 0x10000
	s_nop 0
	v_addc_co_u32_e32 v111, vcc, 0, v131, vcc
	global_store_dwordx4 v[110:111], v[106:109], off sc1 nt
	v_cvt_pk_bf16_f32 v98, v98, v99
	v_cvt_pk_bf16_f32 v99, v100, v101
	v_cvt_pk_bf16_f32 v100, v90, v91
	v_cvt_pk_bf16_f32 v101, v92, v93
	global_store_dwordx4 v[114:115], v[98:101], off offset:256 sc1 nt
	v_cvt_pk_bf16_f32 v90, v102, v103
	v_cvt_pk_bf16_f32 v91, v104, v105
	v_cvt_pk_bf16_f32 v92, v94, v95
	v_cvt_pk_bf16_f32 v93, v96, v97
	s_nop 1
	v_lshl_add_u64 v[98:99], v[130:131], 0, s[14:15]
	s_mov_b32 s14, 0x10000
	v_add_co_u32_e32 v94, vcc, s14, v130
	s_mov_b64 s[14:15], 0x18000
	s_nop 0
	v_addc_co_u32_e32 v95, vcc, 0, v131, vcc
	global_store_dwordx4 v[94:95], v[90:93], off sc1 nt
	v_cvt_pk_bf16_f32 v82, v82, v83
	v_cvt_pk_bf16_f32 v83, v84, v85
	v_cvt_pk_bf16_f32 v84, v74, v75
	v_cvt_pk_bf16_f32 v85, v76, v77
	global_store_dwordx4 v[98:99], v[82:85], off offset:256 sc1 nt
	v_cvt_pk_bf16_f32 v74, v86, v87
	v_cvt_pk_bf16_f32 v75, v88, v89
	v_cvt_pk_bf16_f32 v76, v78, v79
	v_cvt_pk_bf16_f32 v77, v80, v81
	s_nop 1
	v_lshl_add_u64 v[82:83], v[130:131], 0, s[14:15]
	s_mov_b32 s14, 0x18000
	v_add_co_u32_e32 v78, vcc, s14, v130
	s_mov_b32 s14, 0x40000
	s_nop 0
	v_addc_co_u32_e32 v79, vcc, 0, v131, vcc
	global_store_dwordx4 v[78:79], v[74:77], off sc1 nt
	v_cvt_pk_bf16_f32 v70, v70, v71
	v_cvt_pk_bf16_f32 v71, v72, v73
	v_cvt_pk_bf16_f32 v72, v66, v67
	v_cvt_pk_bf16_f32 v73, v68, v69
	global_store_dwordx4 v[82:83], v[70:73], off offset:256 sc1 nt
	v_cvt_pk_bf16_f32 v60, v60, v61
	v_cvt_pk_bf16_f32 v61, v62, v63
	v_cvt_pk_bf16_f32 v62, v56, v57
	v_add_co_u32_e32 v56, vcc, s14, v130
	v_lshl_add_u64 v[66:67], v[130:131], 0, s[90:91]
	s_nop 0
	v_addc_co_u32_e32 v57, vcc, 0, v131, vcc
	v_cvt_pk_bf16_f32 v63, v58, v59
	global_store_dwordx4 v[56:57], v[60:63], off sc1 nt
	v_cvt_pk_bf16_f32 v48, v48, v49
	v_cvt_pk_bf16_f32 v49, v50, v51
	s_mov_b64 s[14:15], 0x48000
	v_cvt_pk_bf16_f32 v50, v40, v41
	v_cvt_pk_bf16_f32 v51, v42, v43
	global_store_dwordx4 v[66:67], v[48:51], off offset:256 sc1 nt
	v_cvt_pk_bf16_f32 v40, v52, v53
	v_cvt_pk_bf16_f32 v41, v54, v55
	v_cvt_pk_bf16_f32 v42, v44, v45
	v_cvt_pk_bf16_f32 v43, v46, v47
	s_nop 1
	v_lshl_add_u64 v[48:49], v[130:131], 0, s[14:15]
	s_mov_b32 s14, 0x48000
	v_add_co_u32_e32 v44, vcc, s14, v130
	s_mov_b64 s[14:15], 0x50000
	s_nop 0
	v_addc_co_u32_e32 v45, vcc, 0, v131, vcc
	global_store_dwordx4 v[44:45], v[40:43], off sc1 nt
	v_cvt_pk_bf16_f32 v32, v32, v33
	v_cvt_pk_bf16_f32 v33, v34, v35
	v_cvt_pk_bf16_f32 v34, v24, v25
	v_cvt_pk_bf16_f32 v35, v26, v27
	global_store_dwordx4 v[48:49], v[32:35], off offset:256 sc1 nt
	v_cvt_pk_bf16_f32 v24, v36, v37
	v_cvt_pk_bf16_f32 v25, v38, v39
	v_cvt_pk_bf16_f32 v26, v28, v29
	v_cvt_pk_bf16_f32 v27, v30, v31
	s_nop 1
	v_lshl_add_u64 v[32:33], v[130:131], 0, s[14:15]
	s_mov_b32 s14, 0x50000
	v_add_co_u32_e32 v28, vcc, s14, v130
	s_mov_b64 s[14:15], 0x58000
	s_nop 0
	v_addc_co_u32_e32 v29, vcc, 0, v131, vcc
	global_store_dwordx4 v[28:29], v[24:27], off sc1 nt
	v_cvt_pk_bf16_f32 v16, v16, v17
	v_cvt_pk_bf16_f32 v17, v18, v19
	v_cvt_pk_bf16_f32 v18, v8, v9
	v_cvt_pk_bf16_f32 v19, v10, v11
	global_store_dwordx4 v[32:33], v[16:19], off offset:256 sc1 nt
	v_cvt_pk_bf16_f32 v8, v20, v21
	v_cvt_pk_bf16_f32 v9, v22, v23
	v_cvt_pk_bf16_f32 v10, v12, v13
	v_cvt_pk_bf16_f32 v11, v14, v15
	s_nop 1
	v_lshl_add_u64 v[16:17], v[130:131], 0, s[14:15]
	s_mov_b32 s14, 0x58000
	v_add_co_u32_e32 v12, vcc, s14, v130
	s_mov_b64 s[14:15], -1
	s_nop 0
	v_addc_co_u32_e32 v13, vcc, 0, v131, vcc
	global_store_dwordx4 v[12:13], v[8:11], off sc1 nt
	v_cvt_pk_bf16_f32 v4, v4, v5
	v_cvt_pk_bf16_f32 v5, v6, v7
	v_cvt_pk_bf16_f32 v6, v0, v1
	v_cvt_pk_bf16_f32 v7, v2, v3
	global_store_dwordx4 v[16:17], v[4:7], off offset:256 sc1 nt
	s_cbranch_scc1 .LBB0_684
	s_andn2_b64 vcc, exec, s[8:9]
	s_cbranch_vccnz .LBB0_683
	s_barrier
	s_branch .LBB0_683
